# v035 + xor-butterfly row reductions in the mLSTM/gMLP mixer units use DPP adds instead of ds_swizzle round trips (same operands, same order)
# speedup vs baseline: 1.0076x; 1.0076x over previous
; __device__ __forceinline__ float bflo(unsigned w) { return __uint_as_float(w << 16); }
; __device__ __forceinline__ float bfhi(unsigned w) { return __uint_as_float(w & 0xffff0000u); }
; __device__ __forceinline__ float geluf_(float x) { const float t = 1.5957691216f * (x + 0.044715f * x * x * x); return x * __builtin_amdgcn_rcpf(1.f + __expf(-t)); }
; __device__ __forceinline__ void gmlp_unit(LAS unsigned char* L, int u, const bf16* z, const bf16* wsb, const float* bs, const float* lng, const float* lnb, bf16* mix, int tid_) {
;     ...
;     { const int j = tid >> 2, part = tid & 3; const bf16* src = z + (size_t)(t0 + j) * 2048 + 256 + part * 64; float x[64]; float s1 = 0.f;
; #pragma unroll
;       for (int q = 0; q < 8; ++q) { const v4u w4 = *(const v4u*)(src + 8 * q); const unsigned ww[4] = {w4.x, w4.y, w4.z, w4.w};
; #pragma unroll
;           for (int i = 0; i < 4; ++i) { x[q * 8 + 2 * i] = geluf_(bflo(ww[i])); x[q * 8 + 2 * i + 1] = geluf_(bfhi(ww[i])); s1 += x[q * 8 + 2 * i] + x[q * 8 + 2 * i + 1]; } }
.LBB0_469:
	s_and_b64 vcc, exec, s[8:9]
	s_cbranch_vccz .LBB0_455
	v_mov_b32_e32 v1, v0
	s_mov_b64 s[38:39], 0
	s_waitcnt vmcnt(0)
	v_ashrrev_i32_e32 v50, 2, v1
	v_lshl_add_u32 v2, s18, 7, v50
	v_ashrrev_i32_e32 v3, 31, v2
	v_lshlrev_b32_e32 v4, 6, v1
	v_lshlrev_b64 v[2:3], 12, v[2:3]
	v_and_b32_e32 v51, 0xc0, v4
	v_lshl_add_u64 v[2:3], s[6:7], 0, v[2:3]
	v_lshlrev_b32_e32 v162, 1, v51
	v_lshl_add_u64 v[18:19], v[2:3], 0, v[162:163]
	global_load_dwordx4 v[2:5], v[18:19], off offset:560
	global_load_dwordx4 v[6:9], v[18:19], off offset:544
	global_load_dwordx4 v[10:13], v[18:19], off offset:528
	global_load_dwordx4 v[14:17], v[18:19], off offset:512
	v_and_b32_e32 v52, 15, v1
	s_waitcnt vmcnt(3)
	v_and_b32_e32 v81, 0xffff0000, v2
	s_waitcnt vmcnt(2)
	v_and_b32_e32 v65, 0xffff0000, v6
	s_waitcnt vmcnt(1)
	v_and_b32_e32 v46, 0xffff0000, v10
	s_waitcnt vmcnt(0)
	v_and_b32_e32 v22, 0xffff0000, v14
	v_lshlrev_b32_e32 v20, 16, v14
	v_mul_f32_e32 v14, 0x3d372713, v22
	v_and_b32_e32 v26, 0xffff0000, v15
	v_mul_f32_e32 v21, 0x3d372713, v20
	v_mul_f32_e32 v14, v14, v22
	v_lshlrev_b32_e32 v24, 16, v15
	v_mul_f32_e32 v15, 0x3d372713, v26
	v_mul_f32_e32 v21, v21, v20
	v_fma_f32 v14, v14, v22, v22
	v_mul_f32_e32 v25, 0x3d372713, v24
	v_mul_f32_e32 v15, v15, v26
	v_fma_f32 v21, v21, v20, v20
	v_mul_f32_e32 v14, 0xbfcc422a, v14
	v_mul_f32_e32 v25, v25, v24
	v_fma_f32 v15, v15, v26, v26
	v_mul_f32_e32 v21, 0xbfcc422a, v21
	v_mul_f32_e32 v14, 0x3fb8aa3b, v14
	v_fma_f32 v25, v25, v24, v24
	v_mul_f32_e32 v15, 0xbfcc422a, v15
	v_mul_f32_e32 v21, 0x3fb8aa3b, v21
	v_exp_f32_e32 v14, v14
	v_mul_f32_e32 v25, 0xbfcc422a, v25
	v_mul_f32_e32 v15, 0x3fb8aa3b, v15
	v_exp_f32_e32 v21, v21
	v_mul_f32_e32 v25, 0x3fb8aa3b, v25
	v_exp_f32_e32 v15, v15
	v_exp_f32_e32 v25, v25
	v_add_f32_e32 v14, 1.0, v14
	v_add_f32_e32 v21, 1.0, v21
	v_rcp_f32_e32 v23, v14
	v_add_f32_e32 v15, 1.0, v15
	v_rcp_f32_e32 v21, v21
	v_add_f32_e32 v25, 1.0, v25
	v_rcp_f32_e32 v27, v15
	v_rcp_f32_e32 v25, v25
	v_mul_f32_e32 v14, v23, v22
	v_fmac_f32_e32 v14, v21, v20
	v_mul_f32_e32 v15, v27, v26
	v_add_f32_e32 v14, 0, v14
	v_fmac_f32_e32 v15, v25, v24
	v_lshlrev_b32_e32 v28, 16, v16
	v_add_f32_e32 v14, v15, v14
	v_mul_f32_e32 v15, 0x3d372713, v28
	v_mul_f32_e32 v15, v15, v28
	v_fma_f32 v15, v15, v28, v28
	v_mul_f32_e32 v15, 0xbfcc422a, v15
	v_mul_f32_e32 v15, 0x3fb8aa3b, v15
	v_exp_f32_e32 v15, v15
	v_and_b32_e32 v30, 0xffff0000, v16
	v_lshlrev_b32_e32 v32, 16, v17
	v_and_b32_e32 v42, 0xffff0000, v17
	v_add_f32_e32 v15, 1.0, v15
	v_rcp_f32_e32 v29, v15
	v_mul_f32_e32 v15, 0x3d372713, v30
	v_mul_f32_e32 v15, v15, v30
	v_fma_f32 v15, v15, v30, v30
	v_mul_f32_e32 v15, 0xbfcc422a, v15
	v_mul_f32_e32 v15, 0x3fb8aa3b, v15
	v_exp_f32_e32 v15, v15
	v_lshlrev_b32_e32 v44, 16, v10
	v_mul_f32_e32 v10, 0x3d372713, v46
	v_mul_f32_e32 v10, v10, v46
	v_add_f32_e32 v15, 1.0, v15
	v_rcp_f32_e32 v31, v15
	v_fma_f32 v10, v10, v46, v46
	v_mul_f32_e32 v10, 0xbfcc422a, v10
	v_mul_f32_e32 v10, 0x3fb8aa3b, v10
	v_mul_f32_e32 v15, v31, v30
	v_fmac_f32_e32 v15, v29, v28
	v_add_f32_e32 v14, v15, v14
	v_mul_f32_e32 v15, 0x3d372713, v32
	v_mul_f32_e32 v15, v15, v32
	v_fma_f32 v15, v15, v32, v32
	v_mul_f32_e32 v15, 0xbfcc422a, v15
	v_mul_f32_e32 v15, 0x3fb8aa3b, v15
	v_exp_f32_e32 v15, v15
	v_exp_f32_e32 v10, v10
	v_and_b32_e32 v53, 0xffff0000, v11
	v_lshlrev_b32_e32 v48, 16, v11
	v_add_f32_e32 v15, 1.0, v15
	v_rcp_f32_e32 v33, v15
	v_mul_f32_e32 v15, 0x3d372713, v42
	v_mul_f32_e32 v15, v15, v42
	v_fma_f32 v15, v15, v42, v42
	v_mul_f32_e32 v15, 0xbfcc422a, v15
	v_mul_f32_e32 v15, 0x3fb8aa3b, v15
	v_exp_f32_e32 v15, v15
	v_add_f32_e32 v10, 1.0, v10
	v_rcp_f32_e32 v47, v10
	v_mul_f32_e32 v11, 0x3d372713, v53
	v_add_f32_e32 v15, 1.0, v15
	v_rcp_f32_e32 v43, v15
	v_mul_f32_e32 v10, v47, v46
	v_mul_f32_e32 v11, v11, v53
	v_fma_f32 v11, v11, v53, v53
	v_mul_f32_e32 v15, v43, v42
	v_fmac_f32_e32 v15, v33, v32
	v_add_f32_e32 v14, v15, v14
	v_mul_f32_e32 v15, 0x3d372713, v44
	v_mul_f32_e32 v15, v15, v44
	v_fma_f32 v15, v15, v44, v44
	v_mul_f32_e32 v15, 0xbfcc422a, v15
	v_mul_f32_e32 v15, 0x3fb8aa3b, v15
	v_exp_f32_e32 v15, v15
	v_mul_f32_e32 v11, 0xbfcc422a, v11
	v_mul_f32_e32 v11, 0x3fb8aa3b, v11
	v_exp_f32_e32 v11, v11
	v_add_f32_e32 v15, 1.0, v15
	v_rcp_f32_e32 v45, v15
	v_lshlrev_b32_e32 v55, 16, v12
	v_add_f32_e32 v11, 1.0, v11
	v_rcp_f32_e32 v54, v11
	v_fmac_f32_e32 v10, v45, v44
	v_add_f32_e32 v10, v10, v14
	v_mul_f32_e32 v14, 0x3d372713, v48
	v_mul_f32_e32 v14, v14, v48
	v_fma_f32 v14, v14, v48, v48
	v_mul_f32_e32 v14, 0xbfcc422a, v14
	v_mul_f32_e32 v14, 0x3fb8aa3b, v14
	v_exp_f32_e32 v14, v14
	v_mul_f32_e32 v11, v54, v53
	v_and_b32_e32 v57, 0xffff0000, v12
	v_lshlrev_b32_e32 v59, 16, v13
	v_add_f32_e32 v14, 1.0, v14
	v_rcp_f32_e32 v49, v14
	v_and_b32_e32 v61, 0xffff0000, v13
	v_lshlrev_b32_e32 v63, 16, v6
	v_mul_f32_e32 v6, 0x3d372713, v65
	v_fmac_f32_e32 v11, v49, v48
	v_add_f32_e32 v10, v11, v10
	v_mul_f32_e32 v11, 0x3d372713, v55
	v_mul_f32_e32 v11, v11, v55
	v_fma_f32 v11, v11, v55, v55
	v_mul_f32_e32 v11, 0xbfcc422a, v11
	v_mul_f32_e32 v11, 0x3fb8aa3b, v11
	v_exp_f32_e32 v11, v11
	v_mul_f32_e32 v6, v6, v65
	v_fma_f32 v6, v6, v65, v65
	v_mul_f32_e32 v6, 0xbfcc422a, v6
	v_add_f32_e32 v11, 1.0, v11
	v_rcp_f32_e32 v56, v11
	v_mul_f32_e32 v11, 0x3d372713, v57
	v_mul_f32_e32 v11, v11, v57
	v_fma_f32 v11, v11, v57, v57
	v_mul_f32_e32 v11, 0xbfcc422a, v11
	v_mul_f32_e32 v11, 0x3fb8aa3b, v11
	v_exp_f32_e32 v11, v11
	v_mul_f32_e32 v6, 0x3fb8aa3b, v6
	v_exp_f32_e32 v6, v6
	v_and_b32_e32 v69, 0xffff0000, v7
	v_add_f32_e32 v11, 1.0, v11
	v_rcp_f32_e32 v58, v11
	v_add_f32_e32 v6, 1.0, v6
	v_rcp_f32_e32 v66, v6
	v_lshlrev_b32_e32 v67, 16, v7
; __device__ __forceinline__ float bflo(unsigned w) { return __uint_as_float(w << 16); }
; __device__ __forceinline__ float bfhi(unsigned w) { return __uint_as_float(w & 0xffff0000u); }
; __device__ __forceinline__ float geluf_(float x) { const float t = 1.5957691216f * (x + 0.044715f * x * x * x); return x * __builtin_amdgcn_rcpf(1.f + __expf(-t)); }
; __device__ __forceinline__ void gmlp_unit(LAS unsigned char* L, int u, const bf16* z, const bf16* wsb, const float* bs, const float* lng, const float* lnb, bf16* mix, int tid_) {
;     ...
;     { const int j = tid >> 2, part = tid & 3; const bf16* src = z + (size_t)(t0 + j) * 2048 + 256 + part * 64; float x[64]; float s1 = 0.f;
; #pragma unroll
;       for (int q = 0; q < 8; ++q) { const v4u w4 = *(const v4u*)(src + 8 * q); const unsigned ww[4] = {w4.x, w4.y, w4.z, w4.w};
; #pragma unroll
;           for (int i = 0; i < 4; ++i) { x[q * 8 + 2 * i] = geluf_(bflo(ww[i])); x[q * 8 + 2 * i + 1] = geluf_(bfhi(ww[i])); s1 += x[q * 8 + 2 * i] + x[q * 8 + 2 * i + 1]; } }
	v_mul_f32_e32 v11, v58, v57
	v_fmac_f32_e32 v11, v56, v55
	v_add_f32_e32 v10, v11, v10
	v_mul_f32_e32 v11, 0x3d372713, v59
	v_mul_f32_e32 v11, v11, v59
	v_fma_f32 v11, v11, v59, v59
	v_mul_f32_e32 v11, 0xbfcc422a, v11
	v_mul_f32_e32 v11, 0x3fb8aa3b, v11
	v_exp_f32_e32 v11, v11
	v_mul_f32_e32 v6, v66, v65
	v_mul_f32_e32 v7, 0x3d372713, v69
	v_mul_f32_e32 v7, v7, v69
	v_add_f32_e32 v11, 1.0, v11
	v_rcp_f32_e32 v60, v11
	v_mul_f32_e32 v11, 0x3d372713, v61
	v_mul_f32_e32 v11, v11, v61
	v_fma_f32 v11, v11, v61, v61
	v_mul_f32_e32 v11, 0xbfcc422a, v11
	v_mul_f32_e32 v11, 0x3fb8aa3b, v11
	v_exp_f32_e32 v11, v11
	v_fma_f32 v7, v7, v69, v69
	v_mul_f32_e32 v7, 0xbfcc422a, v7
	v_mul_f32_e32 v7, 0x3fb8aa3b, v7
	v_add_f32_e32 v11, 1.0, v11
	v_rcp_f32_e32 v62, v11
	v_exp_f32_e32 v7, v7
	v_lshlrev_b32_e32 v71, 16, v8
	v_and_b32_e32 v73, 0xffff0000, v8
	v_mul_f32_e32 v11, v62, v61
	v_fmac_f32_e32 v11, v60, v59
	v_add_f32_e32 v10, v11, v10
	v_mul_f32_e32 v11, 0x3d372713, v63
	v_mul_f32_e32 v11, v11, v63
	v_fma_f32 v11, v11, v63, v63
	v_mul_f32_e32 v11, 0xbfcc422a, v11
	v_mul_f32_e32 v11, 0x3fb8aa3b, v11
	v_exp_f32_e32 v11, v11
	v_add_f32_e32 v7, 1.0, v7
	v_rcp_f32_e32 v70, v7
	v_lshlrev_b32_e32 v75, 16, v9
	v_add_f32_e32 v11, 1.0, v11
	v_rcp_f32_e32 v64, v11
	v_mul_f32_e32 v7, v70, v69
	v_and_b32_e32 v77, 0xffff0000, v9
	v_lshlrev_b32_e32 v79, 16, v2
	v_fmac_f32_e32 v6, v64, v63
	v_add_f32_e32 v6, v6, v10
	v_mul_f32_e32 v10, 0x3d372713, v67
	v_mul_f32_e32 v10, v10, v67
	v_fma_f32 v10, v10, v67, v67
	v_mul_f32_e32 v10, 0xbfcc422a, v10
	v_mul_f32_e32 v10, 0x3fb8aa3b, v10
	v_exp_f32_e32 v10, v10
	v_mul_f32_e32 v2, 0x3d372713, v81
	v_mul_f32_e32 v2, v2, v81
	v_fma_f32 v2, v2, v81, v81
	v_add_f32_e32 v10, 1.0, v10
	v_rcp_f32_e32 v68, v10
	v_mul_f32_e32 v2, 0xbfcc422a, v2
	v_mul_f32_e32 v2, 0x3fb8aa3b, v2
	v_exp_f32_e32 v2, v2
	v_fmac_f32_e32 v7, v68, v67
	v_add_f32_e32 v6, v7, v6
	v_mul_f32_e32 v7, 0x3d372713, v71
	v_mul_f32_e32 v7, v7, v71
	v_fma_f32 v7, v7, v71, v71
	v_mul_f32_e32 v7, 0xbfcc422a, v7
	v_mul_f32_e32 v7, 0x3fb8aa3b, v7
	v_exp_f32_e32 v7, v7
	v_add_f32_e32 v2, 1.0, v2
	v_rcp_f32_e32 v82, v2
	v_and_b32_e32 v84, 0xffff0000, v3
	v_add_f32_e32 v7, 1.0, v7
	v_rcp_f32_e32 v72, v7
	v_mul_f32_e32 v7, 0x3d372713, v73
	v_mul_f32_e32 v7, v7, v73
	v_fma_f32 v7, v7, v73, v73
	v_mul_f32_e32 v7, 0xbfcc422a, v7
	v_mul_f32_e32 v7, 0x3fb8aa3b, v7
	v_exp_f32_e32 v7, v7
	v_mul_f32_e32 v2, v82, v81
	v_lshlrev_b32_e32 v83, 16, v3
	v_mul_f32_e32 v3, 0x3d372713, v84
	v_add_f32_e32 v7, 1.0, v7
	v_rcp_f32_e32 v74, v7
	v_mul_f32_e32 v3, v3, v84
	v_fma_f32 v3, v3, v84, v84
	v_mul_f32_e32 v3, 0xbfcc422a, v3
	v_mul_f32_e32 v7, v74, v73
	v_fmac_f32_e32 v7, v72, v71
	v_add_f32_e32 v6, v7, v6
	v_mul_f32_e32 v7, 0x3d372713, v75
	v_mul_f32_e32 v7, v7, v75
	v_fma_f32 v7, v7, v75, v75
	v_mul_f32_e32 v7, 0xbfcc422a, v7
	v_mul_f32_e32 v7, 0x3fb8aa3b, v7
	v_exp_f32_e32 v7, v7
	v_mul_f32_e32 v3, 0x3fb8aa3b, v3
	v_exp_f32_e32 v3, v3
	v_lshlrev_b32_e32 v87, 16, v4
	v_add_f32_e32 v7, 1.0, v7
	v_rcp_f32_e32 v76, v7
	v_mul_f32_e32 v7, 0x3d372713, v77
	v_mul_f32_e32 v7, v7, v77
	v_fma_f32 v7, v7, v77, v77
	v_mul_f32_e32 v7, 0xbfcc422a, v7
	v_mul_f32_e32 v7, 0x3fb8aa3b, v7
	v_exp_f32_e32 v7, v7
	v_add_f32_e32 v3, 1.0, v3
	v_rcp_f32_e32 v86, v3
	v_and_b32_e32 v88, 0xffff0000, v4
	v_add_f32_e32 v7, 1.0, v7
	v_rcp_f32_e32 v78, v7
	v_mul_f32_e32 v3, v86, v84
	v_lshlrev_b32_e32 v91, 16, v5
	v_and_b32_e32 v92, 0xffff0000, v5
	v_mul_f32_e32 v7, v78, v77
	v_fmac_f32_e32 v7, v76, v75
	v_add_f32_e32 v6, v7, v6
	v_mul_f32_e32 v7, 0x3d372713, v79
	v_mul_f32_e32 v7, v7, v79
	v_fma_f32 v7, v7, v79, v79
	v_mul_f32_e32 v7, 0xbfcc422a, v7
	v_mul_f32_e32 v7, 0x3fb8aa3b, v7
	v_exp_f32_e32 v7, v7
	s_nop 0
	v_add_f32_e32 v7, 1.0, v7
	v_rcp_f32_e32 v80, v7
	s_nop 0
	v_fmac_f32_e32 v2, v80, v79
	v_add_f32_e32 v2, v2, v6
	v_mul_f32_e32 v6, 0x3d372713, v83
	v_mul_f32_e32 v6, v6, v83
	v_fma_f32 v6, v6, v83, v83
	v_mul_f32_e32 v6, 0xbfcc422a, v6
	v_mul_f32_e32 v6, 0x3fb8aa3b, v6
	v_exp_f32_e32 v6, v6
	s_nop 0
	v_add_f32_e32 v6, 1.0, v6
	v_rcp_f32_e32 v85, v6
	s_nop 0
	v_fmac_f32_e32 v3, v85, v83
	v_add_f32_e32 v2, v3, v2
	v_mul_f32_e32 v3, 0x3d372713, v87
	v_mul_f32_e32 v3, v3, v87
	v_fma_f32 v3, v3, v87, v87
	v_mul_f32_e32 v3, 0xbfcc422a, v3
	v_mul_f32_e32 v3, 0x3fb8aa3b, v3
	v_exp_f32_e32 v3, v3
	s_nop 0
	v_add_f32_e32 v3, 1.0, v3
	v_rcp_f32_e32 v89, v3
	v_mul_f32_e32 v3, 0x3d372713, v88
	v_mul_f32_e32 v3, v3, v88
	v_fma_f32 v3, v3, v88, v88
	v_mul_f32_e32 v3, 0xbfcc422a, v3
	v_mul_f32_e32 v3, 0x3fb8aa3b, v3
	v_exp_f32_e32 v3, v3
	s_nop 0
	v_add_f32_e32 v3, 1.0, v3
	v_rcp_f32_e32 v90, v3
	s_nop 0
	v_mul_f32_e32 v3, v90, v88
	v_fmac_f32_e32 v3, v89, v87
	v_add_f32_e32 v2, v3, v2
	v_mul_f32_e32 v3, 0x3d372713, v91
	v_mul_f32_e32 v3, v3, v91
	v_fma_f32 v3, v3, v91, v91
	v_mul_f32_e32 v3, 0xbfcc422a, v3
	v_mul_f32_e32 v3, 0x3fb8aa3b, v3
	v_exp_f32_e32 v3, v3
	s_nop 0
	v_add_f32_e32 v3, 1.0, v3
	v_rcp_f32_e32 v93, v3
	v_mul_f32_e32 v3, 0x3d372713, v92
	v_mul_f32_e32 v3, v3, v92
	v_fma_f32 v3, v3, v92, v92
	v_mul_f32_e32 v3, 0xbfcc422a, v3
	v_mul_f32_e32 v3, 0x3fb8aa3b, v3
	v_exp_f32_e32 v3, v3
	s_nop 0
	v_add_f32_e32 v3, 1.0, v3
	v_rcp_f32_e32 v94, v3
	s_nop 0
	v_mul_f32_e32 v3, v94, v92
	v_fmac_f32_e32 v3, v93, v91
	v_add_f32_e32 v34, v3, v2
	global_load_dwordx4 v[2:5], v[18:19], off offset:624
	global_load_dwordx4 v[6:9], v[18:19], off offset:608
	global_load_dwordx4 v[10:13], v[18:19], off offset:592
	global_load_dwordx4 v[14:17], v[18:19], off offset:576
	s_waitcnt vmcnt(3)
	v_lshlrev_b32_e32 v149, 16, v2
	v_and_b32_e32 v148, 0xffff0000, v2
	s_waitcnt vmcnt(1)
	v_and_b32_e32 v117, 0xffff0000, v10
	s_waitcnt vmcnt(0)
; __device__ __forceinline__ float bflo(unsigned w) { return __uint_as_float(w << 16); }
; __device__ __forceinline__ float bfhi(unsigned w) { return __uint_as_float(w & 0xffff0000u); }
; __device__ __forceinline__ float geluf_(float x) { const float t = 1.5957691216f * (x + 0.044715f * x * x * x); return x * __builtin_amdgcn_rcpf(1.f + __expf(-t)); }
; __device__ __forceinline__ void gmlp_unit(LAS unsigned char* L, int u, const bf16* z, const bf16* wsb, const float* bs, const float* lng, const float* lnb, bf16* mix, int tid_) {
;     ...
;     { const int j = tid >> 2, part = tid & 3; const bf16* src = z + (size_t)(t0 + j) * 2048 + 256 + part * 64; float x[64]; float s1 = 0.f;
; #pragma unroll
;       for (int q = 0; q < 8; ++q) { const v4u w4 = *(const v4u*)(src + 8 * q); const unsigned ww[4] = {w4.x, w4.y, w4.z, w4.w};
; #pragma unroll
;           for (int i = 0; i < 4; ++i) { x[q * 8 + 2 * i] = geluf_(bflo(ww[i])); x[q * 8 + 2 * i + 1] = geluf_(bfhi(ww[i])); s1 += x[q * 8 + 2 * i] + x[q * 8 + 2 * i + 1]; } }
	v_and_b32_e32 v103, 0xffff0000, v14
	v_lshlrev_b32_e32 v18, 16, v14
	v_mul_f32_e32 v14, 0x3d372713, v103
	v_mul_f32_e32 v19, 0x3d372713, v18
	v_mul_f32_e32 v14, v14, v103
	v_mul_f32_e32 v19, v19, v18
	v_fma_f32 v14, v14, v103, v103
	v_fma_f32 v19, v19, v18, v18
	v_mul_f32_e32 v14, 0xbfcc422a, v14
	v_mul_f32_e32 v19, 0xbfcc422a, v19
	v_mul_f32_e32 v14, 0x3fb8aa3b, v14
	v_mul_f32_e32 v19, 0x3fb8aa3b, v19
	v_exp_f32_e32 v14, v14
	v_exp_f32_e32 v19, v19
	v_and_b32_e32 v107, 0xffff0000, v15
	v_lshlrev_b32_e32 v105, 16, v15
	v_add_f32_e32 v14, 1.0, v14
	v_add_f32_e32 v19, 1.0, v19
	v_rcp_f32_e32 v104, v14
	v_rcp_f32_e32 v19, v19
	v_mul_f32_e32 v15, 0x3d372713, v107
	v_mul_f32_e32 v15, v15, v107
	v_mul_f32_e32 v14, v104, v103
	v_fmac_f32_e32 v14, v19, v18
	v_add_f32_e32 v14, v14, v34
	v_mul_f32_e32 v34, 0x3d372713, v105
	v_mul_f32_e32 v34, v34, v105
	v_fma_f32 v15, v15, v107, v107
	v_fma_f32 v34, v34, v105, v105
	v_mul_f32_e32 v15, 0xbfcc422a, v15
	v_mul_f32_e32 v34, 0xbfcc422a, v34
	v_mul_f32_e32 v15, 0x3fb8aa3b, v15
	v_mul_f32_e32 v34, 0x3fb8aa3b, v34
	v_exp_f32_e32 v15, v15
	v_exp_f32_e32 v34, v34
	v_lshlrev_b32_e32 v109, 16, v16
	v_and_b32_e32 v16, 0xffff0000, v16
	v_add_f32_e32 v15, 1.0, v15
	v_add_f32_e32 v34, 1.0, v34
	v_rcp_f32_e32 v108, v15
	v_rcp_f32_e32 v106, v34
	v_lshlrev_b32_e32 v112, 16, v17
	v_and_b32_e32 v17, 0xffff0000, v17
	v_mul_f32_e32 v15, v108, v107
	v_fmac_f32_e32 v15, v106, v105
	v_add_f32_e32 v14, v15, v14
	v_mul_f32_e32 v15, 0x3d372713, v109
	v_mul_f32_e32 v15, v15, v109
	v_fma_f32 v15, v15, v109, v109
	v_mul_f32_e32 v15, 0xbfcc422a, v15
	v_mul_f32_e32 v15, 0x3fb8aa3b, v15
	v_exp_f32_e32 v15, v15
	v_lshlrev_b32_e32 v115, 16, v10
	v_mul_f32_e32 v10, 0x3d372713, v117
	v_mul_f32_e32 v10, v10, v117
	v_add_f32_e32 v15, 1.0, v15
	v_rcp_f32_e32 v110, v15
	v_mul_f32_e32 v15, 0x3d372713, v16
	v_mul_f32_e32 v15, v15, v16
	v_fma_f32 v15, v15, v16, v16
	v_mul_f32_e32 v15, 0xbfcc422a, v15
	v_mul_f32_e32 v15, 0x3fb8aa3b, v15
	v_exp_f32_e32 v15, v15
	v_fma_f32 v10, v10, v117, v117
	v_mul_f32_e32 v10, 0xbfcc422a, v10
	v_mul_f32_e32 v10, 0x3fb8aa3b, v10
	v_add_f32_e32 v15, 1.0, v15
	v_rcp_f32_e32 v111, v15
	v_exp_f32_e32 v10, v10
	v_and_b32_e32 v121, 0xffff0000, v11
	v_lshlrev_b32_e32 v119, 16, v11
	v_mul_f32_e32 v15, v111, v16
	v_fmac_f32_e32 v15, v110, v109
	v_add_f32_e32 v14, v15, v14
	v_mul_f32_e32 v15, 0x3d372713, v112
	v_mul_f32_e32 v15, v15, v112
	v_fma_f32 v15, v15, v112, v112
	v_mul_f32_e32 v15, 0xbfcc422a, v15
	v_mul_f32_e32 v15, 0x3fb8aa3b, v15
	v_exp_f32_e32 v15, v15
	v_add_f32_e32 v10, 1.0, v10
	v_rcp_f32_e32 v118, v10
	v_mul_f32_e32 v11, 0x3d372713, v121
	v_add_f32_e32 v15, 1.0, v15
	v_rcp_f32_e32 v113, v15
	v_mul_f32_e32 v15, 0x3d372713, v17
	v_mul_f32_e32 v15, v15, v17
	v_fma_f32 v15, v15, v17, v17
	v_mul_f32_e32 v15, 0xbfcc422a, v15
	v_mul_f32_e32 v15, 0x3fb8aa3b, v15
	v_exp_f32_e32 v15, v15
	v_mul_f32_e32 v10, v118, v117
	v_mul_f32_e32 v11, v11, v121
	v_fma_f32 v11, v11, v121, v121
	v_add_f32_e32 v15, 1.0, v15
	v_rcp_f32_e32 v114, v15
	v_mul_f32_e32 v11, 0xbfcc422a, v11
	v_mul_f32_e32 v11, 0x3fb8aa3b, v11
	v_exp_f32_e32 v11, v11
	v_mul_f32_e32 v15, v114, v17
	v_fmac_f32_e32 v15, v113, v112
	v_add_f32_e32 v14, v15, v14
	v_mul_f32_e32 v15, 0x3d372713, v115
	v_mul_f32_e32 v15, v15, v115
	v_fma_f32 v15, v15, v115, v115
	v_mul_f32_e32 v15, 0xbfcc422a, v15
	v_mul_f32_e32 v15, 0x3fb8aa3b, v15
	v_exp_f32_e32 v15, v15
	v_add_f32_e32 v11, 1.0, v11
	v_rcp_f32_e32 v123, v11
	v_lshlrev_b32_e32 v133, 16, v12
	v_add_f32_e32 v15, 1.0, v15
	v_rcp_f32_e32 v116, v15
	v_mul_f32_e32 v11, v123, v121
	v_and_b32_e32 v141, 0xffff0000, v12
	v_lshlrev_b32_e32 v143, 16, v13
	v_fmac_f32_e32 v10, v116, v115
	v_add_f32_e32 v10, v10, v14
	v_mul_f32_e32 v14, 0x3d372713, v119
	v_mul_f32_e32 v14, v14, v119
	v_fma_f32 v14, v14, v119, v119
	v_mul_f32_e32 v14, 0xbfcc422a, v14
	v_mul_f32_e32 v14, 0x3fb8aa3b, v14
	v_exp_f32_e32 v14, v14
	v_and_b32_e32 v145, 0xffff0000, v13
	v_mul_f32_e32 v2, 0x3d372713, v149
	v_mul_f32_e32 v2, v2, v149
	v_add_f32_e32 v14, 1.0, v14
	v_rcp_f32_e32 v120, v14
	v_mov_b32_e32 v100, v148
	v_fmac_f32_e32 v11, v120, v119
	v_add_f32_e32 v10, v11, v10
	v_mul_f32_e32 v11, 0x3d372713, v133
	v_mul_f32_e32 v11, v11, v133
	v_fma_f32 v11, v11, v133, v133
	v_mul_f32_e32 v11, 0xbfcc422a, v11
	v_mul_f32_e32 v11, 0x3fb8aa3b, v11
	v_exp_f32_e32 v11, v11
	s_nop 0
	v_add_f32_e32 v11, 1.0, v11
	v_rcp_f32_e32 v139, v11
	v_mul_f32_e32 v11, 0x3d372713, v141
	v_mul_f32_e32 v11, v11, v141
	v_fma_f32 v11, v11, v141, v141
	v_mul_f32_e32 v11, 0xbfcc422a, v11
	v_mul_f32_e32 v11, 0x3fb8aa3b, v11
	v_exp_f32_e32 v11, v11
	s_nop 0
	v_add_f32_e32 v11, 1.0, v11
	v_rcp_f32_e32 v142, v11
	s_nop 0
	v_mul_f32_e32 v11, v142, v141
	v_fmac_f32_e32 v11, v139, v133
	v_add_f32_e32 v10, v11, v10
	v_mul_f32_e32 v11, 0x3d372713, v143
	v_mul_f32_e32 v11, v11, v143
	v_fma_f32 v11, v11, v143, v143
	v_mul_f32_e32 v11, 0xbfcc422a, v11
	v_mul_f32_e32 v11, 0x3fb8aa3b, v11
	v_exp_f32_e32 v11, v11
	s_nop 0
	v_add_f32_e32 v11, 1.0, v11
	v_rcp_f32_e32 v144, v11
	v_mul_f32_e32 v11, 0x3d372713, v145
	v_mul_f32_e32 v11, v11, v145
	v_fma_f32 v11, v11, v145, v145
	v_mul_f32_e32 v11, 0xbfcc422a, v11
	v_mul_f32_e32 v11, 0x3fb8aa3b, v11
	v_exp_f32_e32 v11, v11
	s_nop 0
	v_add_f32_e32 v11, 1.0, v11
	v_rcp_f32_e32 v146, v11
	s_nop 0
	v_mul_f32_e32 v11, v146, v145
	v_fmac_f32_e32 v11, v144, v143
	v_add_f32_e32 v38, v11, v10
	v_lshlrev_b32_e32 v10, 16, v6
	v_mul_f32_e32 v12, 0x3d372713, v10
	v_mul_f32_e32 v12, v12, v10
	v_mov_b32_e32 v13, v10
	v_fmac_f32_e32 v13, v12, v13
	v_and_b32_e32 v6, 0xffff0000, v6
	v_mul_f32_e32 v12, 0xbfcc422a, v13
	v_mul_f32_e32 v13, 0x3d372713, v6
	v_mul_f32_e32 v13, v13, v6
; __device__ __forceinline__ float bflo(unsigned w) { return __uint_as_float(w << 16); }
; __device__ __forceinline__ float bfhi(unsigned w) { return __uint_as_float(w & 0xffff0000u); }
; __device__ __forceinline__ float geluf_(float x) { const float t = 1.5957691216f * (x + 0.044715f * x * x * x); return x * __builtin_amdgcn_rcpf(1.f + __expf(-t)); }
; #define SHX(v, m) (((m) < 32) ? __int_as_float(__builtin_amdgcn_ds_swizzle(__float_as_int(v), ((((m) & 31) << 10) | 0x1f))) : shx32(v))
; __device__ __forceinline__ void gmlp_unit(LAS unsigned char* L, int u, const bf16* z, const bf16* wsb, const float* bs, const float* lng, const float* lnb, bf16* mix, int tid_) {
;     ...
;     { const int j = tid >> 2, part = tid & 3; const bf16* src = z + (size_t)(t0 + j) * 2048 + 256 + part * 64; float x[64]; float s1 = 0.f;
; #pragma unroll
;       for (int q = 0; q < 8; ++q) { const v4u w4 = *(const v4u*)(src + 8 * q); const unsigned ww[4] = {w4.x, w4.y, w4.z, w4.w};
; #pragma unroll
;           for (int i = 0; i < 4; ++i) { x[q * 8 + 2 * i] = geluf_(bflo(ww[i])); x[q * 8 + 2 * i + 1] = geluf_(bfhi(ww[i])); s1 += x[q * 8 + 2 * i] + x[q * 8 + 2 * i + 1]; } }
;       s1 += SHX(s1, 1); s1 += SHX(s1, 2); const float mean = s1 * (1.f / 256.f); float s2 = 0.f;
	v_mov_b32_e32 v14, v6
	v_fmac_f32_e32 v14, v13, v14
	v_mul_f32_e32 v13, 0xbfcc422a, v14
	v_mul_f32_e32 v13, 0x3fb8aa3b, v13
	v_exp_f32_e32 v13, v13
	v_lshlrev_b32_e32 v11, 16, v7
	v_mov_b32_e32 v15, v11
	v_and_b32_e32 v7, 0xffff0000, v7
	v_add_f32_e32 v13, 1.0, v13
	v_rcp_f32_e32 v14, v13
	v_mul_f32_e32 v13, 0x3d372713, v11
	v_mul_f32_e32 v13, v13, v11
	v_fmac_f32_e32 v15, v13, v15
	v_mul_f32_e32 v13, 0xbfcc422a, v15
	v_mul_f32_e32 v15, 0x3d372713, v7
	v_mul_f32_e32 v15, v15, v7
	v_mov_b32_e32 v36, v7
	v_fmac_f32_e32 v36, v15, v36
	v_mul_f32_e32 v15, 0xbfcc422a, v36
	v_mul_f32_e32 v15, 0x3fb8aa3b, v15
	v_mul_f32_e32 v12, 0x3fb8aa3b, v12
	v_mul_f32_e32 v13, 0x3fb8aa3b, v13
	v_exp_f32_e32 v15, v15
	v_exp_f32_e32 v12, v12
	v_exp_f32_e32 v13, v13
	v_add_f32_e32 v15, 1.0, v15
	v_add_f32_e32 v12, 1.0, v12
	v_add_f32_e32 v13, 1.0, v13
	v_rcp_f32_e32 v15, v15
	v_rcp_f32_e32 v12, v12
	v_rcp_f32_e32 v13, v13
	v_pk_mul_f32 v[36:37], v[14:15], v[6:7]
	s_nop 0
	v_pk_fma_f32 v[6:7], v[12:13], v[10:11], v[36:37]
	s_nop 0
	v_add_f32_e32 v6, v6, v38
	v_add_f32_e32 v14, v7, v6
	v_lshlrev_b32_e32 v6, 16, v8
	v_pk_mul_f32 v[34:35], v[12:13], v[10:11]
	v_mul_f32_e32 v10, 0x3d372713, v6
	v_mul_f32_e32 v10, v10, v6
	v_mov_b32_e32 v11, v6
	v_fmac_f32_e32 v11, v10, v11
	v_and_b32_e32 v8, 0xffff0000, v8
	v_mul_f32_e32 v10, 0xbfcc422a, v11
	v_mul_f32_e32 v11, 0x3d372713, v8
	v_mul_f32_e32 v11, v11, v8
	v_mov_b32_e32 v12, v8
	v_fmac_f32_e32 v12, v11, v12
	v_mul_f32_e32 v11, 0xbfcc422a, v12
	v_mul_f32_e32 v11, 0x3fb8aa3b, v11
	v_exp_f32_e32 v11, v11
	v_lshlrev_b32_e32 v7, 16, v9
	v_mov_b32_e32 v13, v7
	v_and_b32_e32 v9, 0xffff0000, v9
	v_add_f32_e32 v11, 1.0, v11
	v_rcp_f32_e32 v12, v11
	v_mul_f32_e32 v11, 0x3d372713, v7
	v_mul_f32_e32 v11, v11, v7
	v_fmac_f32_e32 v13, v11, v13
	v_mul_f32_e32 v11, 0xbfcc422a, v13
	v_mul_f32_e32 v13, 0x3d372713, v9
	v_mul_f32_e32 v13, v13, v9
	v_mov_b32_e32 v15, v9
	v_fmac_f32_e32 v15, v13, v15
	v_mul_f32_e32 v13, 0xbfcc422a, v15
	v_mul_f32_e32 v13, 0x3fb8aa3b, v13
	v_mul_f32_e32 v10, 0x3fb8aa3b, v10
	v_mul_f32_e32 v11, 0x3fb8aa3b, v11
	v_exp_f32_e32 v13, v13
	v_exp_f32_e32 v10, v10
	v_exp_f32_e32 v11, v11
	v_add_f32_e32 v13, 1.0, v13
	v_add_f32_e32 v10, 1.0, v10
	v_add_f32_e32 v11, 1.0, v11
	v_rcp_f32_e32 v13, v13
	v_rcp_f32_e32 v10, v10
	v_rcp_f32_e32 v11, v11
	v_pk_mul_f32 v[40:41], v[12:13], v[8:9]
	v_pk_mul_f32 v[38:39], v[10:11], v[6:7]
	v_pk_fma_f32 v[6:7], v[10:11], v[6:7], v[40:41]
	v_lshlrev_b32_e32 v11, 16, v4
	v_add_f32_e32 v6, v6, v14
	v_add_f32_e32 v95, v7, v6
	v_lshlrev_b32_e32 v7, 16, v5
	v_and_b32_e32 v6, 0xffff0000, v5
	v_mul_f32_e32 v5, 0x3d372713, v7
	v_mul_f32_e32 v5, v5, v7
	v_mov_b32_e32 v8, v7
	v_fmac_f32_e32 v8, v5, v8
	v_mul_f32_e32 v5, 0xbfcc422a, v8
	v_mul_f32_e32 v5, 0x3fb8aa3b, v5
	v_exp_f32_e32 v5, v5
	v_mov_b32_e32 v8, v6
	v_and_b32_e32 v10, 0xffff0000, v4
	v_mul_f32_e32 v4, 0x3d372713, v11
	v_add_f32_e32 v5, 1.0, v5
	v_rcp_f32_e32 v9, v5
	v_mul_f32_e32 v5, 0x3d372713, v6
	v_mul_f32_e32 v5, v5, v6
	v_fmac_f32_e32 v8, v5, v8
	v_mul_f32_e32 v5, 0xbfcc422a, v8
	v_mul_f32_e32 v5, 0x3fb8aa3b, v5
	v_exp_f32_e32 v5, v5
	v_mul_f32_e32 v4, v4, v11
	v_mov_b32_e32 v14, v10
	v_add_f32_e32 v5, 1.0, v5
	v_rcp_f32_e32 v8, v5
	v_mov_b32_e32 v5, v11
	v_fmac_f32_e32 v5, v4, v5
	v_mul_f32_e32 v4, 0xbfcc422a, v5
	v_mul_f32_e32 v4, 0x3fb8aa3b, v4
	v_exp_f32_e32 v4, v4
	v_pk_mul_f32 v[12:13], v[8:9], v[6:7]
	v_add_f32_e32 v4, 1.0, v4
	v_rcp_f32_e32 v5, v4
	v_mul_f32_e32 v4, 0x3d372713, v10
	v_mul_f32_e32 v4, v4, v10
	v_fmac_f32_e32 v14, v4, v14
	v_mul_f32_e32 v4, 0xbfcc422a, v14
	v_mul_f32_e32 v4, 0x3fb8aa3b, v4
	v_exp_f32_e32 v4, v4
	v_mov_b32_e32 v96, v13
	v_add_f32_e32 v4, 1.0, v4
	v_rcp_f32_e32 v4, v4
	s_nop 0
	v_pk_mul_f32 v[14:15], v[4:5], v[10:11]
	s_nop 0
	v_mov_b32_e32 v97, v15
	v_mov_b32_e32 v13, v14
	v_pk_add_f32 v[96:97], v[96:97], v[12:13]
	v_lshlrev_b32_e32 v13, 16, v3
	v_and_b32_e32 v12, 0xffff0000, v3
	v_mul_f32_e32 v3, 0x3d372713, v13
	v_mul_f32_e32 v3, v3, v13
	v_mov_b32_e32 v14, v13
	v_fmac_f32_e32 v14, v3, v14
	v_mul_f32_e32 v3, 0xbfcc422a, v14
	v_mul_f32_e32 v3, 0x3fb8aa3b, v3
	v_exp_f32_e32 v3, v3
	v_mov_b32_e32 v14, v12
	v_add_f32_e32 v3, 1.0, v3
	v_rcp_f32_e32 v15, v3
	v_mul_f32_e32 v3, 0x3d372713, v12
	v_mul_f32_e32 v3, v3, v12
	v_fmac_f32_e32 v14, v3, v14
	v_mul_f32_e32 v3, 0xbfcc422a, v14
	v_mul_f32_e32 v3, 0x3fb8aa3b, v3
	v_exp_f32_e32 v3, v3
	s_nop 0
	v_add_f32_e32 v3, 1.0, v3
	v_rcp_f32_e32 v14, v3
	v_mov_b32_e32 v3, v149
	v_fmac_f32_e32 v3, v2, v3
	v_mul_f32_e32 v2, 0xbfcc422a, v3
	v_mul_f32_e32 v2, 0x3fb8aa3b, v2
	v_exp_f32_e32 v2, v2
	v_pk_mul_f32 v[98:99], v[14:15], v[12:13]
	v_add_f32_e32 v2, 1.0, v2
	v_rcp_f32_e32 v3, v2
	v_mul_f32_e32 v2, 0x3d372713, v148
	v_mul_f32_e32 v2, v2, v148
	v_fmac_f32_e32 v100, v2, v100
	v_mul_f32_e32 v2, 0xbfcc422a, v100
	v_mul_f32_e32 v2, 0x3fb8aa3b, v2
	v_exp_f32_e32 v2, v2
	v_mov_b32_e32 v124, v99
	v_add_f32_e32 v2, 1.0, v2
	v_rcp_f32_e32 v2, v2
	s_nop 0
	v_pk_mul_f32 v[100:101], v[2:3], v[148:149]
	s_nop 0
	v_mov_b32_e32 v125, v101
	v_mov_b32_e32 v99, v100
	v_pk_add_f32 v[98:99], v[124:125], v[98:99]
	s_nop 0
	v_add_f32_e32 v95, v99, v95
	v_add_f32_e32 v95, v98, v95
	v_add_f32_e32 v95, v97, v95
	v_add_f32_e32 v95, v96, v95
	s_waitcnt lgkmcnt(0)
	s_nop 1
	v_add_f32_dpp v95, v95, v95 quad_perm:[1,0,3,2] row_mask:0xf bank_mask:0xf
	ds_swizzle_b32 v96, v95 offset:swizzle(SWAP,2)
	s_waitcnt lgkmcnt(0)
; #define LAS __attribute__((address_space(3)))
; __device__ __forceinline__ unsigned f2bf(float f) { unsigned u = __float_as_uint(f); return (u + 0x7fffu + ((u >> 16) & 1u)) >> 16; }
; #define SHX(v, m) (((m) < 32) ? __int_as_float(__builtin_amdgcn_ds_swizzle(__float_as_int(v), ((((m) & 31) << 10) | 0x1f))) : shx32(v))
; __device__ __forceinline__ void gmlp_unit(LAS unsigned char* L, int u, const bf16* z, const bf16* wsb, const float* bs, const float* lng, const float* lnb, bf16* mix, int tid_) {
;     ...
;       s1 += SHX(s1, 1); s1 += SHX(s1, 2); const float mean = s1 * (1.f / 256.f); float s2 = 0.f;
; #pragma unroll
;       for (int i = 0; i < 64; ++i) { x[i] -= mean; s2 += x[i] * x[i]; }
;       s2 += SHX(s2, 1); s2 += SHX(s2, 2); const float rstd = rsqrtf(s2 * (1.f / 256.f) + EPS);
; #pragma unroll
;       for (int q = 0; q < 16; ++q) { const f32x4 gq = ((const f32x4*)(lng + part * 64))[q], bq = ((const f32x4*)(lnb + part * 64))[q];
; #pragma unroll
;           for (int e = 0; e < 4; ++e) { const int i = 4 * q + e, col = part * 64 + i; *(LAS bf16*)(L + col * 272 + j * 2) = (bf16)f2bf(x[i] * rstd * gq[e] + bq[e]); } } }
	v_add_f32_e32 v147, v95, v96
	v_mul_f32_e32 v150, 0x3b800000, v147
	v_fma_f32 v138, v23, v22, -v150
	v_fma_f32 v140, v21, v20, -v150
	v_mul_f32_e32 v20, v138, v138
	v_fmac_f32_e32 v20, v140, v140
	v_fma_f32 v137, v25, v24, -v150
	v_fmac_f32_e32 v20, v137, v137
	v_fma_f32 v136, v27, v26, -v150
	v_fmac_f32_e32 v20, v136, v136
	v_fma_f32 v135, v29, v28, -v150
	v_fmac_f32_e32 v20, v135, v135
	v_fma_f32 v134, v31, v30, -v150
	v_fmac_f32_e32 v20, v134, v134
	v_fma_f32 v132, v33, v32, -v150
	v_fmac_f32_e32 v20, v132, v132
	v_fma_f32 v131, v43, v42, -v150
	v_fmac_f32_e32 v20, v131, v131
	v_fma_f32 v130, v45, v44, -v150
	v_fmac_f32_e32 v20, v130, v130
	v_fma_f32 v129, v47, v46, -v150
	v_fmac_f32_e32 v20, v129, v129
	v_fma_f32 v128, v49, v48, -v150
	v_fmac_f32_e32 v20, v128, v128
	v_fma_f32 v127, v54, v53, -v150
	v_fmac_f32_e32 v20, v127, v127
	v_fma_f32 v126, v56, v55, -v150
	v_fmac_f32_e32 v20, v126, v126
	v_fma_f32 v125, v58, v57, -v150
	v_fmac_f32_e32 v20, v125, v125
	v_fma_f32 v124, v60, v59, -v150
	v_fmac_f32_e32 v20, v124, v124
	v_fma_f32 v122, v62, v61, -v150
	v_fmac_f32_e32 v20, v122, v122
	v_fma_f32 v102, v64, v63, -v150
	v_fmac_f32_e32 v20, v102, v102
	v_fma_f32 v101, v66, v65, -v150
	v_fmac_f32_e32 v20, v101, v101
	v_fma_f32 v100, v68, v67, -v150
	v_fmac_f32_e32 v20, v100, v100
	v_fma_f32 v99, v70, v69, -v150
	v_fmac_f32_e32 v20, v99, v99
	v_fma_f32 v98, v72, v71, -v150
	v_fmac_f32_e32 v20, v98, v98
	v_fma_f32 v97, v74, v73, -v150
	v_fmac_f32_e32 v20, v97, v97
	v_fma_f32 v96, v76, v75, -v150
	v_fmac_f32_e32 v20, v96, v96
	v_fma_f32 v95, v78, v77, -v150
	v_fmac_f32_e32 v20, v95, v95
	v_fma_f32 v79, v80, v79, -v150
	v_fmac_f32_e32 v20, v79, v79
	v_fma_f32 v78, v82, v81, -v150
	v_fmac_f32_e32 v20, v78, v78
	v_fma_f32 v77, v85, v83, -v150
	v_fmac_f32_e32 v20, v77, v77
	v_fma_f32 v76, v86, v84, -v150
	v_fmac_f32_e32 v20, v76, v76
	v_fma_f32 v75, v89, v87, -v150
	v_fmac_f32_e32 v20, v75, v75
	v_fma_f32 v74, v90, v88, -v150
	v_fmac_f32_e32 v20, v74, v74
	v_fma_f32 v73, v93, v91, -v150
	v_fmac_f32_e32 v20, v73, v73
	v_fma_f32 v72, v94, v92, -v150
	v_fmac_f32_e32 v20, v72, v72
	v_fma_f32 v71, v19, v18, -v150
	v_fmac_f32_e32 v20, v71, v71
	v_fma_f32 v70, v104, v103, -v150
	v_fmac_f32_e32 v20, v70, v70
	v_fma_f32 v69, v106, v105, -v150
	v_fmac_f32_e32 v20, v69, v69
	v_fma_f32 v68, v108, v107, -v150
	v_fmac_f32_e32 v20, v68, v68
	v_fma_f32 v67, v110, v109, -v150
	v_fmac_f32_e32 v20, v67, v67
	v_fma_f32 v66, v111, v16, -v150
	v_fmac_f32_e32 v20, v66, v66
	v_fma_f32 v65, v113, v112, -v150
	v_fmac_f32_e32 v20, v65, v65
	v_fma_f32 v64, v114, v17, -v150
	v_fmac_f32_e32 v20, v64, v64
	v_fma_f32 v63, v116, v115, -v150
	v_fmac_f32_e32 v20, v63, v63
	v_fma_f32 v62, v118, v117, -v150
	v_fmac_f32_e32 v20, v62, v62
	v_fma_f32 v61, v120, v119, -v150
	v_fmac_f32_e32 v20, v61, v61
	v_fma_f32 v60, v123, v121, -v150
	v_fmac_f32_e32 v20, v60, v60
	v_fma_f32 v59, v139, v133, -v150
	v_fmac_f32_e32 v20, v59, v59
	v_fma_f32 v58, v142, v141, -v150
	v_fmac_f32_e32 v20, v58, v58
	v_fma_f32 v57, v144, v143, -v150
	v_fmac_f32_e32 v20, v57, v57
	v_fma_f32 v56, v146, v145, -v150
	v_fmac_f32_e32 v20, v56, v56
	v_fmamk_f32 v54, v147, 0xbb800000, v34
	v_fmac_f32_e32 v20, v54, v54
	v_fmamk_f32 v53, v147, 0xbb800000, v36
	v_fmac_f32_e32 v20, v53, v53
	v_fmac_f32_e32 v35, 0xbb800000, v147
	v_fmac_f32_e32 v20, v35, v35
	v_fmac_f32_e32 v37, 0xbb800000, v147
	v_fmac_f32_e32 v20, v37, v37
	v_fmamk_f32 v38, v147, 0xbb800000, v38
	v_fmac_f32_e32 v20, v38, v38
	v_fmamk_f32 v36, v147, 0xbb800000, v40
	v_fmac_f32_e32 v20, v36, v36
	v_fmac_f32_e32 v39, 0xbb800000, v147
	v_fmac_f32_e32 v20, v39, v39
	v_fmac_f32_e32 v41, 0xbb800000, v147
	v_pk_fma_f32 v[48:49], v[2:3], v[148:149], v[150:151] op_sel_hi:[1,1,0] neg_lo:[0,0,1] neg_hi:[0,0,1]
	v_fmac_f32_e32 v20, v41, v41
	v_pk_mul_f32 v[2:3], v[48:49], v[48:49]
	v_pk_fma_f32 v[46:47], v[14:15], v[12:13], v[150:151] op_sel_hi:[1,1,0] neg_lo:[0,0,1] neg_hi:[0,0,1]
	v_add_f32_e32 v3, v3, v20
	v_add_f32_e32 v16, v2, v3
	v_pk_mul_f32 v[2:3], v[46:47], v[46:47]
	v_pk_fma_f32 v[44:45], v[4:5], v[10:11], v[150:151] op_sel_hi:[1,1,0] neg_lo:[0,0,1] neg_hi:[0,0,1]
	v_add_f32_e32 v3, v3, v16
	v_add_f32_e32 v12, v2, v3
	v_pk_mul_f32 v[2:3], v[44:45], v[44:45]
	v_pk_fma_f32 v[42:43], v[8:9], v[6:7], v[150:151] op_sel_hi:[1,1,0] neg_lo:[0,0,1] neg_hi:[0,0,1]
	v_add_f32_e32 v3, v3, v12
	v_add_f32_e32 v4, v2, v3
	v_pk_mul_f32 v[2:3], v[42:43], v[42:43]
	v_lshlrev_b32_e32 v55, 2, v51
	v_add_f32_e32 v3, v3, v4
	v_add_f32_e32 v2, v2, v3
	v_lshlrev_b32_e32 v40, 1, v50
	s_waitcnt lgkmcnt(0)
	s_nop 1
	v_add_f32_dpp v2, v2, v2 quad_perm:[1,0,3,2] row_mask:0xf bank_mask:0xf
	s_waitcnt lgkmcnt(0)
	s_nop 1
	v_add_f32_dpp v2, v2, v2 quad_perm:[2,3,0,1] row_mask:0xf bank_mask:0xf
	v_fmamk_f32 v2, v2, 0x3b800000, v196
	v_cmp_gt_f32_e32 vcc, s73, v2
	v_mul_f32_e32 v3, 0x4b800000, v2
	s_nop 0
	v_cndmask_b32_e32 v2, v2, v3, vcc
	v_rsq_f32_e32 v2, v2
	s_nop 0
	v_mul_f32_e32 v3, 0x45800000, v2
	v_cndmask_b32_e32 v34, v2, v3, vcc
	global_load_dwordx4 v[2:5], v55, s[54:55] offset:48
	global_load_dwordx4 v[10:13], v55, s[54:55] offset:32
	global_load_dwordx4 v[18:21], v55, s[54:55] offset:16
	global_load_dwordx4 v[26:29], v55, s[54:55]
	global_load_dwordx4 v[6:9], v55, s[42:43] offset:48
	global_load_dwordx4 v[14:17], v55, s[42:43] offset:32
	global_load_dwordx4 v[22:25], v55, s[42:43] offset:16
	global_load_dwordx4 v[30:33], v55, s[42:43]
	v_mul_f32_e32 v80, v140, v34
	s_waitcnt vmcnt(0)
; #define LAS __attribute__((address_space(3)))
; __device__ __forceinline__ unsigned f2bf(float f) { unsigned u = __float_as_uint(f); return (u + 0x7fffu + ((u >> 16) & 1u)) >> 16; }
; __device__ __forceinline__ void gmlp_unit(LAS unsigned char* L, int u, const bf16* z, const bf16* wsb, const float* bs, const float* lng, const float* lnb, bf16* mix, int tid_) {
;     ...
; #pragma unroll
;       for (int q = 0; q < 16; ++q) { const f32x4 gq = ((const f32x4*)(lng + part * 64))[q], bq = ((const f32x4*)(lnb + part * 64))[q];
; #pragma unroll
;           for (int e = 0; e < 4; ++e) { const int i = 4 * q + e, col = part * 64 + i; *(LAS bf16*)(L + col * 272 + j * 2) = (bf16)f2bf(x[i] * rstd * gq[e] + bq[e]); } } }
	v_fma_f32 v26, v26, v80, v30
	v_bfe_u32 v30, v26, 16, 1
	v_add3_u32 v26, v26, v30, s78
	v_mul_u32_u24_e32 v30, 0x110, v51
	v_add3_u32 v40, 0, v40, v30
	ds_write_b16_d16_hi v40, v26
	v_mul_f32_e32 v26, v138, v34
	v_fma_f32 v26, v27, v26, v31
	v_bfe_u32 v27, v26, 16, 1
	v_add3_u32 v26, v26, v27, s78
	ds_write_b16_d16_hi v40, v26 offset:272
	v_mul_f32_e32 v26, v137, v34
	v_fma_f32 v26, v28, v26, v32
	v_bfe_u32 v27, v26, 16, 1
	v_add3_u32 v26, v26, v27, s78
	ds_write_b16_d16_hi v40, v26 offset:544
	v_mul_f32_e32 v26, v136, v34
	v_fmac_f32_e32 v33, v29, v26
	v_bfe_u32 v26, v33, 16, 1
	v_add3_u32 v26, v33, v26, s78
	ds_write_b16_d16_hi v40, v26 offset:816
	v_mul_f32_e32 v26, v135, v34
	v_fma_f32 v18, v18, v26, v22
	v_bfe_u32 v22, v18, 16, 1
	v_add3_u32 v18, v18, v22, s78
	ds_write_b16_d16_hi v40, v18 offset:1088
	v_mul_f32_e32 v18, v134, v34
	v_fma_f32 v18, v19, v18, v23
	v_bfe_u32 v19, v18, 16, 1
	v_add3_u32 v18, v18, v19, s78
	ds_write_b16_d16_hi v40, v18 offset:1360
	v_mul_f32_e32 v18, v132, v34
	v_fma_f32 v18, v20, v18, v24
	v_bfe_u32 v19, v18, 16, 1
	v_add3_u32 v18, v18, v19, s78
	ds_write_b16_d16_hi v40, v18 offset:1632
	v_mul_f32_e32 v18, v131, v34
	v_fmac_f32_e32 v25, v21, v18
	v_bfe_u32 v18, v25, 16, 1
	v_add3_u32 v18, v25, v18, s78
	ds_write_b16_d16_hi v40, v18 offset:1904
	v_mul_f32_e32 v18, v130, v34
	v_fma_f32 v10, v10, v18, v14
	v_bfe_u32 v14, v10, 16, 1
	v_add3_u32 v10, v10, v14, s78
	ds_write_b16_d16_hi v40, v10 offset:2176
	v_mul_f32_e32 v10, v129, v34
	v_fma_f32 v10, v11, v10, v15
	v_bfe_u32 v11, v10, 16, 1
	v_add3_u32 v10, v10, v11, s78
	ds_write_b16_d16_hi v40, v10 offset:2448
	v_mul_f32_e32 v10, v128, v34
	v_fma_f32 v10, v12, v10, v16
	v_bfe_u32 v11, v10, 16, 1
	v_add3_u32 v10, v10, v11, s78
	ds_write_b16_d16_hi v40, v10 offset:2720
	v_mul_f32_e32 v10, v127, v34
	v_fmac_f32_e32 v17, v13, v10
	v_bfe_u32 v10, v17, 16, 1
	v_add3_u32 v10, v17, v10, s78
	ds_write_b16_d16_hi v40, v10 offset:2992
	v_mul_f32_e32 v10, v126, v34
	v_fma_f32 v2, v2, v10, v6
	v_bfe_u32 v6, v2, 16, 1
	v_add3_u32 v2, v2, v6, s78
	ds_write_b16_d16_hi v40, v2 offset:3264
	v_mul_f32_e32 v2, v125, v34
	v_fma_f32 v2, v3, v2, v7
	v_bfe_u32 v3, v2, 16, 1
	v_add3_u32 v2, v2, v3, s78
	ds_write_b16_d16_hi v40, v2 offset:3536
	v_mul_f32_e32 v2, v124, v34
	v_fma_f32 v2, v4, v2, v8
	v_bfe_u32 v3, v2, 16, 1
	v_add3_u32 v2, v2, v3, s78
	ds_write_b16_d16_hi v40, v2 offset:3808
	v_mul_f32_e32 v2, v122, v34
	v_fmac_f32_e32 v9, v5, v2
	v_bfe_u32 v2, v9, 16, 1
	v_add3_u32 v2, v9, v2, s78
	ds_write_b16_d16_hi v40, v2 offset:4080
	global_load_dwordx4 v[2:5], v55, s[54:55] offset:112
	global_load_dwordx4 v[6:9], v55, s[54:55] offset:96
	global_load_dwordx4 v[10:13], v55, s[54:55] offset:80
	global_load_dwordx4 v[26:29], v55, s[54:55] offset:64
	global_load_dwordx4 v[14:17], v55, s[42:43] offset:112
	global_load_dwordx4 v[18:21], v55, s[42:43] offset:96
	global_load_dwordx4 v[22:25], v55, s[42:43] offset:80
	global_load_dwordx4 v[30:33], v55, s[42:43] offset:64
	v_mul_f32_e32 v51, v102, v34
	s_waitcnt vmcnt(0)
	v_fma_f32 v26, v26, v51, v30
	v_bfe_u32 v30, v26, 16, 1
	v_add3_u32 v26, v26, v30, s78
	ds_write_b16_d16_hi v40, v26 offset:4352
	v_mul_f32_e32 v26, v101, v34
	v_fma_f32 v26, v27, v26, v31
	v_bfe_u32 v27, v26, 16, 1
	v_add3_u32 v26, v26, v27, s78
	ds_write_b16_d16_hi v40, v26 offset:4624
	v_mul_f32_e32 v26, v100, v34
	v_fma_f32 v26, v28, v26, v32
	v_bfe_u32 v27, v26, 16, 1
	v_add3_u32 v26, v26, v27, s78
	ds_write_b16_d16_hi v40, v26 offset:4896
	v_mul_f32_e32 v26, v99, v34
	v_fmac_f32_e32 v33, v29, v26
	v_bfe_u32 v26, v33, 16, 1
	v_add3_u32 v26, v33, v26, s78
	ds_write_b16_d16_hi v40, v26 offset:5168
	v_mul_f32_e32 v26, v98, v34
	v_fma_f32 v10, v10, v26, v22
	v_bfe_u32 v22, v10, 16, 1
	v_add3_u32 v10, v10, v22, s78
	ds_write_b16_d16_hi v40, v10 offset:5440
	v_mul_f32_e32 v10, v97, v34
	v_fma_f32 v10, v11, v10, v23
	v_bfe_u32 v11, v10, 16, 1
	v_add3_u32 v10, v10, v11, s78
	ds_write_b16_d16_hi v40, v10 offset:5712
	v_mul_f32_e32 v10, v96, v34
	v_fma_f32 v10, v12, v10, v24
	v_bfe_u32 v11, v10, 16, 1
	v_add3_u32 v10, v10, v11, s78
	ds_write_b16_d16_hi v40, v10 offset:5984
	v_mul_f32_e32 v10, v95, v34
	v_fmac_f32_e32 v25, v13, v10
	v_bfe_u32 v10, v25, 16, 1
	v_add3_u32 v10, v25, v10, s78
	ds_write_b16_d16_hi v40, v10 offset:6256
	v_mul_f32_e32 v10, v79, v34
	v_fma_f32 v6, v6, v10, v18
	v_bfe_u32 v10, v6, 16, 1
	v_add3_u32 v6, v6, v10, s78
	ds_write_b16_d16_hi v40, v6 offset:6528
	v_mul_f32_e32 v6, v78, v34
	v_fma_f32 v6, v7, v6, v19
	v_bfe_u32 v7, v6, 16, 1
	v_add3_u32 v6, v6, v7, s78
	ds_write_b16_d16_hi v40, v6 offset:6800
	v_mul_f32_e32 v6, v77, v34
	v_fma_f32 v6, v8, v6, v20
	v_bfe_u32 v7, v6, 16, 1
	v_add3_u32 v6, v6, v7, s78
	ds_write_b16_d16_hi v40, v6 offset:7072
	v_mul_f32_e32 v6, v76, v34
	v_fmac_f32_e32 v21, v9, v6
	v_bfe_u32 v6, v21, 16, 1
	v_add3_u32 v6, v21, v6, s78
	ds_write_b16_d16_hi v40, v6 offset:7344
	v_mul_f32_e32 v6, v75, v34
	v_fma_f32 v2, v2, v6, v14
	v_bfe_u32 v6, v2, 16, 1
	v_add3_u32 v2, v2, v6, s78
	ds_write_b16_d16_hi v40, v2 offset:7616
	v_mul_f32_e32 v2, v74, v34
	v_fma_f32 v2, v3, v2, v15
	v_bfe_u32 v3, v2, 16, 1
	v_add3_u32 v2, v2, v3, s78
	ds_write_b16_d16_hi v40, v2 offset:7888
	v_mul_f32_e32 v2, v73, v34
	v_fma_f32 v2, v4, v2, v16
	v_bfe_u32 v3, v2, 16, 1
	v_add3_u32 v2, v2, v3, s78
	ds_write_b16_d16_hi v40, v2 offset:8160
	v_mul_f32_e32 v2, v72, v34
	v_fmac_f32_e32 v17, v5, v2
	v_bfe_u32 v2, v17, 16, 1
	v_add3_u32 v2, v17, v2, s78
	ds_write_b16_d16_hi v40, v2 offset:8432
	global_load_dwordx4 v[2:5], v55, s[54:55] offset:176
	global_load_dwordx4 v[6:9], v55, s[54:55] offset:160
	global_load_dwordx4 v[10:13], v55, s[54:55] offset:144
	global_load_dwordx4 v[26:29], v55, s[54:55] offset:128
	global_load_dwordx4 v[14:17], v55, s[42:43] offset:176
	global_load_dwordx4 v[18:21], v55, s[42:43] offset:160
	global_load_dwordx4 v[22:25], v55, s[42:43] offset:144
	global_load_dwordx4 v[30:33], v55, s[42:43] offset:128
	v_mul_f32_e32 v51, v71, v34
	s_waitcnt vmcnt(0)
; #define LAS __attribute__((address_space(3)))
; __device__ __forceinline__ unsigned f2bf(float f) { unsigned u = __float_as_uint(f); return (u + 0x7fffu + ((u >> 16) & 1u)) >> 16; }
; __device__ __forceinline__ void gmlp_unit(LAS unsigned char* L, int u, const bf16* z, const bf16* wsb, const float* bs, const float* lng, const float* lnb, bf16* mix, int tid_) {
;     ...
; #pragma unroll
;       for (int q = 0; q < 16; ++q) { const f32x4 gq = ((const f32x4*)(lng + part * 64))[q], bq = ((const f32x4*)(lnb + part * 64))[q];
; #pragma unroll
;           for (int e = 0; e < 4; ++e) { const int i = 4 * q + e, col = part * 64 + i; *(LAS bf16*)(L + col * 272 + j * 2) = (bf16)f2bf(x[i] * rstd * gq[e] + bq[e]); } } }
;     __syncthreads();
; #pragma unroll 1
;     for (int hh = 0; hh < 4; ++hh) { f32x4 acc[4];
; #pragma unroll
;         for (int nt = 0; nt < 4; ++nt) acc[nt] = (f32x4){0.f, 0.f, 0.f, 0.f};
; #pragma unroll
;         for (int ks = 0; ks < 4; ++ks) { const bf16x8 a = *(const bf16x8*)(wsb + ((size_t)(hh * 128 + 16 * w + fr) * 128 + ks * 32 + fq * 8));
	v_fma_f32 v26, v26, v51, v30
	v_bfe_u32 v30, v26, 16, 1
	v_add3_u32 v26, v26, v30, s78
	ds_write_b16_d16_hi v40, v26 offset:8704
	v_mul_f32_e32 v26, v70, v34
	v_fma_f32 v26, v27, v26, v31
	v_bfe_u32 v27, v26, 16, 1
	v_add3_u32 v26, v26, v27, s78
	ds_write_b16_d16_hi v40, v26 offset:8976
	v_mul_f32_e32 v26, v69, v34
	v_fma_f32 v26, v28, v26, v32
	v_bfe_u32 v27, v26, 16, 1
	v_add3_u32 v26, v26, v27, s78
	ds_write_b16_d16_hi v40, v26 offset:9248
	v_mul_f32_e32 v26, v68, v34
	v_fmac_f32_e32 v33, v29, v26
	v_bfe_u32 v26, v33, 16, 1
	v_add3_u32 v26, v33, v26, s78
	ds_write_b16_d16_hi v40, v26 offset:9520
	v_mul_f32_e32 v26, v67, v34
	v_fma_f32 v10, v10, v26, v22
	v_bfe_u32 v22, v10, 16, 1
	v_add3_u32 v10, v10, v22, s78
	ds_write_b16_d16_hi v40, v10 offset:9792
	v_mul_f32_e32 v10, v66, v34
	v_fma_f32 v10, v11, v10, v23
	v_bfe_u32 v11, v10, 16, 1
	v_add3_u32 v10, v10, v11, s78
	ds_write_b16_d16_hi v40, v10 offset:10064
	v_mul_f32_e32 v10, v65, v34
	v_fma_f32 v10, v12, v10, v24
	v_bfe_u32 v11, v10, 16, 1
	v_add3_u32 v10, v10, v11, s78
	ds_write_b16_d16_hi v40, v10 offset:10336
	v_mul_f32_e32 v10, v64, v34
	v_fmac_f32_e32 v25, v13, v10
	v_bfe_u32 v10, v25, 16, 1
	v_add3_u32 v10, v25, v10, s78
	ds_write_b16_d16_hi v40, v10 offset:10608
	v_mul_f32_e32 v10, v63, v34
	v_fma_f32 v6, v6, v10, v18
	v_bfe_u32 v10, v6, 16, 1
	v_add3_u32 v6, v6, v10, s78
	ds_write_b16_d16_hi v40, v6 offset:10880
	v_mul_f32_e32 v6, v62, v34
	v_fma_f32 v6, v7, v6, v19
	v_bfe_u32 v7, v6, 16, 1
	v_add3_u32 v6, v6, v7, s78
	ds_write_b16_d16_hi v40, v6 offset:11152
	v_mul_f32_e32 v6, v61, v34
	v_fma_f32 v6, v8, v6, v20
	v_bfe_u32 v7, v6, 16, 1
	v_add3_u32 v6, v6, v7, s78
	ds_write_b16_d16_hi v40, v6 offset:11424
	v_mul_f32_e32 v6, v60, v34
	v_fmac_f32_e32 v21, v9, v6
	v_bfe_u32 v6, v21, 16, 1
	v_add3_u32 v6, v21, v6, s78
	ds_write_b16_d16_hi v40, v6 offset:11696
	v_mul_f32_e32 v6, v59, v34
	v_fma_f32 v2, v2, v6, v14
	v_bfe_u32 v6, v2, 16, 1
	v_add3_u32 v2, v2, v6, s78
	ds_write_b16_d16_hi v40, v2 offset:11968
	v_mul_f32_e32 v2, v58, v34
	v_fma_f32 v2, v3, v2, v15
	v_bfe_u32 v3, v2, 16, 1
	v_add3_u32 v2, v2, v3, s78
	ds_write_b16_d16_hi v40, v2 offset:12240
	v_mul_f32_e32 v2, v57, v34
	v_fma_f32 v2, v4, v2, v16
	v_bfe_u32 v3, v2, 16, 1
	v_add3_u32 v2, v2, v3, s78
	ds_write_b16_d16_hi v40, v2 offset:12512
	v_mul_f32_e32 v2, v56, v34
	v_fmac_f32_e32 v17, v5, v2
	v_bfe_u32 v2, v17, 16, 1
	v_add3_u32 v2, v17, v2, s78
	ds_write_b16_d16_hi v40, v2 offset:12784
	global_load_dwordx4 v[2:5], v55, s[54:55] offset:240
	global_load_dwordx4 v[6:9], v55, s[54:55] offset:224
	global_load_dwordx4 v[10:13], v55, s[54:55] offset:208
	global_load_dwordx4 v[26:29], v55, s[54:55] offset:192
	global_load_dwordx4 v[14:17], v55, s[42:43] offset:240
	global_load_dwordx4 v[18:21], v55, s[42:43] offset:224
	global_load_dwordx4 v[22:25], v55, s[42:43] offset:208
	global_load_dwordx4 v[30:33], v55, s[42:43] offset:192
	v_mul_f32_e32 v51, v54, v34
	s_waitcnt vmcnt(0)
	v_fma_f32 v26, v26, v51, v30
	v_bfe_u32 v30, v26, 16, 1
	v_add3_u32 v26, v26, v30, s78
	ds_write_b16_d16_hi v40, v26 offset:13056
	v_mul_f32_e32 v26, v53, v34
	v_fma_f32 v26, v27, v26, v31
	v_bfe_u32 v27, v26, 16, 1
	v_add3_u32 v26, v26, v27, s78
	ds_write_b16_d16_hi v40, v26 offset:13328
	v_mul_f32_e32 v26, v35, v34
	v_fma_f32 v26, v28, v26, v32
	v_bfe_u32 v27, v26, 16, 1
	v_add3_u32 v26, v26, v27, s78
	ds_write_b16_d16_hi v40, v26 offset:13600
	v_mul_f32_e32 v26, v37, v34
	v_fmac_f32_e32 v33, v29, v26
	v_bfe_u32 v26, v33, 16, 1
	v_add3_u32 v26, v33, v26, s78
	ds_write_b16_d16_hi v40, v26 offset:13872
	v_mul_f32_e32 v26, v38, v34
	v_fma_f32 v10, v10, v26, v22
	v_bfe_u32 v22, v10, 16, 1
	v_add3_u32 v10, v10, v22, s78
	ds_write_b16_d16_hi v40, v10 offset:14144
	v_mul_f32_e32 v10, v36, v34
	v_fma_f32 v10, v11, v10, v23
	v_bfe_u32 v11, v10, 16, 1
	v_add3_u32 v10, v10, v11, s78
	ds_write_b16_d16_hi v40, v10 offset:14416
	v_mul_f32_e32 v10, v39, v34
	v_fma_f32 v10, v12, v10, v24
	v_bfe_u32 v11, v10, 16, 1
	v_add3_u32 v10, v10, v11, s78
	ds_write_b16_d16_hi v40, v10 offset:14688
	v_mul_f32_e32 v10, v41, v34
	v_fmac_f32_e32 v25, v13, v10
	v_bfe_u32 v10, v25, 16, 1
	v_add3_u32 v10, v25, v10, s78
	ds_write_b16_d16_hi v40, v10 offset:14960
	v_mul_f32_e32 v10, v49, v34
	v_fma_f32 v6, v6, v10, v18
	v_bfe_u32 v10, v6, 16, 1
	v_add3_u32 v6, v6, v10, s78
	ds_write_b16_d16_hi v40, v6 offset:15232
	v_mul_f32_e32 v6, v48, v34
	v_fma_f32 v6, v7, v6, v19
	v_bfe_u32 v7, v6, 16, 1
	v_add3_u32 v6, v6, v7, s78
	ds_write_b16_d16_hi v40, v6 offset:15504
	v_mul_f32_e32 v6, v47, v34
	v_fma_f32 v6, v8, v6, v20
	v_bfe_u32 v7, v6, 16, 1
	v_add3_u32 v6, v6, v7, s78
	ds_write_b16_d16_hi v40, v6 offset:15776
	v_mul_f32_e32 v6, v46, v34
	v_fmac_f32_e32 v21, v9, v6
	v_bfe_u32 v6, v21, 16, 1
	v_add3_u32 v6, v21, v6, s78
	ds_write_b16_d16_hi v40, v6 offset:16048
	v_mul_f32_e32 v6, v45, v34
	v_fma_f32 v2, v2, v6, v14
	v_bfe_u32 v6, v2, 16, 1
	v_add3_u32 v2, v2, v6, s78
	ds_write_b16_d16_hi v40, v2 offset:16320
	v_mul_f32_e32 v2, v44, v34
	v_fma_f32 v2, v3, v2, v15
	v_bfe_u32 v3, v2, 16, 1
	v_add3_u32 v2, v2, v3, s78
	ds_write_b16_d16_hi v40, v2 offset:16592
	v_mul_f32_e32 v2, v43, v34
	v_fma_f32 v2, v4, v2, v16
	v_bfe_u32 v3, v2, 16, 1
	v_add3_u32 v2, v2, v3, s78
	ds_write_b16_d16_hi v40, v2 offset:16864
	v_mul_f32_e32 v2, v42, v34
	v_fmac_f32_e32 v17, v5, v2
	v_bfe_u32 v2, v17, 16, 1
	v_add3_u32 v2, v17, v2, s78
	ds_write_b16_d16_hi v40, v2 offset:17136
	v_bfe_u32 v2, v1, 4, 2
	v_and_b32_e32 v3, -16, v50
	v_bfi_b32 v14, -16, v50, v1
	v_lshlrev_b32_e32 v1, 3, v2
	v_lshlrev_b32_e32 v162, 4, v2
	v_add3_u32 v2, s11, v3, v52
	v_ashrrev_i32_e32 v3, 31, v2
	v_lshlrev_b64 v[4:5], 11, v[2:3]
	v_lshlrev_b64 v[2:3], 12, v[2:3]
	v_or_b32_e32 v4, v4, v1
	v_or_b32_e32 v2, v2, v1
	v_mul_u32_u24_e32 v1, 0x110, v52
	v_lshl_add_u64 v[16:17], s[50:51], 0, v[162:163]
	v_lshl_add_u64 v[18:19], s[0:1], 0, v[4:5]
	v_lshl_add_u64 v[20:21], s[0:1], 0, v[2:3]
	v_add3_u32 v1, v1, v162, 0
	s_waitcnt lgkmcnt(0)
	s_barrier

; #define LAS __attribute__((address_space(3)))
; __device__ __forceinline__ float bflo(unsigned w) { return __uint_as_float(w << 16); }
; __device__ __forceinline__ float bfhi(unsigned w) { return __uint_as_float(w & 0xffff0000u); }
; __device__ __forceinline__ float geluf_(float x) { const float t = 1.5957691216f * (x + 0.044715f * x * x * x); return x * __builtin_amdgcn_rcpf(1.f + __expf(-t)); }
; __device__ __forceinline__ int otid() { int t = threadIdx.x; asm volatile("" : "+v"(t)); return t; }
; __device__ __forceinline__ void gmlp_unit(LAS unsigned char* L, int u, const bf16* z, const bf16* wsb, const float* bs, const float* lng, const float* lnb, bf16* mix, int tid_) {
;     const int tid = otid(); (void)tid_;
;     const int lane = tid & 63, w = tid >> 6, fr = lane & 15, fq = lane >> 4, t0 = u * 128;
;     { const int j = tid >> 2, part = tid & 3; const bf16* src = z + (size_t)(t0 + j) * 2048 + 256 + part * 64; float x[64]; float s1 = 0.f;
; #pragma unroll
;       for (int q = 0; q < 8; ++q) { const v4u w4 = *(const v4u*)(src + 8 * q); const unsigned ww[4] = {w4.x, w4.y, w4.z, w4.w};
; #pragma unroll
;           for (int i = 0; i < 4; ++i) { x[q * 8 + 2 * i] = geluf_(bflo(ww[i])); x[q * 8 + 2 * i + 1] = geluf_(bfhi(ww[i])); s1 += x[q * 8 + 2 * i] + x[q * 8 + 2 * i + 1]; } }
.LBB0_781:
	s_mov_b64 s[8:9], s[76:77]
	s_load_dwordx2 s[6:7], s[8:9], 0x48
	s_load_dwordx2 s[0:1], s[8:9], 0x58
	s_load_dwordx2 s[64:65], s[8:9], 0xd8
	v_readlane_b32 s4, v254, 17
	v_readlane_b32 s5, v254, 18
	s_andn2_b64 vcc, exec, s[4:5]
	s_cbranch_vccnz .LBB0_785
	s_load_dwordx4 s[24:27], s[8:9], 0x28
	s_load_dwordx2 s[4:5], s[8:9], 0x40
	s_mov_b32 s87, s17
	s_lshl_b64 s[8:9], s[86:87], 17
	s_waitcnt lgkmcnt(0)
	s_add_u32 s20, s64, s8
	s_addc_u32 s21, s65, s9
	s_lshl_b64 s[8:9], s[86:87], 11
	v_mov_b32_e32 v1, v0
	s_add_u32 s12, s4, s8
	v_readlane_b32 s8, v254, 20
	s_waitcnt vmcnt(0)
	v_ashrrev_i32_e32 v50, 2, v1
	s_addc_u32 s13, s5, s9
	s_lshl_b64 s[4:5], s[86:87], 10
	v_add_u32_e32 v2, s8, v50
	s_add_u32 s30, s24, s4
	v_ashrrev_i32_e32 v3, 31, v2
	v_lshlrev_b32_e32 v4, 6, v1
	s_addc_u32 s31, s25, s5
	v_lshlrev_b64 v[2:3], 12, v[2:3]
	v_and_b32_e32 v51, 0xc0, v4
	s_add_u32 s28, s26, s4
	v_lshl_add_u64 v[2:3], s[64:65], 0, v[2:3]
	v_lshlrev_b32_e32 v162, 1, v51
	s_addc_u32 s29, s27, s5
	v_lshl_add_u64 v[2:3], v[2:3], 0, v[162:163]
	s_mov_b64 s[4:5], 0x4e600000
	v_lshl_add_u64 v[18:19], v[2:3], 0, s[4:5]
	global_load_dwordx4 v[2:5], v[18:19], off offset:560
	global_load_dwordx4 v[6:9], v[18:19], off offset:544
	global_load_dwordx4 v[10:13], v[18:19], off offset:528
	global_load_dwordx4 v[14:17], v[18:19], off offset:512
	v_and_b32_e32 v52, 15, v1
	s_mov_b64 s[4:5], 0x2d00000
	s_waitcnt vmcnt(3)
	v_and_b32_e32 v81, 0xffff0000, v2
	s_waitcnt vmcnt(2)
	v_and_b32_e32 v65, 0xffff0000, v6
	s_waitcnt vmcnt(1)
	v_and_b32_e32 v46, 0xffff0000, v10
	s_waitcnt vmcnt(0)
	v_and_b32_e32 v22, 0xffff0000, v14
	v_lshlrev_b32_e32 v20, 16, v14
	v_mul_f32_e32 v14, 0x3d372713, v22
	v_and_b32_e32 v26, 0xffff0000, v15
	v_mul_f32_e32 v21, 0x3d372713, v20
	v_mul_f32_e32 v14, v14, v22
	v_lshlrev_b32_e32 v24, 16, v15
	v_mul_f32_e32 v15, 0x3d372713, v26
	v_mul_f32_e32 v21, v21, v20
	v_fma_f32 v14, v14, v22, v22
	v_mul_f32_e32 v25, 0x3d372713, v24
	v_mul_f32_e32 v15, v15, v26
	v_fma_f32 v21, v21, v20, v20
	v_mul_f32_e32 v14, 0xbfcc422a, v14
	v_mul_f32_e32 v25, v25, v24
	v_fma_f32 v15, v15, v26, v26
	v_mul_f32_e32 v21, 0xbfcc422a, v21
	v_mul_f32_e32 v14, 0x3fb8aa3b, v14
	v_fma_f32 v25, v25, v24, v24
	v_mul_f32_e32 v15, 0xbfcc422a, v15
	v_mul_f32_e32 v21, 0x3fb8aa3b, v21
	v_exp_f32_e32 v14, v14
	v_mul_f32_e32 v25, 0xbfcc422a, v25
	v_mul_f32_e32 v15, 0x3fb8aa3b, v15
	v_exp_f32_e32 v21, v21
	v_mul_f32_e32 v25, 0x3fb8aa3b, v25
	v_exp_f32_e32 v15, v15
	v_exp_f32_e32 v25, v25
	v_add_f32_e32 v14, 1.0, v14
	v_add_f32_e32 v21, 1.0, v21
	v_rcp_f32_e32 v23, v14
	v_add_f32_e32 v15, 1.0, v15
	v_rcp_f32_e32 v21, v21
	v_add_f32_e32 v25, 1.0, v25
	v_rcp_f32_e32 v27, v15
	v_rcp_f32_e32 v25, v25
	v_mul_f32_e32 v14, v23, v22
	v_fmac_f32_e32 v14, v21, v20
	v_mul_f32_e32 v15, v27, v26
	v_add_f32_e32 v14, 0, v14
	v_fmac_f32_e32 v15, v25, v24
	v_lshlrev_b32_e32 v28, 16, v16
	v_add_f32_e32 v14, v15, v14
	v_mul_f32_e32 v15, 0x3d372713, v28
	v_mul_f32_e32 v15, v15, v28
	v_fma_f32 v15, v15, v28, v28
	v_mul_f32_e32 v15, 0xbfcc422a, v15
	v_mul_f32_e32 v15, 0x3fb8aa3b, v15
	v_exp_f32_e32 v15, v15
	v_and_b32_e32 v30, 0xffff0000, v16
	v_lshlrev_b32_e32 v32, 16, v17
	v_and_b32_e32 v42, 0xffff0000, v17
	v_add_f32_e32 v15, 1.0, v15
	v_rcp_f32_e32 v29, v15
	v_mul_f32_e32 v15, 0x3d372713, v30
	v_mul_f32_e32 v15, v15, v30
	v_fma_f32 v15, v15, v30, v30
	v_mul_f32_e32 v15, 0xbfcc422a, v15
	v_mul_f32_e32 v15, 0x3fb8aa3b, v15
	v_exp_f32_e32 v15, v15
	v_lshlrev_b32_e32 v44, 16, v10
	v_mul_f32_e32 v10, 0x3d372713, v46
	v_mul_f32_e32 v10, v10, v46
	v_add_f32_e32 v15, 1.0, v15
	v_rcp_f32_e32 v31, v15
	v_fma_f32 v10, v10, v46, v46
	v_mul_f32_e32 v10, 0xbfcc422a, v10
	v_mul_f32_e32 v10, 0x3fb8aa3b, v10
	v_mul_f32_e32 v15, v31, v30
	v_fmac_f32_e32 v15, v29, v28
	v_add_f32_e32 v14, v15, v14
	v_mul_f32_e32 v15, 0x3d372713, v32
	v_mul_f32_e32 v15, v15, v32
	v_fma_f32 v15, v15, v32, v32
	v_mul_f32_e32 v15, 0xbfcc422a, v15
	v_mul_f32_e32 v15, 0x3fb8aa3b, v15
	v_exp_f32_e32 v15, v15
	v_exp_f32_e32 v10, v10
	v_and_b32_e32 v53, 0xffff0000, v11
	v_lshlrev_b32_e32 v48, 16, v11
	v_add_f32_e32 v15, 1.0, v15
	v_rcp_f32_e32 v33, v15
	v_mul_f32_e32 v15, 0x3d372713, v42
	v_mul_f32_e32 v15, v15, v42
	v_fma_f32 v15, v15, v42, v42
	v_mul_f32_e32 v15, 0xbfcc422a, v15
	v_mul_f32_e32 v15, 0x3fb8aa3b, v15
	v_exp_f32_e32 v15, v15
	v_add_f32_e32 v10, 1.0, v10
	v_rcp_f32_e32 v47, v10
	v_mul_f32_e32 v11, 0x3d372713, v53
	v_add_f32_e32 v15, 1.0, v15
	v_rcp_f32_e32 v43, v15
	v_mul_f32_e32 v10, v47, v46
	v_mul_f32_e32 v11, v11, v53
	v_fma_f32 v11, v11, v53, v53
	v_mul_f32_e32 v15, v43, v42
	v_fmac_f32_e32 v15, v33, v32
	v_add_f32_e32 v14, v15, v14
	v_mul_f32_e32 v15, 0x3d372713, v44
	v_mul_f32_e32 v15, v15, v44
	v_fma_f32 v15, v15, v44, v44
	v_mul_f32_e32 v15, 0xbfcc422a, v15
	v_mul_f32_e32 v15, 0x3fb8aa3b, v15
	v_exp_f32_e32 v15, v15
	v_mul_f32_e32 v11, 0xbfcc422a, v11
	v_mul_f32_e32 v11, 0x3fb8aa3b, v11
	v_exp_f32_e32 v11, v11
	v_add_f32_e32 v15, 1.0, v15
	v_rcp_f32_e32 v45, v15
	v_lshlrev_b32_e32 v55, 16, v12
	v_add_f32_e32 v11, 1.0, v11
	v_rcp_f32_e32 v54, v11
	v_fmac_f32_e32 v10, v45, v44
	v_add_f32_e32 v10, v10, v14
	v_mul_f32_e32 v14, 0x3d372713, v48
	v_mul_f32_e32 v14, v14, v48
	v_fma_f32 v14, v14, v48, v48
	v_mul_f32_e32 v14, 0xbfcc422a, v14
	v_mul_f32_e32 v14, 0x3fb8aa3b, v14
	v_exp_f32_e32 v14, v14
	v_mul_f32_e32 v11, v54, v53
	v_and_b32_e32 v57, 0xffff0000, v12
	v_lshlrev_b32_e32 v59, 16, v13
	v_add_f32_e32 v14, 1.0, v14
	v_rcp_f32_e32 v49, v14
	v_and_b32_e32 v61, 0xffff0000, v13
	v_lshlrev_b32_e32 v63, 16, v6
	v_mul_f32_e32 v6, 0x3d372713, v65
	v_fmac_f32_e32 v11, v49, v48
	v_add_f32_e32 v10, v11, v10
	v_mul_f32_e32 v11, 0x3d372713, v55
; __device__ __forceinline__ float bflo(unsigned w) { return __uint_as_float(w << 16); }
; __device__ __forceinline__ float bfhi(unsigned w) { return __uint_as_float(w & 0xffff0000u); }
; __device__ __forceinline__ float geluf_(float x) { const float t = 1.5957691216f * (x + 0.044715f * x * x * x); return x * __builtin_amdgcn_rcpf(1.f + __expf(-t)); }
; __device__ __forceinline__ void gmlp_unit(LAS unsigned char* L, int u, const bf16* z, const bf16* wsb, const float* bs, const float* lng, const float* lnb, bf16* mix, int tid_) {
;     ...
;     { const int j = tid >> 2, part = tid & 3; const bf16* src = z + (size_t)(t0 + j) * 2048 + 256 + part * 64; float x[64]; float s1 = 0.f;
; #pragma unroll
;       for (int q = 0; q < 8; ++q) { const v4u w4 = *(const v4u*)(src + 8 * q); const unsigned ww[4] = {w4.x, w4.y, w4.z, w4.w};
; #pragma unroll
;           for (int i = 0; i < 4; ++i) { x[q * 8 + 2 * i] = geluf_(bflo(ww[i])); x[q * 8 + 2 * i + 1] = geluf_(bfhi(ww[i])); s1 += x[q * 8 + 2 * i] + x[q * 8 + 2 * i + 1]; } }
	v_mul_f32_e32 v11, v11, v55
	v_fma_f32 v11, v11, v55, v55
	v_mul_f32_e32 v11, 0xbfcc422a, v11
	v_mul_f32_e32 v11, 0x3fb8aa3b, v11
	v_exp_f32_e32 v11, v11
	v_mul_f32_e32 v6, v6, v65
	v_fma_f32 v6, v6, v65, v65
	v_mul_f32_e32 v6, 0xbfcc422a, v6
	v_add_f32_e32 v11, 1.0, v11
	v_rcp_f32_e32 v56, v11
	v_mul_f32_e32 v11, 0x3d372713, v57
	v_mul_f32_e32 v11, v11, v57
	v_fma_f32 v11, v11, v57, v57
	v_mul_f32_e32 v11, 0xbfcc422a, v11
	v_mul_f32_e32 v11, 0x3fb8aa3b, v11
	v_exp_f32_e32 v11, v11
	v_mul_f32_e32 v6, 0x3fb8aa3b, v6
	v_exp_f32_e32 v6, v6
	v_and_b32_e32 v69, 0xffff0000, v7
	v_add_f32_e32 v11, 1.0, v11
	v_rcp_f32_e32 v58, v11
	v_add_f32_e32 v6, 1.0, v6
	v_rcp_f32_e32 v66, v6
	v_lshlrev_b32_e32 v67, 16, v7
	v_mul_f32_e32 v11, v58, v57
	v_fmac_f32_e32 v11, v56, v55
	v_add_f32_e32 v10, v11, v10
	v_mul_f32_e32 v11, 0x3d372713, v59
	v_mul_f32_e32 v11, v11, v59
	v_fma_f32 v11, v11, v59, v59
	v_mul_f32_e32 v11, 0xbfcc422a, v11
	v_mul_f32_e32 v11, 0x3fb8aa3b, v11
	v_exp_f32_e32 v11, v11
	v_mul_f32_e32 v6, v66, v65
	v_mul_f32_e32 v7, 0x3d372713, v69
	v_mul_f32_e32 v7, v7, v69
	v_add_f32_e32 v11, 1.0, v11
	v_rcp_f32_e32 v60, v11
	v_mul_f32_e32 v11, 0x3d372713, v61
	v_mul_f32_e32 v11, v11, v61
	v_fma_f32 v11, v11, v61, v61
	v_mul_f32_e32 v11, 0xbfcc422a, v11
	v_mul_f32_e32 v11, 0x3fb8aa3b, v11
	v_exp_f32_e32 v11, v11
	v_fma_f32 v7, v7, v69, v69
	v_mul_f32_e32 v7, 0xbfcc422a, v7
	v_mul_f32_e32 v7, 0x3fb8aa3b, v7
	v_add_f32_e32 v11, 1.0, v11
	v_rcp_f32_e32 v62, v11
	v_exp_f32_e32 v7, v7
	v_lshlrev_b32_e32 v71, 16, v8
	v_and_b32_e32 v73, 0xffff0000, v8
	v_mul_f32_e32 v11, v62, v61
	v_fmac_f32_e32 v11, v60, v59
	v_add_f32_e32 v10, v11, v10
	v_mul_f32_e32 v11, 0x3d372713, v63
	v_mul_f32_e32 v11, v11, v63
	v_fma_f32 v11, v11, v63, v63
	v_mul_f32_e32 v11, 0xbfcc422a, v11
	v_mul_f32_e32 v11, 0x3fb8aa3b, v11
	v_exp_f32_e32 v11, v11
	v_add_f32_e32 v7, 1.0, v7
	v_rcp_f32_e32 v70, v7
	v_lshlrev_b32_e32 v75, 16, v9
	v_add_f32_e32 v11, 1.0, v11
	v_rcp_f32_e32 v64, v11
	v_mul_f32_e32 v7, v70, v69
	v_and_b32_e32 v77, 0xffff0000, v9
	v_lshlrev_b32_e32 v79, 16, v2
	v_fmac_f32_e32 v6, v64, v63
	v_add_f32_e32 v6, v6, v10
	v_mul_f32_e32 v10, 0x3d372713, v67
	v_mul_f32_e32 v10, v10, v67
	v_fma_f32 v10, v10, v67, v67
	v_mul_f32_e32 v10, 0xbfcc422a, v10
	v_mul_f32_e32 v10, 0x3fb8aa3b, v10
	v_exp_f32_e32 v10, v10
	v_mul_f32_e32 v2, 0x3d372713, v81
	v_mul_f32_e32 v2, v2, v81
	v_fma_f32 v2, v2, v81, v81
	v_add_f32_e32 v10, 1.0, v10
	v_rcp_f32_e32 v68, v10
	v_mul_f32_e32 v2, 0xbfcc422a, v2
	v_mul_f32_e32 v2, 0x3fb8aa3b, v2
	v_exp_f32_e32 v2, v2
	v_fmac_f32_e32 v7, v68, v67
	v_add_f32_e32 v6, v7, v6
	v_mul_f32_e32 v7, 0x3d372713, v71
	v_mul_f32_e32 v7, v7, v71
	v_fma_f32 v7, v7, v71, v71
	v_mul_f32_e32 v7, 0xbfcc422a, v7
	v_mul_f32_e32 v7, 0x3fb8aa3b, v7
	v_exp_f32_e32 v7, v7
	v_add_f32_e32 v2, 1.0, v2
	v_rcp_f32_e32 v82, v2
	v_and_b32_e32 v84, 0xffff0000, v3
	v_add_f32_e32 v7, 1.0, v7
	v_rcp_f32_e32 v72, v7
	v_mul_f32_e32 v7, 0x3d372713, v73
	v_mul_f32_e32 v7, v7, v73
	v_fma_f32 v7, v7, v73, v73
	v_mul_f32_e32 v7, 0xbfcc422a, v7
	v_mul_f32_e32 v7, 0x3fb8aa3b, v7
	v_exp_f32_e32 v7, v7
	v_mul_f32_e32 v2, v82, v81
	v_lshlrev_b32_e32 v83, 16, v3
	v_mul_f32_e32 v3, 0x3d372713, v84
	v_add_f32_e32 v7, 1.0, v7
	v_rcp_f32_e32 v74, v7
	v_mul_f32_e32 v3, v3, v84
	v_fma_f32 v3, v3, v84, v84
	v_mul_f32_e32 v3, 0xbfcc422a, v3
	v_mul_f32_e32 v7, v74, v73
	v_fmac_f32_e32 v7, v72, v71
	v_add_f32_e32 v6, v7, v6
	v_mul_f32_e32 v7, 0x3d372713, v75
	v_mul_f32_e32 v7, v7, v75
	v_fma_f32 v7, v7, v75, v75
	v_mul_f32_e32 v7, 0xbfcc422a, v7
	v_mul_f32_e32 v7, 0x3fb8aa3b, v7
	v_exp_f32_e32 v7, v7
	v_mul_f32_e32 v3, 0x3fb8aa3b, v3
	v_exp_f32_e32 v3, v3
	v_lshlrev_b32_e32 v87, 16, v4
	v_add_f32_e32 v7, 1.0, v7
	v_rcp_f32_e32 v76, v7
	v_mul_f32_e32 v7, 0x3d372713, v77
	v_mul_f32_e32 v7, v7, v77
	v_fma_f32 v7, v7, v77, v77
	v_mul_f32_e32 v7, 0xbfcc422a, v7
	v_mul_f32_e32 v7, 0x3fb8aa3b, v7
	v_exp_f32_e32 v7, v7
	v_add_f32_e32 v3, 1.0, v3
	v_rcp_f32_e32 v86, v3
	v_and_b32_e32 v88, 0xffff0000, v4
	v_add_f32_e32 v7, 1.0, v7
	v_rcp_f32_e32 v78, v7
	v_mul_f32_e32 v3, v86, v84
	v_lshlrev_b32_e32 v91, 16, v5
	v_and_b32_e32 v92, 0xffff0000, v5
	v_mul_f32_e32 v7, v78, v77
	v_fmac_f32_e32 v7, v76, v75
	v_add_f32_e32 v6, v7, v6
	v_mul_f32_e32 v7, 0x3d372713, v79
	v_mul_f32_e32 v7, v7, v79
	v_fma_f32 v7, v7, v79, v79
	v_mul_f32_e32 v7, 0xbfcc422a, v7
	v_mul_f32_e32 v7, 0x3fb8aa3b, v7
	v_exp_f32_e32 v7, v7
	s_nop 0
	v_add_f32_e32 v7, 1.0, v7
	v_rcp_f32_e32 v80, v7
	s_nop 0
	v_fmac_f32_e32 v2, v80, v79
	v_add_f32_e32 v2, v2, v6
	v_mul_f32_e32 v6, 0x3d372713, v83
	v_mul_f32_e32 v6, v6, v83
	v_fma_f32 v6, v6, v83, v83
	v_mul_f32_e32 v6, 0xbfcc422a, v6
	v_mul_f32_e32 v6, 0x3fb8aa3b, v6
	v_exp_f32_e32 v6, v6
	s_nop 0
	v_add_f32_e32 v6, 1.0, v6
	v_rcp_f32_e32 v85, v6
	s_nop 0
	v_fmac_f32_e32 v3, v85, v83
	v_add_f32_e32 v2, v3, v2
	v_mul_f32_e32 v3, 0x3d372713, v87
	v_mul_f32_e32 v3, v3, v87
	v_fma_f32 v3, v3, v87, v87
	v_mul_f32_e32 v3, 0xbfcc422a, v3
	v_mul_f32_e32 v3, 0x3fb8aa3b, v3
	v_exp_f32_e32 v3, v3
	s_nop 0
	v_add_f32_e32 v3, 1.0, v3
	v_rcp_f32_e32 v89, v3
	v_mul_f32_e32 v3, 0x3d372713, v88
	v_mul_f32_e32 v3, v3, v88
	v_fma_f32 v3, v3, v88, v88
	v_mul_f32_e32 v3, 0xbfcc422a, v3
	v_mul_f32_e32 v3, 0x3fb8aa3b, v3
	v_exp_f32_e32 v3, v3
	s_nop 0
	v_add_f32_e32 v3, 1.0, v3
	v_rcp_f32_e32 v90, v3
	s_nop 0
	v_mul_f32_e32 v3, v90, v88
	v_fmac_f32_e32 v3, v89, v87
	v_add_f32_e32 v2, v3, v2
	v_mul_f32_e32 v3, 0x3d372713, v91
	v_mul_f32_e32 v3, v3, v91
	v_fma_f32 v3, v3, v91, v91
	v_mul_f32_e32 v3, 0xbfcc422a, v3
	v_mul_f32_e32 v3, 0x3fb8aa3b, v3
	v_exp_f32_e32 v3, v3
	s_nop 0
	v_add_f32_e32 v3, 1.0, v3
	v_rcp_f32_e32 v93, v3
	v_mul_f32_e32 v3, 0x3d372713, v92
	v_mul_f32_e32 v3, v3, v92
	v_fma_f32 v3, v3, v92, v92
	v_mul_f32_e32 v3, 0xbfcc422a, v3
	v_mul_f32_e32 v3, 0x3fb8aa3b, v3
	v_exp_f32_e32 v3, v3
	s_nop 0
	v_add_f32_e32 v3, 1.0, v3
	v_rcp_f32_e32 v94, v3
	s_nop 0
	v_mul_f32_e32 v3, v94, v92
	v_fmac_f32_e32 v3, v93, v91
	v_add_f32_e32 v34, v3, v2
	global_load_dwordx4 v[2:5], v[18:19], off offset:624
	global_load_dwordx4 v[6:9], v[18:19], off offset:608
	global_load_dwordx4 v[10:13], v[18:19], off offset:592
	global_load_dwordx4 v[14:17], v[18:19], off offset:576
	s_waitcnt vmcnt(1)
; __device__ __forceinline__ float bflo(unsigned w) { return __uint_as_float(w << 16); }
; __device__ __forceinline__ float bfhi(unsigned w) { return __uint_as_float(w & 0xffff0000u); }
; __device__ __forceinline__ float geluf_(float x) { const float t = 1.5957691216f * (x + 0.044715f * x * x * x); return x * __builtin_amdgcn_rcpf(1.f + __expf(-t)); }
; __device__ __forceinline__ void gmlp_unit(LAS unsigned char* L, int u, const bf16* z, const bf16* wsb, const float* bs, const float* lng, const float* lnb, bf16* mix, int tid_) {
;     ...
;     { const int j = tid >> 2, part = tid & 3; const bf16* src = z + (size_t)(t0 + j) * 2048 + 256 + part * 64; float x[64]; float s1 = 0.f;
; #pragma unroll
;       for (int q = 0; q < 8; ++q) { const v4u w4 = *(const v4u*)(src + 8 * q); const unsigned ww[4] = {w4.x, w4.y, w4.z, w4.w};
; #pragma unroll
;           for (int i = 0; i < 4; ++i) { x[q * 8 + 2 * i] = geluf_(bflo(ww[i])); x[q * 8 + 2 * i + 1] = geluf_(bfhi(ww[i])); s1 += x[q * 8 + 2 * i] + x[q * 8 + 2 * i + 1]; } }
	v_and_b32_e32 v119, 0xffff0000, v10
	s_waitcnt vmcnt(0)
	v_and_b32_e32 v103, 0xffff0000, v14
	v_lshlrev_b32_e32 v18, 16, v14
	v_mul_f32_e32 v14, 0x3d372713, v103
	v_mul_f32_e32 v19, 0x3d372713, v18
	v_mul_f32_e32 v14, v14, v103
	v_mul_f32_e32 v19, v19, v18
	v_fma_f32 v14, v14, v103, v103
	v_fma_f32 v19, v19, v18, v18
	v_mul_f32_e32 v14, 0xbfcc422a, v14
	v_mul_f32_e32 v19, 0xbfcc422a, v19
	v_mul_f32_e32 v14, 0x3fb8aa3b, v14
	v_mul_f32_e32 v19, 0x3fb8aa3b, v19
	v_exp_f32_e32 v14, v14
	v_exp_f32_e32 v19, v19
	v_and_b32_e32 v107, 0xffff0000, v15
	v_lshlrev_b32_e32 v105, 16, v15
	v_add_f32_e32 v14, 1.0, v14
	v_add_f32_e32 v19, 1.0, v19
	v_rcp_f32_e32 v104, v14
	v_rcp_f32_e32 v19, v19
	v_mul_f32_e32 v15, 0x3d372713, v107
	v_mul_f32_e32 v15, v15, v107
	v_mul_f32_e32 v14, v104, v103
	v_fmac_f32_e32 v14, v19, v18
	v_add_f32_e32 v14, v14, v34
	v_mul_f32_e32 v34, 0x3d372713, v105
	v_mul_f32_e32 v34, v34, v105
	v_fma_f32 v15, v15, v107, v107
	v_fma_f32 v34, v34, v105, v105
	v_mul_f32_e32 v15, 0xbfcc422a, v15
	v_mul_f32_e32 v34, 0xbfcc422a, v34
	v_mul_f32_e32 v15, 0x3fb8aa3b, v15
	v_mul_f32_e32 v34, 0x3fb8aa3b, v34
	v_exp_f32_e32 v15, v15
	v_exp_f32_e32 v34, v34
	v_lshlrev_b32_e32 v109, 16, v16
	v_and_b32_e32 v111, 0xffff0000, v16
	v_add_f32_e32 v15, 1.0, v15
	v_add_f32_e32 v34, 1.0, v34
	v_rcp_f32_e32 v108, v15
	v_rcp_f32_e32 v106, v34
	v_lshlrev_b32_e32 v113, 16, v17
	v_and_b32_e32 v115, 0xffff0000, v17
	v_mul_f32_e32 v15, v108, v107
	v_fmac_f32_e32 v15, v106, v105
	v_add_f32_e32 v14, v15, v14
	v_mul_f32_e32 v15, 0x3d372713, v109
	v_mul_f32_e32 v15, v15, v109
	v_fma_f32 v15, v15, v109, v109
	v_mul_f32_e32 v15, 0xbfcc422a, v15
	v_mul_f32_e32 v15, 0x3fb8aa3b, v15
	v_exp_f32_e32 v15, v15
	v_lshlrev_b32_e32 v117, 16, v10
	v_mul_f32_e32 v10, 0x3d372713, v119
	v_mul_f32_e32 v10, v10, v119
	v_add_f32_e32 v15, 1.0, v15
	v_rcp_f32_e32 v110, v15
	v_mul_f32_e32 v15, 0x3d372713, v111
	v_mul_f32_e32 v15, v15, v111
	v_fma_f32 v15, v15, v111, v111
	v_mul_f32_e32 v15, 0xbfcc422a, v15
	v_mul_f32_e32 v15, 0x3fb8aa3b, v15
	v_exp_f32_e32 v15, v15
	v_fma_f32 v10, v10, v119, v119
	v_mul_f32_e32 v10, 0xbfcc422a, v10
	v_mul_f32_e32 v10, 0x3fb8aa3b, v10
	v_add_f32_e32 v15, 1.0, v15
	v_rcp_f32_e32 v112, v15
	v_exp_f32_e32 v10, v10
	v_and_b32_e32 v123, 0xffff0000, v11
	v_lshlrev_b32_e32 v121, 16, v11
	v_mul_f32_e32 v15, v112, v111
	v_fmac_f32_e32 v15, v110, v109
	v_add_f32_e32 v14, v15, v14
	v_mul_f32_e32 v15, 0x3d372713, v113
	v_mul_f32_e32 v15, v15, v113
	v_fma_f32 v15, v15, v113, v113
	v_mul_f32_e32 v15, 0xbfcc422a, v15
	v_mul_f32_e32 v15, 0x3fb8aa3b, v15
	v_exp_f32_e32 v15, v15
	v_add_f32_e32 v10, 1.0, v10
	v_rcp_f32_e32 v120, v10
	v_mul_f32_e32 v11, 0x3d372713, v123
	v_add_f32_e32 v15, 1.0, v15
	v_rcp_f32_e32 v114, v15
	v_mul_f32_e32 v15, 0x3d372713, v115
	v_mul_f32_e32 v15, v15, v115
	v_fma_f32 v15, v15, v115, v115
	v_mul_f32_e32 v15, 0xbfcc422a, v15
	v_mul_f32_e32 v15, 0x3fb8aa3b, v15
	v_exp_f32_e32 v15, v15
	v_mul_f32_e32 v10, v120, v119
	v_mul_f32_e32 v11, v11, v123
	v_fma_f32 v11, v11, v123, v123
	v_add_f32_e32 v15, 1.0, v15
	v_rcp_f32_e32 v116, v15
	v_mul_f32_e32 v11, 0xbfcc422a, v11
	v_mul_f32_e32 v11, 0x3fb8aa3b, v11
	v_exp_f32_e32 v11, v11
	v_mul_f32_e32 v15, v116, v115
	v_fmac_f32_e32 v15, v114, v113
	v_add_f32_e32 v14, v15, v14
	v_mul_f32_e32 v15, 0x3d372713, v117
	v_mul_f32_e32 v15, v15, v117
	v_fma_f32 v15, v15, v117, v117
	v_mul_f32_e32 v15, 0xbfcc422a, v15
	v_mul_f32_e32 v15, 0x3fb8aa3b, v15
	v_exp_f32_e32 v15, v15
	v_add_f32_e32 v11, 1.0, v11
	v_rcp_f32_e32 v124, v11
	v_lshlrev_b32_e32 v125, 16, v12
	v_add_f32_e32 v15, 1.0, v15
	v_rcp_f32_e32 v118, v15
	v_mul_f32_e32 v11, v124, v123
	v_and_b32_e32 v139, 0xffff0000, v12
	v_lshlrev_b32_e32 v145, 16, v13
	v_fmac_f32_e32 v10, v118, v117
	v_add_f32_e32 v10, v10, v14
	v_mul_f32_e32 v14, 0x3d372713, v121
	v_mul_f32_e32 v14, v14, v121
	v_fma_f32 v14, v14, v121, v121
	v_mul_f32_e32 v14, 0xbfcc422a, v14
	v_mul_f32_e32 v14, 0x3fb8aa3b, v14
	v_exp_f32_e32 v14, v14
	v_and_b32_e32 v147, 0xffff0000, v13
	v_add_f32_e32 v14, 1.0, v14
	v_rcp_f32_e32 v122, v14
	s_nop 0
	v_fmac_f32_e32 v11, v122, v121
	v_add_f32_e32 v10, v11, v10
	v_mul_f32_e32 v11, 0x3d372713, v125
	v_mul_f32_e32 v11, v11, v125
	v_fma_f32 v11, v11, v125, v125
	v_mul_f32_e32 v11, 0xbfcc422a, v11
	v_mul_f32_e32 v11, 0x3fb8aa3b, v11
	v_exp_f32_e32 v11, v11
	s_nop 0
	v_add_f32_e32 v11, 1.0, v11
	v_rcp_f32_e32 v128, v11
	v_mul_f32_e32 v11, 0x3d372713, v139
	v_mul_f32_e32 v11, v11, v139
	v_fma_f32 v11, v11, v139, v139
	v_mul_f32_e32 v11, 0xbfcc422a, v11
	v_mul_f32_e32 v11, 0x3fb8aa3b, v11
	v_exp_f32_e32 v11, v11
	s_nop 0
	v_add_f32_e32 v11, 1.0, v11
	v_rcp_f32_e32 v144, v11
	s_nop 0
	v_mul_f32_e32 v11, v144, v139
	v_fmac_f32_e32 v11, v128, v125
	v_add_f32_e32 v10, v11, v10
	v_mul_f32_e32 v11, 0x3d372713, v145
	v_mul_f32_e32 v11, v11, v145
	v_fma_f32 v11, v11, v145, v145
	v_mul_f32_e32 v11, 0xbfcc422a, v11
	v_mul_f32_e32 v11, 0x3fb8aa3b, v11
	v_exp_f32_e32 v11, v11
	s_nop 0
	v_add_f32_e32 v11, 1.0, v11
	v_rcp_f32_e32 v146, v11
	v_mul_f32_e32 v11, 0x3d372713, v147
	v_mul_f32_e32 v11, v11, v147
	v_fma_f32 v11, v11, v147, v147
	v_mul_f32_e32 v11, 0xbfcc422a, v11
	v_mul_f32_e32 v11, 0x3fb8aa3b, v11
	v_exp_f32_e32 v11, v11
	s_nop 0
	v_add_f32_e32 v11, 1.0, v11
	v_rcp_f32_e32 v148, v11
	s_nop 0
	v_mul_f32_e32 v11, v148, v147
	v_fmac_f32_e32 v11, v146, v145
	v_add_f32_e32 v16, v11, v10
	v_lshlrev_b32_e32 v10, 16, v6
	v_mul_f32_e32 v12, 0x3d372713, v10
	v_mul_f32_e32 v12, v12, v10
	v_mov_b32_e32 v13, v10
	v_fmac_f32_e32 v13, v12, v13
	v_and_b32_e32 v6, 0xffff0000, v6
	v_mul_f32_e32 v12, 0xbfcc422a, v13
	v_mul_f32_e32 v13, 0x3d372713, v6
	v_mul_f32_e32 v13, v13, v6
; __device__ __forceinline__ float bflo(unsigned w) { return __uint_as_float(w << 16); }
; __device__ __forceinline__ float bfhi(unsigned w) { return __uint_as_float(w & 0xffff0000u); }
; __device__ __forceinline__ float geluf_(float x) { const float t = 1.5957691216f * (x + 0.044715f * x * x * x); return x * __builtin_amdgcn_rcpf(1.f + __expf(-t)); }
; #define SHX(v, m) (((m) < 32) ? __int_as_float(__builtin_amdgcn_ds_swizzle(__float_as_int(v), ((((m) & 31) << 10) | 0x1f))) : shx32(v))
; __device__ __forceinline__ void gmlp_unit(LAS unsigned char* L, int u, const bf16* z, const bf16* wsb, const float* bs, const float* lng, const float* lnb, bf16* mix, int tid_) {
;     ...
;     { const int j = tid >> 2, part = tid & 3; const bf16* src = z + (size_t)(t0 + j) * 2048 + 256 + part * 64; float x[64]; float s1 = 0.f;
; #pragma unroll
;       for (int q = 0; q < 8; ++q) { const v4u w4 = *(const v4u*)(src + 8 * q); const unsigned ww[4] = {w4.x, w4.y, w4.z, w4.w};
; #pragma unroll
;           for (int i = 0; i < 4; ++i) { x[q * 8 + 2 * i] = geluf_(bflo(ww[i])); x[q * 8 + 2 * i + 1] = geluf_(bfhi(ww[i])); s1 += x[q * 8 + 2 * i] + x[q * 8 + 2 * i + 1]; } }
;       s1 += SHX(s1, 1); s1 += SHX(s1, 2); const float mean = s1 * (1.f / 256.f); float s2 = 0.f;
	v_mov_b32_e32 v14, v6
	v_fmac_f32_e32 v14, v13, v14
	v_mul_f32_e32 v13, 0xbfcc422a, v14
	v_mul_f32_e32 v13, 0x3fb8aa3b, v13
	v_exp_f32_e32 v13, v13
	v_lshlrev_b32_e32 v11, 16, v7
	v_mov_b32_e32 v15, v11
	v_and_b32_e32 v7, 0xffff0000, v7
	v_add_f32_e32 v13, 1.0, v13
	v_rcp_f32_e32 v14, v13
	v_mul_f32_e32 v13, 0x3d372713, v11
	v_mul_f32_e32 v13, v13, v11
	v_fmac_f32_e32 v15, v13, v15
	v_mul_f32_e32 v13, 0xbfcc422a, v15
	v_mul_f32_e32 v15, 0x3d372713, v7
	v_mul_f32_e32 v15, v15, v7
	v_mov_b32_e32 v17, v7
	v_fmac_f32_e32 v17, v15, v17
	v_mul_f32_e32 v15, 0xbfcc422a, v17
	v_mul_f32_e32 v15, 0x3fb8aa3b, v15
	v_mul_f32_e32 v12, 0x3fb8aa3b, v12
	v_mul_f32_e32 v13, 0x3fb8aa3b, v13
	v_exp_f32_e32 v15, v15
	v_exp_f32_e32 v12, v12
	v_exp_f32_e32 v13, v13
	v_add_f32_e32 v15, 1.0, v15
	v_add_f32_e32 v12, 1.0, v12
	v_add_f32_e32 v13, 1.0, v13
	v_rcp_f32_e32 v15, v15
	v_rcp_f32_e32 v12, v12
	v_rcp_f32_e32 v13, v13
	v_pk_mul_f32 v[36:37], v[14:15], v[6:7]
	s_nop 0
	v_pk_fma_f32 v[6:7], v[12:13], v[10:11], v[36:37]
	s_nop 0
	v_add_f32_e32 v6, v6, v16
	v_add_f32_e32 v14, v7, v6
	v_lshlrev_b32_e32 v6, 16, v8
	v_pk_mul_f32 v[34:35], v[12:13], v[10:11]
	v_mul_f32_e32 v10, 0x3d372713, v6
	v_mul_f32_e32 v10, v10, v6
	v_mov_b32_e32 v11, v6
	v_fmac_f32_e32 v11, v10, v11
	v_and_b32_e32 v8, 0xffff0000, v8
	v_mul_f32_e32 v10, 0xbfcc422a, v11
	v_mul_f32_e32 v11, 0x3d372713, v8
	v_mul_f32_e32 v11, v11, v8
	v_mov_b32_e32 v12, v8
	v_fmac_f32_e32 v12, v11, v12
	v_mul_f32_e32 v11, 0xbfcc422a, v12
	v_mul_f32_e32 v11, 0x3fb8aa3b, v11
	v_exp_f32_e32 v11, v11
	v_lshlrev_b32_e32 v7, 16, v9
	v_mov_b32_e32 v13, v7
	v_and_b32_e32 v9, 0xffff0000, v9
	v_add_f32_e32 v11, 1.0, v11
	v_rcp_f32_e32 v12, v11
	v_mul_f32_e32 v11, 0x3d372713, v7
	v_mul_f32_e32 v11, v11, v7
	v_fmac_f32_e32 v13, v11, v13
	v_mul_f32_e32 v11, 0xbfcc422a, v13
	v_mul_f32_e32 v13, 0x3d372713, v9
	v_mul_f32_e32 v13, v13, v9
	v_mov_b32_e32 v15, v9
	v_fmac_f32_e32 v15, v13, v15
	v_mul_f32_e32 v13, 0xbfcc422a, v15
	v_mul_f32_e32 v13, 0x3fb8aa3b, v13
	v_mul_f32_e32 v10, 0x3fb8aa3b, v10
	v_mul_f32_e32 v11, 0x3fb8aa3b, v11
	v_exp_f32_e32 v13, v13
	v_exp_f32_e32 v10, v10
	v_exp_f32_e32 v11, v11
	v_add_f32_e32 v13, 1.0, v13
	v_add_f32_e32 v10, 1.0, v10
	v_add_f32_e32 v11, 1.0, v11
	v_rcp_f32_e32 v13, v13
	v_rcp_f32_e32 v10, v10
	v_rcp_f32_e32 v11, v11
	v_pk_mul_f32 v[40:41], v[12:13], v[8:9]
	v_pk_mul_f32 v[38:39], v[10:11], v[6:7]
	v_pk_fma_f32 v[6:7], v[10:11], v[6:7], v[40:41]
	v_lshlrev_b32_e32 v11, 16, v4
	v_add_f32_e32 v6, v6, v14
	v_add_f32_e32 v95, v7, v6
	v_lshlrev_b32_e32 v7, 16, v5
	v_and_b32_e32 v6, 0xffff0000, v5
	v_mul_f32_e32 v5, 0x3d372713, v7
	v_mul_f32_e32 v5, v5, v7
	v_mov_b32_e32 v8, v7
	v_fmac_f32_e32 v8, v5, v8
	v_mul_f32_e32 v5, 0xbfcc422a, v8
	v_mul_f32_e32 v5, 0x3fb8aa3b, v5
	v_exp_f32_e32 v5, v5
	v_mov_b32_e32 v8, v6
	v_and_b32_e32 v10, 0xffff0000, v4
	v_mul_f32_e32 v4, 0x3d372713, v11
	v_add_f32_e32 v5, 1.0, v5
	v_rcp_f32_e32 v9, v5
	v_mul_f32_e32 v5, 0x3d372713, v6
	v_mul_f32_e32 v5, v5, v6
	v_fmac_f32_e32 v8, v5, v8
	v_mul_f32_e32 v5, 0xbfcc422a, v8
	v_mul_f32_e32 v5, 0x3fb8aa3b, v5
	v_exp_f32_e32 v5, v5
	v_mul_f32_e32 v4, v4, v11
	v_mov_b32_e32 v14, v10
	v_add_f32_e32 v5, 1.0, v5
	v_rcp_f32_e32 v8, v5
	v_mov_b32_e32 v5, v11
	v_fmac_f32_e32 v5, v4, v5
	v_mul_f32_e32 v4, 0xbfcc422a, v5
	v_mul_f32_e32 v4, 0x3fb8aa3b, v4
	v_exp_f32_e32 v4, v4
	v_pk_mul_f32 v[12:13], v[8:9], v[6:7]
	v_add_f32_e32 v4, 1.0, v4
	v_rcp_f32_e32 v5, v4
	v_mul_f32_e32 v4, 0x3d372713, v10
	v_mul_f32_e32 v4, v4, v10
	v_fmac_f32_e32 v14, v4, v14
	v_mul_f32_e32 v4, 0xbfcc422a, v14
	v_mul_f32_e32 v4, 0x3fb8aa3b, v4
	v_exp_f32_e32 v4, v4
	v_mov_b32_e32 v16, v13
	v_add_f32_e32 v4, 1.0, v4
	v_rcp_f32_e32 v4, v4
	s_nop 0
	v_pk_mul_f32 v[14:15], v[4:5], v[10:11]
	s_nop 0
	v_mov_b32_e32 v17, v15
	v_mov_b32_e32 v13, v14
	v_pk_add_f32 v[96:97], v[16:17], v[12:13]
	v_lshlrev_b32_e32 v13, 16, v3
	v_and_b32_e32 v12, 0xffff0000, v3
	v_mul_f32_e32 v3, 0x3d372713, v13
	v_mul_f32_e32 v3, v3, v13
	v_mov_b32_e32 v14, v13
	v_fmac_f32_e32 v14, v3, v14
	v_mul_f32_e32 v3, 0xbfcc422a, v14
	v_mul_f32_e32 v3, 0x3fb8aa3b, v3
	v_exp_f32_e32 v3, v3
	v_mov_b32_e32 v14, v12
	v_lshlrev_b32_e32 v17, 16, v2
	v_and_b32_e32 v16, 0xffff0000, v2
	v_add_f32_e32 v3, 1.0, v3
	v_rcp_f32_e32 v15, v3
	v_mul_f32_e32 v3, 0x3d372713, v12
	v_mul_f32_e32 v3, v3, v12
	v_fmac_f32_e32 v14, v3, v14
	v_mul_f32_e32 v3, 0xbfcc422a, v14
	v_mul_f32_e32 v3, 0x3fb8aa3b, v3
	v_exp_f32_e32 v3, v3
	v_mul_f32_e32 v2, 0x3d372713, v17
	v_mul_f32_e32 v2, v2, v17
	v_mov_b32_e32 v100, v16
	v_add_f32_e32 v3, 1.0, v3
	v_rcp_f32_e32 v14, v3
	v_mov_b32_e32 v3, v17
	v_fmac_f32_e32 v3, v2, v3
	v_mul_f32_e32 v2, 0xbfcc422a, v3
	v_mul_f32_e32 v2, 0x3fb8aa3b, v2
	v_exp_f32_e32 v2, v2
	v_pk_mul_f32 v[98:99], v[14:15], v[12:13]
	v_add_f32_e32 v2, 1.0, v2
	v_rcp_f32_e32 v3, v2
	v_mul_f32_e32 v2, 0x3d372713, v16
	v_mul_f32_e32 v2, v2, v16
	v_fmac_f32_e32 v100, v2, v100
	v_mul_f32_e32 v2, 0xbfcc422a, v100
	v_mul_f32_e32 v2, 0x3fb8aa3b, v2
	v_exp_f32_e32 v2, v2
	v_mov_b32_e32 v126, v99
	v_add_f32_e32 v2, 1.0, v2
	v_rcp_f32_e32 v2, v2
	s_nop 0
	v_pk_mul_f32 v[100:101], v[2:3], v[16:17]
	s_nop 0
	v_mov_b32_e32 v127, v101
	v_mov_b32_e32 v99, v100
	v_pk_add_f32 v[98:99], v[126:127], v[98:99]
	s_nop 0
	v_add_f32_e32 v95, v99, v95
	v_add_f32_e32 v95, v98, v95
	v_add_f32_e32 v95, v97, v95
	v_add_f32_e32 v95, v96, v95
	s_waitcnt lgkmcnt(0)
	s_nop 1
	v_add_f32_dpp v95, v95, v95 quad_perm:[1,0,3,2] row_mask:0xf bank_mask:0xf
	ds_swizzle_b32 v96, v95 offset:swizzle(SWAP,2)
	s_waitcnt lgkmcnt(0)
; #define LAS __attribute__((address_space(3)))
; __device__ __forceinline__ unsigned f2bf(float f) { unsigned u = __float_as_uint(f); return (u + 0x7fffu + ((u >> 16) & 1u)) >> 16; }
; #define SHX(v, m) (((m) < 32) ? __int_as_float(__builtin_amdgcn_ds_swizzle(__float_as_int(v), ((((m) & 31) << 10) | 0x1f))) : shx32(v))
; __device__ __forceinline__ void gmlp_unit(LAS unsigned char* L, int u, const bf16* z, const bf16* wsb, const float* bs, const float* lng, const float* lnb, bf16* mix, int tid_) {
;     ...
;       s1 += SHX(s1, 1); s1 += SHX(s1, 2); const float mean = s1 * (1.f / 256.f); float s2 = 0.f;
; #pragma unroll
;       for (int i = 0; i < 64; ++i) { x[i] -= mean; s2 += x[i] * x[i]; }
;       s2 += SHX(s2, 1); s2 += SHX(s2, 2); const float rstd = rsqrtf(s2 * (1.f / 256.f) + EPS);
; #pragma unroll
;       for (int q = 0; q < 16; ++q) { const f32x4 gq = ((const f32x4*)(lng + part * 64))[q], bq = ((const f32x4*)(lnb + part * 64))[q];
; #pragma unroll
;           for (int e = 0; e < 4; ++e) { const int i = 4 * q + e, col = part * 64 + i; *(LAS bf16*)(L + col * 272 + j * 2) = (bf16)f2bf(x[i] * rstd * gq[e] + bq[e]); } } }
	v_add_f32_e32 v149, v95, v96
	v_mul_f32_e32 v150, 0x3b800000, v149
	v_fma_f32 v142, v23, v22, -v150
	v_fma_f32 v143, v21, v20, -v150
	v_mul_f32_e32 v20, v142, v142
	v_fmac_f32_e32 v20, v143, v143
	v_fma_f32 v141, v25, v24, -v150
	v_fmac_f32_e32 v20, v141, v141
	v_fma_f32 v140, v27, v26, -v150
	v_fmac_f32_e32 v20, v140, v140
	v_fma_f32 v138, v29, v28, -v150
	v_fmac_f32_e32 v20, v138, v138
	v_fma_f32 v137, v31, v30, -v150
	v_fmac_f32_e32 v20, v137, v137
	v_fma_f32 v136, v33, v32, -v150
	v_fmac_f32_e32 v20, v136, v136
	v_fma_f32 v135, v43, v42, -v150
	v_fmac_f32_e32 v20, v135, v135
	v_fma_f32 v134, v45, v44, -v150
	v_fmac_f32_e32 v20, v134, v134
	v_fma_f32 v133, v47, v46, -v150
	v_fmac_f32_e32 v20, v133, v133
	v_fma_f32 v132, v49, v48, -v150
	v_fmac_f32_e32 v20, v132, v132
	v_fma_f32 v131, v54, v53, -v150
	v_fmac_f32_e32 v20, v131, v131
	v_fma_f32 v130, v56, v55, -v150
	v_fmac_f32_e32 v20, v130, v130
	v_fma_f32 v129, v58, v57, -v150
	v_fmac_f32_e32 v20, v129, v129
	v_fma_f32 v127, v60, v59, -v150
	v_fmac_f32_e32 v20, v127, v127
	v_fma_f32 v126, v62, v61, -v150
	v_fmac_f32_e32 v20, v126, v126
	v_fma_f32 v102, v64, v63, -v150
	v_fmac_f32_e32 v20, v102, v102
	v_fma_f32 v101, v66, v65, -v150
	v_fmac_f32_e32 v20, v101, v101
	v_fma_f32 v100, v68, v67, -v150
	v_fmac_f32_e32 v20, v100, v100
	v_fma_f32 v99, v70, v69, -v150
	v_fmac_f32_e32 v20, v99, v99
	v_fma_f32 v98, v72, v71, -v150
	v_fmac_f32_e32 v20, v98, v98
	v_fma_f32 v97, v74, v73, -v150
	v_fmac_f32_e32 v20, v97, v97
	v_fma_f32 v96, v76, v75, -v150
	v_fmac_f32_e32 v20, v96, v96
	v_fma_f32 v95, v78, v77, -v150
	v_fmac_f32_e32 v20, v95, v95
	v_fma_f32 v79, v80, v79, -v150
	v_fmac_f32_e32 v20, v79, v79
	v_fma_f32 v78, v82, v81, -v150
	v_fmac_f32_e32 v20, v78, v78
	v_fma_f32 v77, v85, v83, -v150
	v_fmac_f32_e32 v20, v77, v77
	v_fma_f32 v76, v86, v84, -v150
	v_fmac_f32_e32 v20, v76, v76
	v_fma_f32 v75, v89, v87, -v150
	v_fmac_f32_e32 v20, v75, v75
	v_fma_f32 v74, v90, v88, -v150
	v_fmac_f32_e32 v20, v74, v74
	v_fma_f32 v73, v93, v91, -v150
	v_fmac_f32_e32 v20, v73, v73
	v_fma_f32 v72, v94, v92, -v150
	v_fmac_f32_e32 v20, v72, v72
	v_fma_f32 v71, v19, v18, -v150
	v_fmac_f32_e32 v20, v71, v71
	v_fma_f32 v70, v104, v103, -v150
	v_fmac_f32_e32 v20, v70, v70
	v_fma_f32 v69, v106, v105, -v150
	v_fmac_f32_e32 v20, v69, v69
	v_fma_f32 v68, v108, v107, -v150
	v_fmac_f32_e32 v20, v68, v68
	v_fma_f32 v67, v110, v109, -v150
	v_fmac_f32_e32 v20, v67, v67
	v_fma_f32 v66, v112, v111, -v150
	v_fmac_f32_e32 v20, v66, v66
	v_fma_f32 v65, v114, v113, -v150
	v_fmac_f32_e32 v20, v65, v65
	v_fma_f32 v64, v116, v115, -v150
	v_fmac_f32_e32 v20, v64, v64
	v_fma_f32 v63, v118, v117, -v150
	v_fmac_f32_e32 v20, v63, v63
	v_fma_f32 v62, v120, v119, -v150
	v_fmac_f32_e32 v20, v62, v62
	v_fma_f32 v61, v122, v121, -v150
	v_fmac_f32_e32 v20, v61, v61
	v_fma_f32 v60, v124, v123, -v150
	v_fmac_f32_e32 v20, v60, v60
	v_fma_f32 v59, v128, v125, -v150
	v_fmac_f32_e32 v20, v59, v59
	v_fma_f32 v58, v144, v139, -v150
	v_fmac_f32_e32 v20, v58, v58
	v_fma_f32 v57, v146, v145, -v150
	v_fmac_f32_e32 v20, v57, v57
	v_fma_f32 v56, v148, v147, -v150
	v_fmac_f32_e32 v20, v56, v56
	v_fmamk_f32 v54, v149, 0xbb800000, v34
	v_fmac_f32_e32 v20, v54, v54
	v_fmamk_f32 v53, v149, 0xbb800000, v36
	v_fmac_f32_e32 v20, v53, v53
	v_fmac_f32_e32 v35, 0xbb800000, v149
	v_fmac_f32_e32 v20, v35, v35
	v_fmac_f32_e32 v37, 0xbb800000, v149
	v_fmac_f32_e32 v20, v37, v37
	v_fmamk_f32 v38, v149, 0xbb800000, v38
	v_fmac_f32_e32 v20, v38, v38
	v_fmamk_f32 v36, v149, 0xbb800000, v40
	v_fmac_f32_e32 v20, v36, v36
	v_fmac_f32_e32 v39, 0xbb800000, v149
	v_fmac_f32_e32 v20, v39, v39
	v_fmac_f32_e32 v41, 0xbb800000, v149
	v_pk_fma_f32 v[48:49], v[2:3], v[16:17], v[150:151] op_sel_hi:[1,1,0] neg_lo:[0,0,1] neg_hi:[0,0,1]
	v_fmac_f32_e32 v20, v41, v41
	v_pk_mul_f32 v[2:3], v[48:49], v[48:49]
	v_pk_fma_f32 v[46:47], v[14:15], v[12:13], v[150:151] op_sel_hi:[1,1,0] neg_lo:[0,0,1] neg_hi:[0,0,1]
	v_add_f32_e32 v3, v3, v20
	v_add_f32_e32 v16, v2, v3
	v_pk_mul_f32 v[2:3], v[46:47], v[46:47]
	v_pk_fma_f32 v[44:45], v[4:5], v[10:11], v[150:151] op_sel_hi:[1,1,0] neg_lo:[0,0,1] neg_hi:[0,0,1]
	v_add_f32_e32 v3, v3, v16
	v_add_f32_e32 v12, v2, v3
	v_pk_mul_f32 v[2:3], v[44:45], v[44:45]
	v_pk_fma_f32 v[42:43], v[8:9], v[6:7], v[150:151] op_sel_hi:[1,1,0] neg_lo:[0,0,1] neg_hi:[0,0,1]
	v_add_f32_e32 v3, v3, v12
	v_add_f32_e32 v4, v2, v3
	v_pk_mul_f32 v[2:3], v[42:43], v[42:43]
	v_lshlrev_b32_e32 v55, 2, v51
	v_add_f32_e32 v3, v3, v4
	v_add_f32_e32 v2, v2, v3
	v_lshlrev_b32_e32 v40, 1, v50
	s_waitcnt lgkmcnt(0)
	s_nop 1
	v_add_f32_dpp v2, v2, v2 quad_perm:[1,0,3,2] row_mask:0xf bank_mask:0xf
	s_waitcnt lgkmcnt(0)
	s_nop 1
	v_add_f32_dpp v2, v2, v2 quad_perm:[2,3,0,1] row_mask:0xf bank_mask:0xf
	v_fmamk_f32 v2, v2, 0x3b800000, v196
	v_cmp_gt_f32_e32 vcc, s73, v2
	v_mul_f32_e32 v3, 0x4b800000, v2
	s_nop 0
	v_cndmask_b32_e32 v2, v2, v3, vcc
	v_rsq_f32_e32 v2, v2
	s_nop 0
	v_mul_f32_e32 v3, 0x45800000, v2
	v_cndmask_b32_e32 v34, v2, v3, vcc
	global_load_dwordx4 v[2:5], v55, s[30:31] offset:48
	global_load_dwordx4 v[10:13], v55, s[30:31] offset:32
	global_load_dwordx4 v[18:21], v55, s[30:31] offset:16
	global_load_dwordx4 v[26:29], v55, s[30:31]
	global_load_dwordx4 v[6:9], v55, s[28:29] offset:48
	global_load_dwordx4 v[14:17], v55, s[28:29] offset:32
	global_load_dwordx4 v[22:25], v55, s[28:29] offset:16
	global_load_dwordx4 v[30:33], v55, s[28:29]
	v_mul_f32_e32 v80, v143, v34
	s_waitcnt vmcnt(0)
; #define LAS __attribute__((address_space(3)))
; __device__ __forceinline__ unsigned f2bf(float f) { unsigned u = __float_as_uint(f); return (u + 0x7fffu + ((u >> 16) & 1u)) >> 16; }
; __device__ __forceinline__ void gmlp_unit(LAS unsigned char* L, int u, const bf16* z, const bf16* wsb, const float* bs, const float* lng, const float* lnb, bf16* mix, int tid_) {
;     ...
; #pragma unroll
;       for (int q = 0; q < 16; ++q) { const f32x4 gq = ((const f32x4*)(lng + part * 64))[q], bq = ((const f32x4*)(lnb + part * 64))[q];
; #pragma unroll
;           for (int e = 0; e < 4; ++e) { const int i = 4 * q + e, col = part * 64 + i; *(LAS bf16*)(L + col * 272 + j * 2) = (bf16)f2bf(x[i] * rstd * gq[e] + bq[e]); } } }
	v_fma_f32 v26, v26, v80, v30
	v_bfe_u32 v30, v26, 16, 1
	v_add3_u32 v26, v26, v30, s78
	v_mul_u32_u24_e32 v30, 0x110, v51
	v_add3_u32 v40, 0, v40, v30
	ds_write_b16_d16_hi v40, v26
	v_mul_f32_e32 v26, v142, v34
	v_fma_f32 v26, v27, v26, v31
	v_bfe_u32 v27, v26, 16, 1
	v_add3_u32 v26, v26, v27, s78
	ds_write_b16_d16_hi v40, v26 offset:272
	v_mul_f32_e32 v26, v141, v34
	v_fma_f32 v26, v28, v26, v32
	v_bfe_u32 v27, v26, 16, 1
	v_add3_u32 v26, v26, v27, s78
	ds_write_b16_d16_hi v40, v26 offset:544
	v_mul_f32_e32 v26, v140, v34
	v_fmac_f32_e32 v33, v29, v26
	v_bfe_u32 v26, v33, 16, 1
	v_add3_u32 v26, v33, v26, s78
	ds_write_b16_d16_hi v40, v26 offset:816
	v_mul_f32_e32 v26, v138, v34
	v_fma_f32 v18, v18, v26, v22
	v_bfe_u32 v22, v18, 16, 1
	v_add3_u32 v18, v18, v22, s78
	ds_write_b16_d16_hi v40, v18 offset:1088
	v_mul_f32_e32 v18, v137, v34
	v_fma_f32 v18, v19, v18, v23
	v_bfe_u32 v19, v18, 16, 1
	v_add3_u32 v18, v18, v19, s78
	ds_write_b16_d16_hi v40, v18 offset:1360
	v_mul_f32_e32 v18, v136, v34
	v_fma_f32 v18, v20, v18, v24
	v_bfe_u32 v19, v18, 16, 1
	v_add3_u32 v18, v18, v19, s78
	ds_write_b16_d16_hi v40, v18 offset:1632
	v_mul_f32_e32 v18, v135, v34
	v_fmac_f32_e32 v25, v21, v18
	v_bfe_u32 v18, v25, 16, 1
	v_add3_u32 v18, v25, v18, s78
	ds_write_b16_d16_hi v40, v18 offset:1904
	v_mul_f32_e32 v18, v134, v34
	v_fma_f32 v10, v10, v18, v14
	v_bfe_u32 v14, v10, 16, 1
	v_add3_u32 v10, v10, v14, s78
	ds_write_b16_d16_hi v40, v10 offset:2176
	v_mul_f32_e32 v10, v133, v34
	v_fma_f32 v10, v11, v10, v15
	v_bfe_u32 v11, v10, 16, 1
	v_add3_u32 v10, v10, v11, s78
	ds_write_b16_d16_hi v40, v10 offset:2448
	v_mul_f32_e32 v10, v132, v34
	v_fma_f32 v10, v12, v10, v16
	v_bfe_u32 v11, v10, 16, 1
	v_add3_u32 v10, v10, v11, s78
	ds_write_b16_d16_hi v40, v10 offset:2720
	v_mul_f32_e32 v10, v131, v34
	v_fmac_f32_e32 v17, v13, v10
	v_bfe_u32 v10, v17, 16, 1
	v_add3_u32 v10, v17, v10, s78
	ds_write_b16_d16_hi v40, v10 offset:2992
	v_mul_f32_e32 v10, v130, v34
	v_fma_f32 v2, v2, v10, v6
	v_bfe_u32 v6, v2, 16, 1
	v_add3_u32 v2, v2, v6, s78
	ds_write_b16_d16_hi v40, v2 offset:3264
	v_mul_f32_e32 v2, v129, v34
	v_fma_f32 v2, v3, v2, v7
	v_bfe_u32 v3, v2, 16, 1
	v_add3_u32 v2, v2, v3, s78
	ds_write_b16_d16_hi v40, v2 offset:3536
	v_mul_f32_e32 v2, v127, v34
	v_fma_f32 v2, v4, v2, v8
	v_bfe_u32 v3, v2, 16, 1
	v_add3_u32 v2, v2, v3, s78
	ds_write_b16_d16_hi v40, v2 offset:3808
	v_mul_f32_e32 v2, v126, v34
	v_fmac_f32_e32 v9, v5, v2
	v_bfe_u32 v2, v9, 16, 1
	v_add3_u32 v2, v9, v2, s78
	ds_write_b16_d16_hi v40, v2 offset:4080
	global_load_dwordx4 v[2:5], v55, s[30:31] offset:112
	global_load_dwordx4 v[6:9], v55, s[30:31] offset:96
	global_load_dwordx4 v[10:13], v55, s[30:31] offset:80
	global_load_dwordx4 v[26:29], v55, s[30:31] offset:64
	global_load_dwordx4 v[14:17], v55, s[28:29] offset:112
	global_load_dwordx4 v[18:21], v55, s[28:29] offset:96
	global_load_dwordx4 v[22:25], v55, s[28:29] offset:80
	global_load_dwordx4 v[30:33], v55, s[28:29] offset:64
	v_mul_f32_e32 v51, v102, v34
	s_waitcnt vmcnt(0)
	v_fma_f32 v26, v26, v51, v30
	v_bfe_u32 v30, v26, 16, 1
	v_add3_u32 v26, v26, v30, s78
	ds_write_b16_d16_hi v40, v26 offset:4352
	v_mul_f32_e32 v26, v101, v34
	v_fma_f32 v26, v27, v26, v31
	v_bfe_u32 v27, v26, 16, 1
	v_add3_u32 v26, v26, v27, s78
	ds_write_b16_d16_hi v40, v26 offset:4624
	v_mul_f32_e32 v26, v100, v34
	v_fma_f32 v26, v28, v26, v32
	v_bfe_u32 v27, v26, 16, 1
	v_add3_u32 v26, v26, v27, s78
	ds_write_b16_d16_hi v40, v26 offset:4896
	v_mul_f32_e32 v26, v99, v34
	v_fmac_f32_e32 v33, v29, v26
	v_bfe_u32 v26, v33, 16, 1
	v_add3_u32 v26, v33, v26, s78
	ds_write_b16_d16_hi v40, v26 offset:5168
	v_mul_f32_e32 v26, v98, v34
	v_fma_f32 v10, v10, v26, v22
	v_bfe_u32 v22, v10, 16, 1
	v_add3_u32 v10, v10, v22, s78
	ds_write_b16_d16_hi v40, v10 offset:5440
	v_mul_f32_e32 v10, v97, v34
	v_fma_f32 v10, v11, v10, v23
	v_bfe_u32 v11, v10, 16, 1
	v_add3_u32 v10, v10, v11, s78
	ds_write_b16_d16_hi v40, v10 offset:5712
	v_mul_f32_e32 v10, v96, v34
	v_fma_f32 v10, v12, v10, v24
	v_bfe_u32 v11, v10, 16, 1
	v_add3_u32 v10, v10, v11, s78
	ds_write_b16_d16_hi v40, v10 offset:5984
	v_mul_f32_e32 v10, v95, v34
	v_fmac_f32_e32 v25, v13, v10
	v_bfe_u32 v10, v25, 16, 1
	v_add3_u32 v10, v25, v10, s78
	ds_write_b16_d16_hi v40, v10 offset:6256
	v_mul_f32_e32 v10, v79, v34
	v_fma_f32 v6, v6, v10, v18
	v_bfe_u32 v10, v6, 16, 1
	v_add3_u32 v6, v6, v10, s78
	ds_write_b16_d16_hi v40, v6 offset:6528
	v_mul_f32_e32 v6, v78, v34
	v_fma_f32 v6, v7, v6, v19
	v_bfe_u32 v7, v6, 16, 1
	v_add3_u32 v6, v6, v7, s78
	ds_write_b16_d16_hi v40, v6 offset:6800
	v_mul_f32_e32 v6, v77, v34
	v_fma_f32 v6, v8, v6, v20
	v_bfe_u32 v7, v6, 16, 1
	v_add3_u32 v6, v6, v7, s78
	ds_write_b16_d16_hi v40, v6 offset:7072
	v_mul_f32_e32 v6, v76, v34
	v_fmac_f32_e32 v21, v9, v6
	v_bfe_u32 v6, v21, 16, 1
	v_add3_u32 v6, v21, v6, s78
	ds_write_b16_d16_hi v40, v6 offset:7344
	v_mul_f32_e32 v6, v75, v34
	v_fma_f32 v2, v2, v6, v14
	v_bfe_u32 v6, v2, 16, 1
	v_add3_u32 v2, v2, v6, s78
	ds_write_b16_d16_hi v40, v2 offset:7616
	v_mul_f32_e32 v2, v74, v34
	v_fma_f32 v2, v3, v2, v15
	v_bfe_u32 v3, v2, 16, 1
	v_add3_u32 v2, v2, v3, s78
	ds_write_b16_d16_hi v40, v2 offset:7888
	v_mul_f32_e32 v2, v73, v34
	v_fma_f32 v2, v4, v2, v16
	v_bfe_u32 v3, v2, 16, 1
	v_add3_u32 v2, v2, v3, s78
	ds_write_b16_d16_hi v40, v2 offset:8160
	v_mul_f32_e32 v2, v72, v34
	v_fmac_f32_e32 v17, v5, v2
	v_bfe_u32 v2, v17, 16, 1
	v_add3_u32 v2, v17, v2, s78
	ds_write_b16_d16_hi v40, v2 offset:8432
	global_load_dwordx4 v[2:5], v55, s[30:31] offset:176
	global_load_dwordx4 v[6:9], v55, s[30:31] offset:160
	global_load_dwordx4 v[10:13], v55, s[30:31] offset:144
	global_load_dwordx4 v[26:29], v55, s[30:31] offset:128
	global_load_dwordx4 v[14:17], v55, s[28:29] offset:176
	global_load_dwordx4 v[18:21], v55, s[28:29] offset:160
	global_load_dwordx4 v[22:25], v55, s[28:29] offset:144
	global_load_dwordx4 v[30:33], v55, s[28:29] offset:128
	v_mul_f32_e32 v51, v71, v34
	s_waitcnt vmcnt(0)
; #define LAS __attribute__((address_space(3)))
; __device__ __forceinline__ unsigned f2bf(float f) { unsigned u = __float_as_uint(f); return (u + 0x7fffu + ((u >> 16) & 1u)) >> 16; }
; __device__ __forceinline__ void gmlp_unit(LAS unsigned char* L, int u, const bf16* z, const bf16* wsb, const float* bs, const float* lng, const float* lnb, bf16* mix, int tid_) {
;     ...
; #pragma unroll
;       for (int q = 0; q < 16; ++q) { const f32x4 gq = ((const f32x4*)(lng + part * 64))[q], bq = ((const f32x4*)(lnb + part * 64))[q];
; #pragma unroll
;           for (int e = 0; e < 4; ++e) { const int i = 4 * q + e, col = part * 64 + i; *(LAS bf16*)(L + col * 272 + j * 2) = (bf16)f2bf(x[i] * rstd * gq[e] + bq[e]); } } }
;     __syncthreads();
; #pragma unroll 1
;     for (int hh = 0; hh < 4; ++hh) { f32x4 acc[4];
; #pragma unroll
;         for (int nt = 0; nt < 4; ++nt) acc[nt] = (f32x4){0.f, 0.f, 0.f, 0.f};
; #pragma unroll
;         for (int ks = 0; ks < 4; ++ks) { const bf16x8 a = *(const bf16x8*)(wsb + ((size_t)(hh * 128 + 16 * w + fr) * 128 + ks * 32 + fq * 8));
	v_fma_f32 v26, v26, v51, v30
	v_bfe_u32 v30, v26, 16, 1
	v_add3_u32 v26, v26, v30, s78
	ds_write_b16_d16_hi v40, v26 offset:8704
	v_mul_f32_e32 v26, v70, v34
	v_fma_f32 v26, v27, v26, v31
	v_bfe_u32 v27, v26, 16, 1
	v_add3_u32 v26, v26, v27, s78
	ds_write_b16_d16_hi v40, v26 offset:8976
	v_mul_f32_e32 v26, v69, v34
	v_fma_f32 v26, v28, v26, v32
	v_bfe_u32 v27, v26, 16, 1
	v_add3_u32 v26, v26, v27, s78
	ds_write_b16_d16_hi v40, v26 offset:9248
	v_mul_f32_e32 v26, v68, v34
	v_fmac_f32_e32 v33, v29, v26
	v_bfe_u32 v26, v33, 16, 1
	v_add3_u32 v26, v33, v26, s78
	ds_write_b16_d16_hi v40, v26 offset:9520
	v_mul_f32_e32 v26, v67, v34
	v_fma_f32 v10, v10, v26, v22
	v_bfe_u32 v22, v10, 16, 1
	v_add3_u32 v10, v10, v22, s78
	ds_write_b16_d16_hi v40, v10 offset:9792
	v_mul_f32_e32 v10, v66, v34
	v_fma_f32 v10, v11, v10, v23
	v_bfe_u32 v11, v10, 16, 1
	v_add3_u32 v10, v10, v11, s78
	ds_write_b16_d16_hi v40, v10 offset:10064
	v_mul_f32_e32 v10, v65, v34
	v_fma_f32 v10, v12, v10, v24
	v_bfe_u32 v11, v10, 16, 1
	v_add3_u32 v10, v10, v11, s78
	ds_write_b16_d16_hi v40, v10 offset:10336
	v_mul_f32_e32 v10, v64, v34
	v_fmac_f32_e32 v25, v13, v10
	v_bfe_u32 v10, v25, 16, 1
	v_add3_u32 v10, v25, v10, s78
	ds_write_b16_d16_hi v40, v10 offset:10608
	v_mul_f32_e32 v10, v63, v34
	v_fma_f32 v6, v6, v10, v18
	v_bfe_u32 v10, v6, 16, 1
	v_add3_u32 v6, v6, v10, s78
	ds_write_b16_d16_hi v40, v6 offset:10880
	v_mul_f32_e32 v6, v62, v34
	v_fma_f32 v6, v7, v6, v19
	v_bfe_u32 v7, v6, 16, 1
	v_add3_u32 v6, v6, v7, s78
	ds_write_b16_d16_hi v40, v6 offset:11152
	v_mul_f32_e32 v6, v61, v34
	v_fma_f32 v6, v8, v6, v20
	v_bfe_u32 v7, v6, 16, 1
	v_add3_u32 v6, v6, v7, s78
	ds_write_b16_d16_hi v40, v6 offset:11424
	v_mul_f32_e32 v6, v60, v34
	v_fmac_f32_e32 v21, v9, v6
	v_bfe_u32 v6, v21, 16, 1
	v_add3_u32 v6, v21, v6, s78
	ds_write_b16_d16_hi v40, v6 offset:11696
	v_mul_f32_e32 v6, v59, v34
	v_fma_f32 v2, v2, v6, v14
	v_bfe_u32 v6, v2, 16, 1
	v_add3_u32 v2, v2, v6, s78
	ds_write_b16_d16_hi v40, v2 offset:11968
	v_mul_f32_e32 v2, v58, v34
	v_fma_f32 v2, v3, v2, v15
	v_bfe_u32 v3, v2, 16, 1
	v_add3_u32 v2, v2, v3, s78
	ds_write_b16_d16_hi v40, v2 offset:12240
	v_mul_f32_e32 v2, v57, v34
	v_fma_f32 v2, v4, v2, v16
	v_bfe_u32 v3, v2, 16, 1
	v_add3_u32 v2, v2, v3, s78
	ds_write_b16_d16_hi v40, v2 offset:12512
	v_mul_f32_e32 v2, v56, v34
	v_fmac_f32_e32 v17, v5, v2
	v_bfe_u32 v2, v17, 16, 1
	v_add3_u32 v2, v17, v2, s78
	ds_write_b16_d16_hi v40, v2 offset:12784
	global_load_dwordx4 v[2:5], v55, s[30:31] offset:240
	global_load_dwordx4 v[6:9], v55, s[30:31] offset:224
	global_load_dwordx4 v[10:13], v55, s[30:31] offset:208
	global_load_dwordx4 v[26:29], v55, s[30:31] offset:192
	global_load_dwordx4 v[14:17], v55, s[28:29] offset:240
	global_load_dwordx4 v[18:21], v55, s[28:29] offset:224
	global_load_dwordx4 v[22:25], v55, s[28:29] offset:208
	global_load_dwordx4 v[30:33], v55, s[28:29] offset:192
	v_mul_f32_e32 v51, v54, v34
	s_waitcnt vmcnt(0)
	v_fma_f32 v26, v26, v51, v30
	v_bfe_u32 v30, v26, 16, 1
	v_add3_u32 v26, v26, v30, s78
	ds_write_b16_d16_hi v40, v26 offset:13056
	v_mul_f32_e32 v26, v53, v34
	v_fma_f32 v26, v27, v26, v31
	v_bfe_u32 v27, v26, 16, 1
	v_add3_u32 v26, v26, v27, s78
	ds_write_b16_d16_hi v40, v26 offset:13328
	v_mul_f32_e32 v26, v35, v34
	v_fma_f32 v26, v28, v26, v32
	v_bfe_u32 v27, v26, 16, 1
	v_add3_u32 v26, v26, v27, s78
	ds_write_b16_d16_hi v40, v26 offset:13600
	v_mul_f32_e32 v26, v37, v34
	v_fmac_f32_e32 v33, v29, v26
	v_bfe_u32 v26, v33, 16, 1
	v_add3_u32 v26, v33, v26, s78
	ds_write_b16_d16_hi v40, v26 offset:13872
	v_mul_f32_e32 v26, v38, v34
	v_fma_f32 v10, v10, v26, v22
	v_bfe_u32 v22, v10, 16, 1
	v_add3_u32 v10, v10, v22, s78
	ds_write_b16_d16_hi v40, v10 offset:14144
	v_mul_f32_e32 v10, v36, v34
	v_fma_f32 v10, v11, v10, v23
	v_bfe_u32 v11, v10, 16, 1
	v_add3_u32 v10, v10, v11, s78
	ds_write_b16_d16_hi v40, v10 offset:14416
	v_mul_f32_e32 v10, v39, v34
	v_fma_f32 v10, v12, v10, v24
	v_bfe_u32 v11, v10, 16, 1
	v_add3_u32 v10, v10, v11, s78
	ds_write_b16_d16_hi v40, v10 offset:14688
	v_mul_f32_e32 v10, v41, v34
	v_fmac_f32_e32 v25, v13, v10
	v_bfe_u32 v10, v25, 16, 1
	v_add3_u32 v10, v25, v10, s78
	ds_write_b16_d16_hi v40, v10 offset:14960
	v_mul_f32_e32 v10, v49, v34
	v_fma_f32 v6, v6, v10, v18
	v_bfe_u32 v10, v6, 16, 1
	v_add3_u32 v6, v6, v10, s78
	ds_write_b16_d16_hi v40, v6 offset:15232
	v_mul_f32_e32 v6, v48, v34
	v_fma_f32 v6, v7, v6, v19
	v_bfe_u32 v7, v6, 16, 1
	v_add3_u32 v6, v6, v7, s78
	ds_write_b16_d16_hi v40, v6 offset:15504
	v_mul_f32_e32 v6, v47, v34
	v_fma_f32 v6, v8, v6, v20
	v_bfe_u32 v7, v6, 16, 1
	v_add3_u32 v6, v6, v7, s78
	ds_write_b16_d16_hi v40, v6 offset:15776
	v_mul_f32_e32 v6, v46, v34
	v_fmac_f32_e32 v21, v9, v6
	v_bfe_u32 v6, v21, 16, 1
	v_add3_u32 v6, v21, v6, s78
	ds_write_b16_d16_hi v40, v6 offset:16048
	v_mul_f32_e32 v6, v45, v34
	v_fma_f32 v2, v2, v6, v14
	v_bfe_u32 v6, v2, 16, 1
	v_add3_u32 v2, v2, v6, s78
	ds_write_b16_d16_hi v40, v2 offset:16320
	v_mul_f32_e32 v2, v44, v34
	v_fma_f32 v2, v3, v2, v15
	v_bfe_u32 v3, v2, 16, 1
	v_add3_u32 v2, v2, v3, s78
	ds_write_b16_d16_hi v40, v2 offset:16592
	v_mul_f32_e32 v2, v43, v34
	v_fma_f32 v2, v4, v2, v16
	v_bfe_u32 v3, v2, 16, 1
	v_add3_u32 v2, v2, v3, s78
	ds_write_b16_d16_hi v40, v2 offset:16864
	v_mul_f32_e32 v2, v42, v34
	v_fmac_f32_e32 v17, v5, v2
	v_bfe_u32 v2, v17, 16, 1
	v_add3_u32 v2, v17, v2, s78
	ds_write_b16_d16_hi v40, v2 offset:17136
	v_bfe_u32 v2, v1, 4, 2
	v_lshlrev_b32_e32 v162, 4, v2
	v_bfi_b32 v14, -16, v50, v1
	v_lshlrev_b32_e32 v1, 3, v2
	v_lshl_add_u64 v[2:3], s[20:21], 0, v[162:163]
	v_lshl_add_u64 v[16:17], v[2:3], 0, s[4:5]
	v_add_u32_e32 v2, s8, v14
	v_ashrrev_i32_e32 v3, 31, v2
	v_lshlrev_b64 v[2:3], 11, v[2:3]
	v_and_b32_e32 v4, -16, v50
	v_or_b32_e32 v2, v2, v1
	v_lshl_add_u64 v[18:19], s[64:65], 0, v[2:3]
	v_add3_u32 v2, s8, v4, v52
	v_ashrrev_i32_e32 v3, 31, v2
	v_lshlrev_b64 v[2:3], 12, v[2:3]
	v_or_b32_e32 v2, v2, v1
	v_mul_u32_u24_e32 v1, 0x110, v52
	v_lshl_add_u64 v[20:21], s[64:65], 0, v[2:3]
	v_add3_u32 v1, v1, v162, 0
	s_mov_b64 s[20:21], 0
	s_waitcnt lgkmcnt(0)
	s_barrier

; #define LAS __attribute__((address_space(3)))
; __device__ __forceinline__ unsigned pk2(float lo, float hi) { unsigned r; asm("v_cvt_pk_bf16_f32 %0, %1, %2" : "=v"(r) : "v"(lo), "v"(hi)); return r; }
; #define MFMA16(a, b, c) __builtin_amdgcn_mfma_f32_16x16x32_bf16((a), (b), (c), 0, 0, 0)
; template <int DIR>
; __device__ __forceinline__ void m3_dir(LAS unsigned char* L, const LAS float* ga, const f32x4 (&S)[8], const bf16x8 (&aq)[2], const bf16x8 (&cpf)[8][2], f32x4 npv, float mp, f32x4 (&acc)[8], float (&inter)[4], float (&mt)[4], float (&rs)[4], int w, int lane) {
;     ...
;     const LAS float* li = ga + DIR * 384; const LAS float* bb = li + 128; const LAS float* pm = li + 256;
;     float bj[4];
; #pragma unroll
;     for (int r = 0; r < 4; ++r) { const int j = 16 * w + 4 * fq + r; bj[r] = bb[j]; mt[r] = fmaxf(bj[r] + pm[j], bj[r] + mp); inter[r] = __expf(bj[r] + mp - mt[r]); rs[r] = 0.f; }
; #pragma unroll
;     for (int nt = 0; nt < 8; ++nt) { const int s = nt * 16 + fr; const float xs = li[s] - bb[s];
; #pragma unroll
;         for (int r = 0; r < 4; ++r) { const int j = 16 * w + 4 * fq + r; const bool valid = DIR ? (s >= j) : (s <= j);
;             const float pv = valid ? __expf(bj[r] + xs - mt[r]) * S[nt][r] : 0.f; rs[r] += pv; *(LAS bf16*)(L + SM + j * 272 + s * 2) = (bf16)pk2(pv, 0.f); } }
; __device__ __forceinline__ void m3_unit(LAS unsigned char* L, int u, const bf16* z, const float* gates, const float* cw, const bf16* cprev, const float* nprev, const float* mprev, const float* normg, bf16* mix, int tid_) {
;     ...
;     f32x4 S[8]; bf16x8 aq[2];
; #pragma unroll
;     for (int ks = 0; ks < 2; ++ks) aq[ks] = *(const LAS bf16x8*)(L + QS + (16 * w + fr) * 144 + ks * 64 + fq * 16);
; #pragma unroll
;     for (int nt = 0; nt < 8; ++nt) { f32x4 a = {0.f, 0.f, 0.f, 0.f};
; #pragma unroll
;         for (int ks = 0; ks < 2; ++ks) { const bf16x8 bk = *(const LAS bf16x8*)(L + KS + (nt * 16 + fr) * 144 + ks * 64 + fq * 16); a = MFMA16(aq[ks], bk, a); }
;         S[nt] = a; }
.LBB0_787:
	s_or_b64 exec, exec, s[8:9]
	v_lshlrev_b32_e32 v188, 4, v111
	v_or_b32_e32 v190, v188, v162
	v_add_u32_e32 v170, 0, v158
	s_movk_i32 s8, 0x90
	v_mad_u64_u32 v[6:7], s[4:5], v190, s8, v[170:171]
	v_mad_u32_u24 v111, v162, s8, v170
	s_waitcnt lgkmcnt(0)
	s_barrier
	ds_read_b128 v[2:5], v6
	ds_read_b128 v[6:9], v6 offset:64
	ds_read_b128 v[10:13], v111 offset:18432
	ds_read_b128 v[14:17], v111 offset:18496
	s_waitcnt lgkmcnt(1)
	v_mfma_f32_16x16x32_bf16 v[10:13], v[2:5], v[10:13], 0
	v_bfe_u32 v1, v110, 4, 2
	v_lshrrev_b32_e32 v110, 2, v110
	v_and_or_b32 v159, v110, 12, v188
	s_waitcnt lgkmcnt(0)
	v_mfma_f32_16x16x32_bf16 v[70:73], v[6:9], v[14:17], v[10:13]
	ds_read_b128 v[14:17], v111 offset:20800
	v_lshlrev_b32_e32 v192, 2, v159
	v_add_u32_e32 v193, 0, v192
	ds_read_b128 v[10:13], v111 offset:20736
	s_waitcnt lgkmcnt(0)
	v_mfma_f32_16x16x32_bf16 v[10:13], v[2:5], v[10:13], 0
	v_add_u32_e32 v110, s37, v192
	v_add_u32_e32 v114, 0x1a400, v193
	v_lshlrev_b32_e32 v194, 2, v162
	v_mfma_f32_16x16x32_bf16 v[66:69], v[6:9], v[14:17], v[10:13]
	ds_read_b128 v[14:17], v111 offset:23104
	s_add_i32 s4, 0, 0x1a000
	v_or_b32_e32 v185, 32, v162
	s_nop 0
	ds_read_b128 v[10:13], v111 offset:23040
	s_waitcnt lgkmcnt(0)
	v_mfma_f32_16x16x32_bf16 v[10:13], v[2:5], v[10:13], 0
	v_mul_lo_u32 v129, v159, s53
	v_or_b32_e32 v180, 0x50, v162
	v_or_b32_e32 v183, 0x60, v162
	v_mfma_f32_16x16x32_bf16 v[62:65], v[6:9], v[14:17], v[10:13]
	ds_read_b128 v[14:17], v111 offset:25408
	v_add_u32_e32 v127, 0x330, v129
	v_lshl_add_u32 v131, v185, 1, s97
	s_nop 0
	ds_read_b128 v[10:13], v111 offset:25344
	s_waitcnt lgkmcnt(0)
	v_mfma_f32_16x16x32_bf16 v[10:13], v[2:5], v[10:13], 0
	v_or_b32_e32 v189, 0x70, v119
	v_add_u32_e32 v217, v131, v129
	v_add_u32_e32 v220, v131, v127
	v_mfma_f32_16x16x32_bf16 v[58:61], v[6:9], v[14:17], v[10:13]
	ds_read_b128 v[14:17], v111 offset:27712
	v_lshlrev_b32_e32 v237, 2, v183
	v_lshlrev_b32_e32 v242, 2, v189
	s_nop 0
	ds_read_b128 v[10:13], v111 offset:27648
	s_waitcnt lgkmcnt(0)
	v_mfma_f32_16x16x32_bf16 v[10:13], v[2:5], v[10:13], 0
	ds_read_b128 v[120:123], v111 offset:34624
	v_or_b32_e32 v187, 48, v119
	v_add_u32_e32 v119, s4, v242
	v_mfma_f32_16x16x32_bf16 v[54:57], v[6:9], v[14:17], v[10:13]
	ds_read_b128 v[14:17], v111 offset:30016
	v_cmp_gt_i32_e32 vcc, v162, v159
	v_or_b32_e32 v181, 2, v159
	s_nop 0
	ds_read_b128 v[10:13], v111 offset:29952
	s_waitcnt lgkmcnt(0)
	v_mfma_f32_16x16x32_bf16 v[10:13], v[2:5], v[10:13], 0
	v_or_b32_e32 v171, 3, v159
	v_or_b32_e32 v186, 16, v162
	v_lshlrev_b32_e32 v207, 2, v186
	v_mfma_f32_16x16x32_bf16 v[22:25], v[6:9], v[14:17], v[10:13]
	ds_read_b128 v[14:17], v111 offset:32320
	v_lshlrev_b32_e32 v214, 2, v185
	v_lshlrev_b32_e32 v221, 2, v187
	s_nop 0
	ds_read_b128 v[10:13], v111 offset:32256
	s_waitcnt lgkmcnt(0)
	v_mfma_f32_16x16x32_bf16 v[10:13], v[2:5], v[10:13], 0
	v_or_b32_e32 v182, 64, v162
	v_lshlrev_b32_e32 v224, 2, v182
	v_lshlrev_b32_e32 v232, 2, v180
	v_mfma_f32_16x16x32_bf16 v[14:17], v[6:9], v[14:17], v[10:13]
	s_movk_i32 s84, 0x90
	s_nop 2
	ds_read_b128 v[10:13], v111 offset:34560
	s_waitcnt lgkmcnt(0)
	v_mfma_f32_16x16x32_bf16 v[10:13], v[2:5], v[10:13], 0
	ds_read_b128 v[110:113], v110
	v_mfma_f32_16x16x32_bf16 v[10:13], v[6:9], v[120:123], v[10:13]
	ds_read_b128 v[122:125], v114
	s_waitcnt vmcnt(1) lgkmcnt(1)
	v_add_f32_e32 v116, v115, v110
	v_add_f32_e32 v117, v115, v111
	v_add_f32_e32 v118, v115, v112
	v_add_f32_e32 v115, v115, v113
	s_waitcnt lgkmcnt(0)
	v_add_f32_e32 v114, v110, v122
	v_max_f32_e32 v215, v114, v116
	v_sub_f32_e32 v114, v116, v215
	v_mul_f32_e32 v114, 0x3fb8aa3b, v114
	v_exp_f32_e32 v116, v114
	v_add_f32_e32 v114, v111, v123
	v_max_f32_e32 v216, v114, v117
	v_sub_f32_e32 v114, v117, v216
	v_mul_f32_e32 v114, 0x3fb8aa3b, v114
	v_exp_f32_e32 v117, v114
	v_add_f32_e32 v114, v112, v124
	v_max_f32_e32 v213, v114, v118
	v_sub_f32_e32 v114, v118, v213
	v_add_f32_e32 v118, v113, v125
	v_max_f32_e32 v212, v118, v115
	v_add_u32_e32 v118, s4, v194
	v_add_u32_e32 v120, s37, v194
	ds_read_b32 v118, v118
	ds_read_b32 v120, v120
	v_add_u32_e32 v123, 0x110, v129
	v_add_u32_e32 v125, 0x220, v129
	v_add_u32_e32 v218, v131, v123
	v_add_u32_e32 v219, v131, v125
	v_lshl_add_u32 v131, v180, 1, s97
	v_add_u32_e32 v233, v131, v129
	v_add_u32_e32 v234, v131, v123
	v_add_u32_e32 v235, v131, v125
	v_add_u32_e32 v236, v131, v127
	v_add_u32_e32 v131, s4, v237
	ds_read_b32 v131, v131
	ds_read_b32 v119, v119
	s_waitcnt lgkmcnt(2)
	v_sub_f32_e32 v118, v118, v120
	v_add_f32_e32 v122, v110, v118
	v_sub_f32_e32 v122, v122, v215
	v_mul_f32_e32 v122, 0x3fb8aa3b, v122
	v_exp_f32_e32 v122, v122
	v_lshl_add_u32 v120, v162, 1, s97
	v_add_u32_e32 v195, v120, v129
	v_or_b32_e32 v121, 1, v159
	v_mul_f32_e32 v122, v70, v122
	v_cndmask_b32_e64 v122, v122, 0, vcc
	v_add_f32_e32 v124, 0, v122
	v_cvt_pk_bf16_f32 v122, v122, v163
	ds_write_b16 v195, v122
	v_add_f32_e32 v122, v111, v118
	v_sub_f32_e32 v122, v122, v216
	v_mul_f32_e32 v122, 0x3fb8aa3b, v122
	v_exp_f32_e32 v122, v122
	v_cmp_le_i32_e64 s[38:39], v162, v121
	v_add_u32_e32 v204, v120, v123
	v_add_u32_e32 v205, v120, v125
	v_mul_f32_e32 v122, v71, v122
	v_cndmask_b32_e64 v122, 0, v122, s[38:39]
	v_add_f32_e32 v126, 0, v122
	v_cvt_pk_bf16_f32 v122, v122, v163
	ds_write_b16 v204, v122
	v_add_f32_e32 v122, v112, v118
	v_sub_f32_e32 v122, v122, v213
	v_add_f32_e32 v118, v113, v118
	v_mul_f32_e32 v122, 0x3fb8aa3b, v122
	v_sub_f32_e32 v118, v118, v212
	v_exp_f32_e32 v122, v122
	v_mul_f32_e32 v118, 0x3fb8aa3b, v118
	v_exp_f32_e32 v118, v118
	v_cmp_le_i32_e64 s[38:39], v162, v181
	v_mul_f32_e32 v122, v72, v122
	v_add_u32_e32 v206, v120, v127
	v_cndmask_b32_e64 v122, 0, v122, s[38:39]
	v_mul_f32_e32 v118, v73, v118
	v_cmp_le_i32_e64 s[38:39], v162, v171
	v_add_f32_e32 v128, 0, v122
	v_cvt_pk_bf16_f32 v122, v122, v163
	ds_write_b16 v205, v122
	v_cndmask_b32_e64 v118, 0, v118, s[38:39]
	v_add_f32_e32 v122, 0, v118
	v_cvt_pk_bf16_f32 v118, v118, v163
	ds_write_b16 v206, v118
	v_add_u32_e32 v118, s4, v207
	v_add_u32_e32 v120, s37, v207
	ds_read_b32 v118, v118
	ds_read_b32 v120, v120
	v_cmp_gt_i32_e64 s[38:39], v186, v159
	v_cmp_le_i32_e64 s[40:41], v186, v121
	v_cmp_le_i32_e64 s[42:43], v185, v121
	v_cmp_le_i32_e64 s[44:45], v187, v121
	s_waitcnt lgkmcnt(0)
; #define LAS __attribute__((address_space(3)))
; __device__ __forceinline__ unsigned pk2(float lo, float hi) { unsigned r; asm("v_cvt_pk_bf16_f32 %0, %1, %2" : "=v"(r) : "v"(lo), "v"(hi)); return r; }
; #define SHX(v, m) (((m) < 32) ? __int_as_float(__builtin_amdgcn_ds_swizzle(__float_as_int(v), ((((m) & 31) << 10) | 0x1f))) : shx32(v))
; #define LDS_FENCE() asm volatile("s_waitcnt lgkmcnt(0)" ::: "memory")
; #define MFMA16(a, b, c) __builtin_amdgcn_mfma_f32_16x16x32_bf16((a), (b), (c), 0, 0, 0)
; template <int DIR>
; __device__ __forceinline__ void m3_dir(LAS unsigned char* L, const LAS float* ga, const f32x4 (&S)[8], const bf16x8 (&aq)[2], const bf16x8 (&cpf)[8][2], f32x4 npv, float mp, f32x4 (&acc)[8], float (&inter)[4], float (&mt)[4], float (&rs)[4], int w, int lane) {
;     ...
;     for (int r = 0; r < 4; ++r) { const int j = 16 * w + 4 * fq + r; bj[r] = bb[j]; mt[r] = fmaxf(bj[r] + pm[j], bj[r] + mp); inter[r] = __expf(bj[r] + mp - mt[r]); rs[r] = 0.f; }
; #pragma unroll
;     for (int nt = 0; nt < 8; ++nt) { const int s = nt * 16 + fr; const float xs = li[s] - bb[s];
; #pragma unroll
;         for (int r = 0; r < 4; ++r) { const int j = 16 * w + 4 * fq + r; const bool valid = DIR ? (s >= j) : (s <= j);
;             const float pv = valid ? __expf(bj[r] + xs - mt[r]) * S[nt][r] : 0.f; rs[r] += pv; *(LAS bf16*)(L + SM + j * 272 + s * 2) = (bf16)pk2(pv, 0.f); } }
; #pragma unroll
;     for (int r = 0; r < 4; ++r) { rs[r] += SHX(rs[r], 1); rs[r] += SHX(rs[r], 2); rs[r] += SHX(rs[r], 4); rs[r] += SHX(rs[r], 8); }
;     LDS_FENCE();
; #pragma unroll
;     for (int nt = 0; nt < 8; ++nt) { f32x4 a = {0.f, 0.f, 0.f, 0.f};
; #pragma unroll
;         for (int ks = 0; ks < 2; ++ks) a = MFMA16(aq[ks], cpf[nt][ks], a);
; #pragma unroll
;         for (int r = 0; r < 4; ++r) a[r] *= inter[r];
;         acc[nt] = a; }
	v_sub_f32_e32 v118, v118, v120
	v_add_f32_e32 v130, v110, v118
	v_sub_f32_e32 v130, v130, v215
	v_mul_f32_e32 v130, 0x3fb8aa3b, v130
	v_exp_f32_e32 v130, v130
	v_lshl_add_u32 v120, v186, 1, s97
	v_add_u32_e32 v208, v120, v129
	v_add_u32_e32 v209, v120, v123
	v_mul_f32_e32 v130, v66, v130
	v_cndmask_b32_e64 v130, v130, 0, s[38:39]
	v_add_f32_e32 v124, v124, v130
	v_cvt_pk_bf16_f32 v130, v130, v163
	ds_write_b16 v208, v130
	v_add_f32_e32 v130, v111, v118
	v_sub_f32_e32 v130, v130, v216
	v_mul_f32_e32 v130, 0x3fb8aa3b, v130
	v_exp_f32_e32 v130, v130
	v_add_u32_e32 v210, v120, v125
	v_add_u32_e32 v211, v120, v127
	v_add_u32_e32 v120, s37, v214
	v_mul_f32_e32 v130, v67, v130
	v_cndmask_b32_e64 v130, 0, v130, s[40:41]
	v_add_f32_e32 v126, v126, v130
	v_cvt_pk_bf16_f32 v130, v130, v163
	ds_write_b16 v209, v130
	v_add_f32_e32 v130, v112, v118
	v_sub_f32_e32 v130, v130, v213
	v_add_f32_e32 v118, v113, v118
	v_mul_f32_e32 v130, 0x3fb8aa3b, v130
	v_sub_f32_e32 v118, v118, v212
	v_exp_f32_e32 v130, v130
	v_mul_f32_e32 v118, 0x3fb8aa3b, v118
	v_exp_f32_e32 v118, v118
	v_cmp_le_i32_e64 s[40:41], v186, v181
	v_mul_f32_e32 v130, v68, v130
	ds_read_b32 v120, v120
	v_cndmask_b32_e64 v130, 0, v130, s[40:41]
	v_mul_f32_e32 v118, v69, v118
	v_cmp_le_i32_e64 s[40:41], v186, v171
	v_add_f32_e32 v128, v128, v130
	v_cvt_pk_bf16_f32 v130, v130, v163
	ds_write_b16 v210, v130
	v_cndmask_b32_e64 v118, 0, v118, s[40:41]
	v_add_f32_e32 v130, v122, v118
	v_cvt_pk_bf16_f32 v118, v118, v163
	ds_write_b16 v211, v118
	v_add_u32_e32 v118, s4, v214
	ds_read_b32 v118, v118
	v_cmp_gt_i32_e64 s[40:41], v185, v159
	v_cmp_le_i32_e64 s[46:47], v182, v121
	v_cmp_le_i32_e64 s[48:49], v180, v121
	v_cmp_le_i32_e64 s[50:51], v183, v121
	s_waitcnt lgkmcnt(0)
	v_sub_f32_e32 v118, v118, v120
	v_add_f32_e32 v120, v110, v118
	v_sub_f32_e32 v120, v120, v215
	v_mul_f32_e32 v120, 0x3fb8aa3b, v120
	v_exp_f32_e32 v120, v120
	v_cmp_le_i32_e64 s[54:55], v189, v121
	v_mfma_f32_16x16x32_bf16 v[30:33], v[2:5], v[30:33], 0
	v_sub_f32_e32 v115, v115, v212
	v_mul_f32_e32 v120, v62, v120
	v_cndmask_b32_e64 v120, v120, 0, s[40:41]
	v_add_f32_e32 v124, v124, v120
	v_cvt_pk_bf16_f32 v120, v120, v163
	ds_write_b16 v217, v120
	v_add_f32_e32 v120, v111, v118
	v_sub_f32_e32 v120, v120, v216
	v_mul_f32_e32 v120, 0x3fb8aa3b, v120
	v_exp_f32_e32 v120, v120
	v_mfma_f32_16x16x32_bf16 v[30:33], v[6:9], v[34:37], v[30:33]
	v_lshlrev_b32_e32 v34, 3, v162
	v_mul_lo_u32 v35, v159, s8
	v_mul_f32_e32 v120, v63, v120
	v_cndmask_b32_e64 v120, 0, v120, s[42:43]
	v_add_f32_e32 v122, v126, v120
	v_cvt_pk_bf16_f32 v120, v120, v163
	ds_write_b16 v218, v120
	v_add_f32_e32 v120, v112, v118
	v_sub_f32_e32 v120, v120, v213
	v_mul_f32_e32 v120, 0x3fb8aa3b, v120
	v_add_f32_e32 v118, v113, v118
	v_exp_f32_e32 v120, v120
	v_sub_f32_e32 v118, v118, v212
	v_mul_f32_e32 v118, 0x3fb8aa3b, v118
	v_exp_f32_e32 v118, v118
	v_mul_f32_e32 v120, v64, v120
	v_cmp_le_i32_e64 s[42:43], v185, v181
	v_add3_u32 v222, 0, v34, v35
	v_mul_f32_e32 v118, v65, v118
	v_cndmask_b32_e64 v126, 0, v120, s[42:43]
	v_add_f32_e32 v120, v128, v126
	v_cvt_pk_bf16_f32 v126, v126, v163
	v_cmp_le_i32_e64 s[42:43], v185, v171
	ds_write_b16 v219, v126
	v_add_u32_e32 v128, s37, v221
	v_cndmask_b32_e64 v126, 0, v118, s[42:43]
	v_add_f32_e32 v118, v130, v126
	v_cvt_pk_bf16_f32 v126, v126, v163
	ds_write_b16 v220, v126
	v_add_u32_e32 v126, s4, v221
	ds_read_b32 v126, v126
	ds_read_b32 v128, v128
	v_cmp_gt_i32_e64 s[42:43], v187, v159
	v_mfma_f32_16x16x32_bf16 v[38:41], v[2:5], v[38:41], 0
	v_mul_f32_e32 v114, 0x3fb8aa3b, v114
	v_mul_f32_e32 v115, 0x3fb8aa3b, v115
	s_waitcnt lgkmcnt(0)
	v_sub_f32_e32 v126, v126, v128
	v_add_f32_e32 v130, v110, v126
	v_sub_f32_e32 v130, v130, v215
	v_mul_f32_e32 v130, 0x3fb8aa3b, v130
	v_exp_f32_e32 v130, v130
	v_lshl_add_u32 v128, v187, 1, s97
	v_add_u32_e32 v223, v128, v129
	v_add_u32_e32 v225, v128, v123
	v_mul_f32_e32 v130, v58, v130
	v_cndmask_b32_e64 v130, v130, 0, s[42:43]
	v_add_f32_e32 v124, v124, v130
	v_cvt_pk_bf16_f32 v130, v130, v163
	ds_write_b16 v223, v130
	v_add_f32_e32 v130, v111, v126
	v_sub_f32_e32 v130, v130, v216
	v_mul_f32_e32 v130, 0x3fb8aa3b, v130
	v_exp_f32_e32 v130, v130
	v_add_u32_e32 v230, v128, v127
	v_add_u32_e32 v226, v128, v125
	v_add_u32_e32 v128, s37, v224
	v_mul_f32_e32 v130, v59, v130
	v_cndmask_b32_e64 v130, 0, v130, s[44:45]
	v_add_f32_e32 v122, v122, v130
	v_cvt_pk_bf16_f32 v130, v130, v163
	ds_write_b16 v225, v130
	v_add_f32_e32 v130, v112, v126
	v_sub_f32_e32 v130, v130, v213
	v_add_f32_e32 v126, v113, v126
	v_mul_f32_e32 v130, 0x3fb8aa3b, v130
	v_sub_f32_e32 v126, v126, v212
	v_exp_f32_e32 v130, v130
	v_mul_f32_e32 v126, 0x3fb8aa3b, v126
	v_exp_f32_e32 v126, v126
	v_cmp_le_i32_e64 s[44:45], v187, v181
	v_mul_f32_e32 v130, v60, v130
	ds_read_b32 v128, v128
	v_cndmask_b32_e64 v130, 0, v130, s[44:45]
	v_mul_f32_e32 v126, v61, v126
	v_cmp_le_i32_e64 s[44:45], v187, v171
	v_add_f32_e32 v120, v120, v130
	v_cvt_pk_bf16_f32 v130, v130, v163
	ds_write_b16 v226, v130
	v_cndmask_b32_e64 v126, 0, v126, s[44:45]
	v_add_f32_e32 v118, v118, v126
	v_cvt_pk_bf16_f32 v126, v126, v163
	ds_write_b16 v230, v126
	v_add_u32_e32 v126, s4, v224
	ds_read_b32 v126, v126
	v_cmp_gt_i32_e64 s[44:45], v182, v159
	v_mfma_f32_16x16x32_bf16 v[38:41], v[6:9], v[42:45], v[38:41]
	v_exp_f32_e32 v114, v114
	v_exp_f32_e32 v115, v115
	s_waitcnt lgkmcnt(0)
; #define LAS __attribute__((address_space(3)))
; __device__ __forceinline__ unsigned pk2(float lo, float hi) { unsigned r; asm("v_cvt_pk_bf16_f32 %0, %1, %2" : "=v"(r) : "v"(lo), "v"(hi)); return r; }
; #define SHX(v, m) (((m) < 32) ? __int_as_float(__builtin_amdgcn_ds_swizzle(__float_as_int(v), ((((m) & 31) << 10) | 0x1f))) : shx32(v))
; #define LDS_FENCE() asm volatile("s_waitcnt lgkmcnt(0)" ::: "memory")
; #define MFMA16(a, b, c) __builtin_amdgcn_mfma_f32_16x16x32_bf16((a), (b), (c), 0, 0, 0)
; template <int DIR>
; __device__ __forceinline__ void m3_dir(LAS unsigned char* L, const LAS float* ga, const f32x4 (&S)[8], const bf16x8 (&aq)[2], const bf16x8 (&cpf)[8][2], f32x4 npv, float mp, f32x4 (&acc)[8], float (&inter)[4], float (&mt)[4], float (&rs)[4], int w, int lane) {
;     ...
;     for (int r = 0; r < 4; ++r) { const int j = 16 * w + 4 * fq + r; bj[r] = bb[j]; mt[r] = fmaxf(bj[r] + pm[j], bj[r] + mp); inter[r] = __expf(bj[r] + mp - mt[r]); rs[r] = 0.f; }
; #pragma unroll
;     for (int nt = 0; nt < 8; ++nt) { const int s = nt * 16 + fr; const float xs = li[s] - bb[s];
; #pragma unroll
;         for (int r = 0; r < 4; ++r) { const int j = 16 * w + 4 * fq + r; const bool valid = DIR ? (s >= j) : (s <= j);
;             const float pv = valid ? __expf(bj[r] + xs - mt[r]) * S[nt][r] : 0.f; rs[r] += pv; *(LAS bf16*)(L + SM + j * 272 + s * 2) = (bf16)pk2(pv, 0.f); } }
; #pragma unroll
;     for (int r = 0; r < 4; ++r) { rs[r] += SHX(rs[r], 1); rs[r] += SHX(rs[r], 2); rs[r] += SHX(rs[r], 4); rs[r] += SHX(rs[r], 8); }
;     LDS_FENCE();
; #pragma unroll
;     for (int nt = 0; nt < 8; ++nt) { f32x4 a = {0.f, 0.f, 0.f, 0.f};
; #pragma unroll
;         for (int ks = 0; ks < 2; ++ks) a = MFMA16(aq[ks], cpf[nt][ks], a);
; #pragma unroll
;         for (int r = 0; r < 4; ++r) a[r] *= inter[r];
;         acc[nt] = a; }
	v_sub_f32_e32 v126, v126, v128
	v_add_f32_e32 v130, v110, v126
	v_sub_f32_e32 v130, v130, v215
	v_mul_f32_e32 v130, 0x3fb8aa3b, v130
	v_exp_f32_e32 v130, v130
	v_lshl_add_u32 v128, v182, 1, s97
	v_add_u32_e32 v227, v128, v129
	v_add_u32_e32 v228, v128, v123
	v_mul_f32_e32 v130, v54, v130
	v_cndmask_b32_e64 v130, v130, 0, s[44:45]
	v_add_f32_e32 v124, v124, v130
	v_cvt_pk_bf16_f32 v130, v130, v163
	ds_write_b16 v227, v130
	v_add_f32_e32 v130, v111, v126
	v_sub_f32_e32 v130, v130, v216
	v_mul_f32_e32 v130, 0x3fb8aa3b, v130
	v_exp_f32_e32 v130, v130
	v_add_u32_e32 v231, v128, v127
	v_add_u32_e32 v229, v128, v125
	v_add_u32_e32 v128, s37, v232
	v_mul_f32_e32 v130, v55, v130
	v_cndmask_b32_e64 v130, 0, v130, s[46:47]
	v_add_f32_e32 v122, v122, v130
	v_cvt_pk_bf16_f32 v130, v130, v163
	ds_write_b16 v228, v130
	v_add_f32_e32 v130, v112, v126
	v_sub_f32_e32 v130, v130, v213
	v_add_f32_e32 v126, v113, v126
	v_mul_f32_e32 v130, 0x3fb8aa3b, v130
	v_sub_f32_e32 v126, v126, v212
	v_exp_f32_e32 v130, v130
	v_mul_f32_e32 v126, 0x3fb8aa3b, v126
	v_exp_f32_e32 v126, v126
	v_cmp_le_i32_e64 s[46:47], v182, v181
	v_mul_f32_e32 v130, v56, v130
	ds_read_b32 v128, v128
	v_cndmask_b32_e64 v130, 0, v130, s[46:47]
	v_mul_f32_e32 v126, v57, v126
	v_cmp_le_i32_e64 s[46:47], v182, v171
	v_add_f32_e32 v120, v120, v130
	v_cvt_pk_bf16_f32 v130, v130, v163
	ds_write_b16 v229, v130
	v_cndmask_b32_e64 v126, 0, v126, s[46:47]
	v_add_f32_e32 v118, v118, v126
	v_cvt_pk_bf16_f32 v126, v126, v163
	ds_write_b16 v231, v126
	v_add_u32_e32 v126, s4, v232
	ds_read_b32 v126, v126
	v_cmp_gt_i32_e64 s[46:47], v180, v159
	v_mfma_f32_16x16x32_bf16 v[106:109], v[2:5], v[106:109], 0
	s_mov_b64 s[4:5], 0x800000
	v_pk_mul_f32 v[40:41], v[114:115], v[40:41]
	s_waitcnt lgkmcnt(0)
	v_sub_f32_e32 v126, v126, v128
	v_add_f32_e32 v128, v110, v126
	v_sub_f32_e32 v128, v128, v215
	v_mul_f32_e32 v128, 0x3fb8aa3b, v128
	v_exp_f32_e32 v128, v128
	v_mfma_f32_16x16x32_bf16 v[98:101], v[2:5], v[98:101], 0
	v_mul_f32_e64 v38, v116, v38
	v_mul_f32_e64 v39, v117, v39
	v_pk_mul_f32 v[32:33], v[114:115], v[32:33]
	v_mul_f32_e32 v128, v22, v128
	v_cndmask_b32_e64 v132, v128, 0, s[46:47]
	v_cvt_pk_bf16_f32 v128, v132, v163
	ds_write_b16 v233, v128
	v_add_f32_e32 v128, v111, v126
	v_sub_f32_e32 v128, v128, v216
	v_mul_f32_e32 v128, 0x3fb8aa3b, v128
	v_exp_f32_e32 v128, v128
	v_mfma_f32_16x16x32_bf16 v[90:93], v[2:5], v[90:93], 0
	v_mul_f32_e64 v30, v116, v30
	v_mul_f32_e64 v31, v117, v31
	v_mul_f32_e32 v128, v23, v128
	v_cndmask_b32_e64 v130, 0, v128, s[48:49]
	v_cvt_pk_bf16_f32 v128, v130, v163
	ds_write_b16 v234, v128
	v_add_f32_e32 v128, v112, v126
	v_sub_f32_e32 v128, v128, v213
	v_add_f32_e32 v126, v113, v126
	v_mul_f32_e32 v128, 0x3fb8aa3b, v128
	v_sub_f32_e32 v126, v126, v212
	v_exp_f32_e32 v128, v128
	v_mul_f32_e32 v126, 0x3fb8aa3b, v126
	v_exp_f32_e32 v126, v126
	v_cmp_le_i32_e64 s[48:49], v180, v181
	v_mul_f32_e32 v128, v24, v128
	v_mfma_f32_16x16x32_bf16 v[82:85], v[2:5], v[82:85], 0
	v_cndmask_b32_e64 v128, 0, v128, s[48:49]
	v_cvt_pk_bf16_f32 v133, v128, v163
	v_mul_f32_e32 v126, v25, v126
	v_cmp_le_i32_e64 s[48:49], v180, v171
	ds_write_b16 v235, v133
	v_mfma_f32_16x16x32_bf16 v[74:77], v[2:5], v[74:77], 0
	v_cndmask_b32_e64 v126, 0, v126, s[48:49]
	v_cvt_pk_bf16_f32 v133, v126, v163
	ds_write_b16 v236, v133
	v_add_u32_e32 v133, s37, v237
	ds_read_b32 v133, v133
	v_cmp_gt_i32_e64 s[48:49], v183, v159
	v_mfma_f32_16x16x32_bf16 v[46:49], v[2:5], v[46:49], 0
	s_waitcnt lgkmcnt(0)
	v_sub_f32_e32 v131, v131, v133
	v_add_f32_e32 v134, v110, v131
	v_sub_f32_e32 v134, v134, v215
	v_mul_f32_e32 v134, 0x3fb8aa3b, v134
	v_exp_f32_e32 v134, v134
	v_lshl_add_u32 v133, v183, 1, s97
	v_add_u32_e32 v238, v133, v129
	v_add_u32_e32 v239, v133, v123
	v_mul_f32_e32 v134, v14, v134
	v_cndmask_b32_e64 v140, v134, 0, s[48:49]
	v_cvt_pk_bf16_f32 v134, v140, v163
	ds_write_b16 v238, v134
	v_add_f32_e32 v134, v111, v131
	v_sub_f32_e32 v134, v134, v216
	v_mul_f32_e32 v134, 0x3fb8aa3b, v134
	v_exp_f32_e32 v134, v134
	v_add_u32_e32 v240, v133, v125
	v_add_u32_e32 v241, v133, v127
	v_mfma_f32_16x16x32_bf16 v[102:105], v[6:9], v[102:105], v[106:109]
	v_mul_f32_e32 v134, v15, v134
	v_cndmask_b32_e64 v138, 0, v134, s[50:51]
	v_cvt_pk_bf16_f32 v134, v138, v163
	ds_write_b16 v239, v134
	v_add_f32_e32 v134, v112, v131
	v_sub_f32_e32 v134, v134, v213
	v_add_f32_e32 v131, v113, v131
	v_mul_f32_e32 v134, 0x3fb8aa3b, v134
	v_sub_f32_e32 v131, v131, v212
	v_exp_f32_e32 v134, v134
	v_mul_f32_e32 v131, 0x3fb8aa3b, v131
	v_exp_f32_e32 v131, v131
	v_cmp_le_i32_e64 s[50:51], v183, v181
	v_mul_f32_e32 v134, v16, v134
	v_mfma_f32_16x16x32_bf16 v[94:97], v[6:9], v[94:97], v[98:101]
	v_cndmask_b32_e64 v136, 0, v134, s[50:51]
	v_cvt_pk_bf16_f32 v134, v136, v163
	v_mul_f32_e32 v131, v17, v131
	v_cmp_le_i32_e64 s[50:51], v183, v171
	ds_write_b16 v240, v134
	v_mfma_f32_16x16x32_bf16 v[86:89], v[6:9], v[86:89], v[90:93]
	v_cndmask_b32_e64 v134, 0, v131, s[50:51]
	v_cvt_pk_bf16_f32 v131, v134, v163
	ds_write_b16 v241, v131
	v_add_u32_e32 v131, s37, v242
	ds_read_b32 v131, v131
	v_cmp_gt_i32_e64 s[50:51], v189, v159
	v_mfma_f32_16x16x32_bf16 v[78:81], v[6:9], v[78:81], v[82:85]
	v_mul_f32_e64 v144, v114, v104
	v_mul_f32_e64 v145, v115, v105
	v_pk_mul_f32 v[142:143], v[116:117], v[102:103]
	s_waitcnt lgkmcnt(0)
; #define LAS __attribute__((address_space(3)))
; __device__ __forceinline__ unsigned pk2(float lo, float hi) { unsigned r; asm("v_cvt_pk_bf16_f32 %0, %1, %2" : "=v"(r) : "v"(lo), "v"(hi)); return r; }
; __device__ __forceinline__ float bflo(unsigned w) { return __uint_as_float(w << 16); }
; __device__ __forceinline__ float bfhi(unsigned w) { return __uint_as_float(w & 0xffff0000u); }
; #define SHX(v, m) (((m) < 32) ? __int_as_float(__builtin_amdgcn_ds_swizzle(__float_as_int(v), ((((m) & 31) << 10) | 0x1f))) : shx32(v))
; #define LDS_FENCE() asm volatile("s_waitcnt lgkmcnt(0)" ::: "memory")
; #define MFMA16(a, b, c) __builtin_amdgcn_mfma_f32_16x16x32_bf16((a), (b), (c), 0, 0, 0)
; template <int DIR>
; __device__ __forceinline__ void m3_dir(LAS unsigned char* L, const LAS float* ga, const f32x4 (&S)[8], const bf16x8 (&aq)[2], const bf16x8 (&cpf)[8][2], f32x4 npv, float mp, f32x4 (&acc)[8], float (&inter)[4], float (&mt)[4], float (&rs)[4], int w, int lane) {
;     ...
;     for (int nt = 0; nt < 8; ++nt) { const int s = nt * 16 + fr; const float xs = li[s] - bb[s];
; #pragma unroll
;         for (int r = 0; r < 4; ++r) { const int j = 16 * w + 4 * fq + r; const bool valid = DIR ? (s >= j) : (s <= j);
;             const float pv = valid ? __expf(bj[r] + xs - mt[r]) * S[nt][r] : 0.f; rs[r] += pv; *(LAS bf16*)(L + SM + j * 272 + s * 2) = (bf16)pk2(pv, 0.f); } }
; #pragma unroll
;     for (int r = 0; r < 4; ++r) { rs[r] += SHX(rs[r], 1); rs[r] += SHX(rs[r], 2); rs[r] += SHX(rs[r], 4); rs[r] += SHX(rs[r], 8); }
;     LDS_FENCE();
; #pragma unroll
;     for (int nt = 0; nt < 8; ++nt) { f32x4 a = {0.f, 0.f, 0.f, 0.f};
; #pragma unroll
;         for (int ks = 0; ks < 2; ++ks) a = MFMA16(aq[ks], cpf[nt][ks], a);
; #pragma unroll
;         for (int r = 0; r < 4; ++r) a[r] *= inter[r];
;         acc[nt] = a; }
;     { const f32x4 np = npv;
; #pragma unroll
;       for (int r = 0; r < 4; ++r) { const int j = 16 * w + 4 * fq + r; const v2u qw = *(const LAS v2u*)(L + QS + j * 144 + fr * 8);
;           float qn = bflo(qw.x) * np[0] + bfhi(qw.x) * np[1] + bflo(qw.y) * np[2] + bfhi(qw.y) * np[3];
;           qn += SHX(qn, 1); qn += SHX(qn, 2); qn += SHX(qn, 4); qn += SHX(qn, 8);
;           rs[r] = rs[r] + inter[r] * qn; } }
	v_sub_f32_e32 v119, v119, v131
	v_add_f32_e32 v110, v110, v119
	v_sub_f32_e32 v110, v110, v215
	v_mul_f32_e32 v110, 0x3fb8aa3b, v110
	v_exp_f32_e32 v110, v110
	v_lshl_add_u32 v131, v189, 1, s97
	v_add_u32_e32 v243, v131, v129
	v_add_u32_e32 v244, v131, v123
	v_mul_f32_e32 v110, v10, v110
	v_cndmask_b32_e64 v172, v110, 0, s[50:51]
	v_cvt_pk_bf16_f32 v110, v172, v163
	ds_write_b16 v243, v110
	v_add_f32_e32 v110, v111, v119
	v_sub_f32_e32 v110, v110, v216
	v_mul_f32_e32 v110, 0x3fb8aa3b, v110
	v_exp_f32_e32 v110, v110
	v_add_u32_e32 v245, v131, v125
	v_add_u32_e32 v246, v131, v127
	v_mfma_f32_16x16x32_bf16 v[50:53], v[6:9], v[50:53], v[74:77]
	v_mul_f32_e32 v110, v11, v110
	v_cndmask_b32_e64 v174, 0, v110, s[54:55]
	v_cvt_pk_bf16_f32 v110, v174, v163
	ds_write_b16 v244, v110
	v_add_f32_e32 v110, v112, v119
	v_sub_f32_e32 v110, v110, v213
	v_mul_f32_e32 v110, 0x3fb8aa3b, v110
	v_exp_f32_e32 v110, v110
	v_cmp_le_i32_e64 s[54:55], v189, v181
	v_mfma_f32_16x16x32_bf16 v[26:29], v[6:9], v[26:29], v[46:49]
	v_mul_f32_e64 v148, v114, v96
	v_mul_f32_e64 v149, v115, v97
	v_mul_f32_e32 v110, v12, v110
	v_cndmask_b32_e64 v112, 0, v110, s[54:55]
	v_cvt_pk_bf16_f32 v110, v112, v163
	ds_write_b16 v245, v110
	v_add_f32_e32 v110, v113, v119
	v_sub_f32_e32 v110, v110, v212
	v_mul_f32_e32 v110, 0x3fb8aa3b, v110
	v_exp_f32_e32 v110, v110
	v_cmp_le_i32_e64 s[54:55], v189, v171
	v_pk_mul_f32 v[146:147], v[116:117], v[94:95]
	v_pk_mul_f32 v[152:153], v[114:115], v[88:89]
	v_mul_f32_e32 v110, v13, v110
	v_cndmask_b32_e64 v110, 0, v110, s[54:55]
	v_cvt_pk_bf16_f32 v111, v110, v163
	ds_write_b16 v246, v111
	s_waitcnt lgkmcnt(0)
	ds_read2_b64 v[34:37], v222 offset1:18
	v_pk_mul_f32 v[150:151], v[116:117], v[86:87]
	v_pk_mul_f32 v[156:157], v[114:115], v[80:81]
	v_pk_mul_f32 v[154:155], v[116:117], v[78:79]
	v_pk_mul_f32 v[52:53], v[114:115], v[52:53]
	s_waitcnt lgkmcnt(0)
	v_lshlrev_b32_e32 v42, 16, v34
	v_and_b32_e32 v34, 0xffff0000, v34
	v_mul_f32_e32 v133, v19, v34
	v_lshlrev_b32_e32 v34, 16, v35
	v_mul_f32_e32 v125, v18, v42
	v_mul_f32_e32 v141, v20, v34
	v_and_b32_e32 v34, 0xffff0000, v35
	v_mul_f32_e32 v173, v21, v34
	v_pk_add_f32 v[34:35], v[124:125], v[132:133]
	v_pk_mul_f32 v[50:51], v[116:117], v[50:51]
	v_pk_add_f32 v[34:35], v[34:35], v[140:141]
	v_pk_mul_f32 v[28:29], v[114:115], v[28:29]
	v_pk_add_f32 v[34:35], v[34:35], v[172:173]
	v_pk_mul_f32 v[26:27], v[116:117], v[26:27]
	s_waitcnt lgkmcnt(0)
	s_nop 1
	v_add_f32_dpp v34, v34, v34 quad_perm:[1,0,3,2] row_mask:0xf bank_mask:0xf
	v_add_f32_dpp v35, v35, v35 quad_perm:[1,0,3,2] row_mask:0xf bank_mask:0xf
	s_waitcnt lgkmcnt(0)
	s_nop 1
	v_add_f32_dpp v34, v34, v34 quad_perm:[2,3,0,1] row_mask:0xf bank_mask:0xf
	v_add_f32_dpp v35, v35, v35 quad_perm:[2,3,0,1] row_mask:0xf bank_mask:0xf
	s_waitcnt lgkmcnt(0)
	s_nop 1
	v_add_f32_dpp v34, v34, v34 row_half_mirror row_mask:0xf bank_mask:0xf
	v_add_f32_dpp v35, v35, v35 row_half_mirror row_mask:0xf bank_mask:0xf
	s_waitcnt lgkmcnt(0)
	s_nop 1
	v_add_f32_dpp v172, v34, v34 row_mirror row_mask:0xf bank_mask:0xf
	v_add_f32_dpp v173, v35, v35 row_mirror row_mask:0xf bank_mask:0xf
	v_lshlrev_b32_e32 v34, 16, v36
	v_mul_f32_e32 v123, v18, v34
	v_and_b32_e32 v34, 0xffff0000, v36
	v_mul_f32_e32 v131, v19, v34
	v_lshlrev_b32_e32 v34, 16, v37
	v_mul_f32_e32 v139, v20, v34
	v_and_b32_e32 v34, 0xffff0000, v37
	v_mul_f32_e32 v175, v21, v34
	v_pk_add_f32 v[34:35], v[122:123], v[130:131]
	v_fmac_f32_e32 v172, v116, v173
	v_pk_add_f32 v[34:35], v[34:35], v[138:139]
	s_nop 0
	v_pk_add_f32 v[34:35], v[34:35], v[174:175]
	s_waitcnt lgkmcnt(0)
	s_nop 1
	v_add_f32_dpp v34, v34, v34 quad_perm:[1,0,3,2] row_mask:0xf bank_mask:0xf
	v_add_f32_dpp v35, v35, v35 quad_perm:[1,0,3,2] row_mask:0xf bank_mask:0xf
	s_waitcnt lgkmcnt(0)
	s_nop 1
	v_add_f32_dpp v34, v34, v34 quad_perm:[2,3,0,1] row_mask:0xf bank_mask:0xf
	v_add_f32_dpp v35, v35, v35 quad_perm:[2,3,0,1] row_mask:0xf bank_mask:0xf
	s_waitcnt lgkmcnt(0)
	s_nop 1
	v_add_f32_dpp v34, v34, v34 row_half_mirror row_mask:0xf bank_mask:0xf
	v_add_f32_dpp v35, v35, v35 row_half_mirror row_mask:0xf bank_mask:0xf
	s_waitcnt lgkmcnt(0)
	s_nop 1
	v_add_f32_dpp v174, v34, v34 row_mirror row_mask:0xf bank_mask:0xf
	v_add_f32_dpp v175, v35, v35 row_mirror row_mask:0xf bank_mask:0xf
	ds_read2_b64 v[34:37], v222 offset0:36 offset1:54
	v_fmac_f32_e32 v174, v117, v175
	s_waitcnt lgkmcnt(0)
	v_lshlrev_b32_e32 v42, 16, v34
	v_and_b32_e32 v34, 0xffff0000, v34
	v_mul_f32_e32 v129, v19, v34
	v_lshlrev_b32_e32 v34, 16, v35
	v_mul_f32_e32 v121, v18, v42
	v_mul_f32_e32 v137, v20, v34
	v_and_b32_e32 v34, 0xffff0000, v35
	v_mul_f32_e32 v113, v21, v34
	v_pk_add_f32 v[34:35], v[120:121], v[128:129]
	s_nop 0
	v_pk_add_f32 v[34:35], v[34:35], v[136:137]
	s_nop 0
	v_pk_add_f32 v[34:35], v[34:35], v[112:113]
	s_waitcnt lgkmcnt(0)
	s_nop 1
	v_add_f32_dpp v34, v34, v34 quad_perm:[1,0,3,2] row_mask:0xf bank_mask:0xf
	v_add_f32_dpp v35, v35, v35 quad_perm:[1,0,3,2] row_mask:0xf bank_mask:0xf
	s_waitcnt lgkmcnt(0)
	s_nop 1
	v_add_f32_dpp v34, v34, v34 quad_perm:[2,3,0,1] row_mask:0xf bank_mask:0xf
	v_add_f32_dpp v35, v35, v35 quad_perm:[2,3,0,1] row_mask:0xf bank_mask:0xf
	s_waitcnt lgkmcnt(0)
	s_nop 1
	v_add_f32_dpp v34, v34, v34 row_half_mirror row_mask:0xf bank_mask:0xf
	v_add_f32_dpp v35, v35, v35 row_half_mirror row_mask:0xf bank_mask:0xf
	s_waitcnt lgkmcnt(0)
	s_nop 1
	v_add_f32_dpp v176, v34, v34 row_mirror row_mask:0xf bank_mask:0xf
	v_add_f32_dpp v177, v35, v35 row_mirror row_mask:0xf bank_mask:0xf
	v_lshlrev_b32_e32 v34, 16, v36
	v_mul_f32_e32 v119, v18, v34
	v_and_b32_e32 v18, 0xffff0000, v36
	v_mul_f32_e32 v127, v19, v18
	v_lshlrev_b32_e32 v18, 16, v37
	v_mul_f32_e32 v135, v20, v18
	v_and_b32_e32 v18, 0xffff0000, v37
	v_mul_f32_e32 v111, v21, v18
	v_pk_add_f32 v[18:19], v[118:119], v[126:127]
	v_fmac_f32_e32 v176, v114, v177
	v_pk_add_f32 v[18:19], v[18:19], v[134:135]
	s_nop 0
	v_pk_add_f32 v[18:19], v[18:19], v[110:111]
	s_waitcnt lgkmcnt(0)
; #define LAS __attribute__((address_space(3)))
; __device__ __forceinline__ float bflo(unsigned w) { return __uint_as_float(w << 16); }
; __device__ __forceinline__ float bfhi(unsigned w) { return __uint_as_float(w & 0xffff0000u); }
; #define SHX(v, m) (((m) < 32) ? __int_as_float(__builtin_amdgcn_ds_swizzle(__float_as_int(v), ((((m) & 31) << 10) | 0x1f))) : shx32(v))
; #define MFMA16(a, b, c) __builtin_amdgcn_mfma_f32_16x16x32_bf16((a), (b), (c), 0, 0, 0)
; template <int DIR>
; __device__ __forceinline__ void m3_dir(LAS unsigned char* L, const LAS float* ga, const f32x4 (&S)[8], const bf16x8 (&aq)[2], const bf16x8 (&cpf)[8][2], f32x4 npv, float mp, f32x4 (&acc)[8], float (&inter)[4], float (&mt)[4], float (&rs)[4], int w, int lane) {
;     ...
;     { const f32x4 np = npv;
; #pragma unroll
;       for (int r = 0; r < 4; ++r) { const int j = 16 * w + 4 * fq + r; const v2u qw = *(const LAS v2u*)(L + QS + j * 144 + fr * 8);
;           float qn = bflo(qw.x) * np[0] + bfhi(qw.x) * np[1] + bflo(qw.y) * np[2] + bfhi(qw.y) * np[3];
;           qn += SHX(qn, 1); qn += SHX(qn, 2); qn += SHX(qn, 4); qn += SHX(qn, 8);
;           rs[r] = rs[r] + inter[r] * qn; } }
; }
; __device__ __forceinline__ void m3_pv(LAS unsigned char* L, f32x4 (&acc)[8], int w, int lane) {
;     constexpr int VT = 36864, SM = 71680; const int fr = lane & 15, fq = lane >> 4;
; #pragma unroll
;     for (int ks = 0; ks < 4; ++ks) { const bf16x8 ap = *(const LAS bf16x8*)(L + SM + (16 * w + fr) * 272 + ks * 64 + fq * 16);
; #pragma unroll
;         for (int nt = 0; nt < 8; ++nt) { const bf16x8 bv = *(const LAS bf16x8*)(L + VT + (nt * 16 + fr) * 272 + ks * 64 + fq * 16); acc[nt] = MFMA16(ap, bv, acc[nt]); } }
; }
; __device__ __forceinline__ void m3_unit(LAS unsigned char* L, int u, const bf16* z, const float* gates, const float* cw, const bf16* cprev, const float* nprev, const float* mprev, const float* normg, bf16* mix, int tid_) {
;     ...
; #pragma unroll
;     for (int nt = 0; nt < 8; ++nt)
; #pragma unroll
;         for (int ks = 0; ks < 2; ++ks) cpf[nt][ks] = *(const bf16x8*)(cprev + (((size_t)512 + u) * 128 + nt * 16 + fr) * 64 + ks * 32 + fq * 8);
;     npv = *(const f32x4*)(nprev + ((size_t)512 + u) * 64 + fr * 4);
;     m3_pv(L, acc, w, lane);
	s_nop 1
	v_add_f32_dpp v18, v18, v18 quad_perm:[1,0,3,2] row_mask:0xf bank_mask:0xf
	v_add_f32_dpp v19, v19, v19 quad_perm:[1,0,3,2] row_mask:0xf bank_mask:0xf
	s_waitcnt lgkmcnt(0)
	s_nop 1
	v_add_f32_dpp v18, v18, v18 quad_perm:[2,3,0,1] row_mask:0xf bank_mask:0xf
	v_add_f32_dpp v19, v19, v19 quad_perm:[2,3,0,1] row_mask:0xf bank_mask:0xf
	s_waitcnt lgkmcnt(0)
	s_nop 1
	v_add_f32_dpp v18, v18, v18 row_half_mirror row_mask:0xf bank_mask:0xf
	v_add_f32_dpp v19, v19, v19 row_half_mirror row_mask:0xf bank_mask:0xf
	s_waitcnt lgkmcnt(0)
	s_nop 1
	v_add_f32_dpp v178, v18, v18 row_mirror row_mask:0xf bank_mask:0xf
	v_add_f32_dpp v179, v19, v19 row_mirror row_mask:0xf bank_mask:0xf
	v_lshl_add_u64 v[18:19], v[160:161], 0, s[4:5]
	s_mov_b32 s4, 0x801000
	v_add_co_u32_e64 v20, s[54:55], s4, v160
	s_mov_b32 s4, 0x802000
	s_nop 0
	v_addc_co_u32_e64 v21, s[54:55], 0, v161, s[54:55]
	v_fmac_f32_e32 v178, v115, v179
	global_load_dwordx4 v[138:141], v[20:21], off offset:-4096
	global_load_dwordx4 v[134:137], v[18:19], off offset:64
	global_load_dwordx4 v[130:133], v[18:19], off offset:2048
	global_load_dwordx4 v[126:129], v[18:19], off offset:2112
	global_load_dwordx4 v[122:125], v[20:21], off
	global_load_dwordx4 v[118:121], v[20:21], off offset:64
	global_load_dwordx4 v[114:117], v[20:21], off offset:2048
	global_load_dwordx4 v[110:113], v[20:21], off offset:2112
	v_add_co_u32_e64 v18, s[54:55], s4, v160
	s_mov_b32 s4, 0x803000
	s_nop 0
	v_addc_co_u32_e64 v19, s[54:55], 0, v161, s[54:55]
	v_add_co_u32_e64 v20, s[54:55], s4, v160
	s_mov_b32 s4, 0x58760000
	s_nop 0
	v_addc_co_u32_e64 v21, s[54:55], 0, v161, s[54:55]
	global_load_dwordx4 v[106:109], v[20:21], off offset:-4096
	global_load_dwordx4 v[102:105], v[18:19], off offset:64
	global_load_dwordx4 v[98:101], v[18:19], off offset:2048
	global_load_dwordx4 v[94:97], v[18:19], off offset:2112
	global_load_dwordx4 v[86:89], v[20:21], off
	global_load_dwordx4 v[90:93], v[20:21], off offset:64
	global_load_dwordx4 v[78:81], v[20:21], off offset:2048
	global_load_dwordx4 v[82:85], v[20:21], off offset:2112
	v_add_co_u32_e64 v18, s[54:55], s4, v168
	v_add_u32_e32 v160, s14, v194
	s_nop 0
	v_addc_co_u32_e64 v19, s[54:55], 0, v169, s[54:55]
	global_load_dwordx4 v[74:77], v[18:19], off
	v_mul_lo_u32 v18, v190, s53
	v_add3_u32 v191, s97, v18, v158
	ds_read_b128 v[18:21], v191
	v_mad_u32_u24 v190, v162, s53, v170
	ds_read_b128 v[34:37], v190 offset:36864
	ds_read_b128 v[42:45], v190 offset:41216
	ds_read_b128 v[46:49], v190 offset:45568
	s_waitcnt lgkmcnt(1)
	v_mfma_f32_16x16x32_bf16 v[42:45], v[18:21], v[42:45], v[146:149]
	s_nop 2
	v_mad_u32_u24 v147, v187, s53, v170
	v_cmp_ge_i32_e64 s[54:55], v162, v159
	s_lshl_b32 s4, s35, 1
	s_waitcnt lgkmcnt(0)
	v_mfma_f32_16x16x32_bf16 v[46:49], v[18:21], v[46:49], v[150:153]
	s_add_u32 s8, s66, s4
	s_addc_u32 s9, s67, 0
	s_nop 0
	ds_read_b128 v[148:151], v190 offset:54272
	s_waitcnt lgkmcnt(0)
	v_mfma_f32_16x16x32_bf16 v[50:53], v[18:21], v[148:151], v[50:53]
	ds_read_b128 v[148:151], v190 offset:58624
	s_waitcnt lgkmcnt(0)
	v_mfma_f32_16x16x32_bf16 v[26:29], v[18:21], v[148:151], v[26:29]
	ds_read_b128 v[148:151], v190 offset:62976
	s_waitcnt lgkmcnt(0)
	v_mfma_f32_16x16x32_bf16 v[38:41], v[18:21], v[148:151], v[38:41]
	v_mad_u32_u24 v149, v189, s53, v170
	ds_read_b128 v[150:153], v149 offset:36864
	v_mfma_f32_16x16x32_bf16 v[34:37], v[18:21], v[34:37], v[142:145]
	s_nop 2
	ds_read_b128 v[142:145], v147 offset:36864
	s_waitcnt lgkmcnt(0)
	v_mfma_f32_16x16x32_bf16 v[142:145], v[18:21], v[142:145], v[154:157]
	v_mfma_f32_16x16x32_bf16 v[18:21], v[18:21], v[150:153], v[30:33]
	s_nop 2
	ds_read_b128 v[30:33], v191 offset:64
	ds_read_b128 v[150:153], v190 offset:36928
	s_waitcnt lgkmcnt(0)
	v_mfma_f32_16x16x32_bf16 v[34:37], v[30:33], v[150:153], v[34:37]
	ds_read_b128 v[150:153], v190 offset:41280
	s_waitcnt lgkmcnt(0)
	v_mfma_f32_16x16x32_bf16 v[42:45], v[30:33], v[150:153], v[42:45]
	ds_read_b128 v[150:153], v190 offset:45632
	s_waitcnt lgkmcnt(0)
	v_mfma_f32_16x16x32_bf16 v[46:49], v[30:33], v[150:153], v[46:49]
	ds_read_b128 v[150:153], v147 offset:36928
	s_waitcnt lgkmcnt(0)
	v_mfma_f32_16x16x32_bf16 v[142:145], v[30:33], v[150:153], v[142:145]
	ds_read_b128 v[150:153], v190 offset:54336
	s_waitcnt lgkmcnt(0)
	v_mfma_f32_16x16x32_bf16 v[50:53], v[30:33], v[150:153], v[50:53]
	ds_read_b128 v[150:153], v190 offset:58688
	s_waitcnt lgkmcnt(0)
	v_mfma_f32_16x16x32_bf16 v[26:29], v[30:33], v[150:153], v[26:29]
	ds_read_b128 v[150:153], v190 offset:63040
	s_waitcnt lgkmcnt(0)
	v_mfma_f32_16x16x32_bf16 v[38:41], v[30:33], v[150:153], v[38:41]
	ds_read_b128 v[150:153], v149 offset:36928
	s_waitcnt lgkmcnt(0)
	v_mfma_f32_16x16x32_bf16 v[18:21], v[30:33], v[150:153], v[18:21]
	ds_read_b128 v[30:33], v191 offset:128
	ds_read_b128 v[150:153], v190 offset:36992
	s_waitcnt lgkmcnt(0)
	v_mfma_f32_16x16x32_bf16 v[34:37], v[30:33], v[150:153], v[34:37]
	ds_read_b128 v[150:153], v190 offset:41344
	s_waitcnt lgkmcnt(0)
	v_mfma_f32_16x16x32_bf16 v[42:45], v[30:33], v[150:153], v[42:45]
	ds_read_b128 v[150:153], v190 offset:45696
	s_waitcnt lgkmcnt(0)
	v_mfma_f32_16x16x32_bf16 v[46:49], v[30:33], v[150:153], v[46:49]
	ds_read_b128 v[150:153], v147 offset:36992
	s_waitcnt lgkmcnt(0)
	v_mfma_f32_16x16x32_bf16 v[142:145], v[30:33], v[150:153], v[142:145]
	ds_read_b128 v[150:153], v190 offset:54400
	s_waitcnt lgkmcnt(0)
	v_mfma_f32_16x16x32_bf16 v[50:53], v[30:33], v[150:153], v[50:53]
	ds_read_b128 v[150:153], v190 offset:58752
	s_waitcnt lgkmcnt(0)
	v_mfma_f32_16x16x32_bf16 v[150:153], v[30:33], v[150:153], v[26:29]
	s_nop 2
	ds_read_b128 v[26:29], v190 offset:63104
	s_waitcnt lgkmcnt(0)
; #define LAS __attribute__((address_space(3)))
; __device__ __forceinline__ unsigned pk2(float lo, float hi) { unsigned r; asm("v_cvt_pk_bf16_f32 %0, %1, %2" : "=v"(r) : "v"(lo), "v"(hi)); return r; }
; #define LDS_FENCE() asm volatile("s_waitcnt lgkmcnt(0)" ::: "memory")
; template <int DIR>
; __device__ __forceinline__ void m3_dir(LAS unsigned char* L, const LAS float* ga, const f32x4 (&S)[8], const bf16x8 (&aq)[2], const bf16x8 (&cpf)[8][2], f32x4 npv, float mp, f32x4 (&acc)[8], float (&inter)[4], float (&mt)[4], float (&rs)[4], int w, int lane) {
;     ...
;     const LAS float* li = ga + DIR * 384; const LAS float* bb = li + 128; const LAS float* pm = li + 256;
;     float bj[4];
; #pragma unroll
;     for (int r = 0; r < 4; ++r) { const int j = 16 * w + 4 * fq + r; bj[r] = bb[j]; mt[r] = fmaxf(bj[r] + pm[j], bj[r] + mp); inter[r] = __expf(bj[r] + mp - mt[r]); rs[r] = 0.f; }
; #pragma unroll
;     for (int nt = 0; nt < 8; ++nt) { const int s = nt * 16 + fr; const float xs = li[s] - bb[s];
; #pragma unroll
;         for (int r = 0; r < 4; ++r) { const int j = 16 * w + 4 * fq + r; const bool valid = DIR ? (s >= j) : (s <= j);
;             const float pv = valid ? __expf(bj[r] + xs - mt[r]) * S[nt][r] : 0.f; rs[r] += pv; *(LAS bf16*)(L + SM + j * 272 + s * 2) = (bf16)pk2(pv, 0.f); } }
; __device__ __forceinline__ void m3_pv(LAS unsigned char* L, f32x4 (&acc)[8], int w, int lane) {
;     constexpr int VT = 36864, SM = 71680; const int fr = lane & 15, fq = lane >> 4;
; #pragma unroll
;     for (int ks = 0; ks < 4; ++ks) { const bf16x8 ap = *(const LAS bf16x8*)(L + SM + (16 * w + fr) * 272 + ks * 64 + fq * 16);
; #pragma unroll
;         for (int nt = 0; nt < 8; ++nt) { const bf16x8 bv = *(const LAS bf16x8*)(L + VT + (nt * 16 + fr) * 272 + ks * 64 + fq * 16); acc[nt] = MFMA16(ap, bv, acc[nt]); } }
; }
; __device__ __forceinline__ void m3_unit(LAS unsigned char* L, int u, const bf16* z, const float* gates, const float* cw, const bf16* cprev, const float* nprev, const float* mprev, const float* normg, bf16* mix, int tid_) {
;     ...
;     m3_pv(L, acc, w, lane);
; #pragma unroll
;     for (int nt = 0; nt < 8; ++nt)
; #pragma unroll
;         for (int r = 0; r < 4; ++r) hsum[nt][r] = acc[nt][r] * __builtin_amdgcn_rcpf(fmaxf(fabsf(den[r]), __expf(-mt[r])));
;     LDS_FENCE();
;     m3_dir<1>(L, ga, S, aq, cpf, npv, mp1, acc, inter, mt, den, w, lane);
	v_mfma_f32_16x16x32_bf16 v[154:157], v[30:33], v[26:29], v[38:41]
	ds_read_b128 v[26:29], v149 offset:36992
	s_waitcnt lgkmcnt(0)
	v_mfma_f32_16x16x32_bf16 v[200:203], v[30:33], v[26:29], v[18:21]
	ds_read_b128 v[248:251], v191 offset:192
	s_nop 1
	ds_read_b128 v[18:21], v190 offset:37056
	ds_read_b128 v[26:29], v190 offset:41408
	ds_read_b128 v[30:33], v190 offset:45760
	s_waitcnt lgkmcnt(2)
	v_mfma_f32_16x16x32_bf16 v[18:21], v[248:251], v[18:21], v[34:37]
	ds_read_b128 v[38:41], v190 offset:54464
	s_nop 1
	ds_read_b128 v[34:37], v147 offset:37056
	s_waitcnt lgkmcnt(3)
	v_mfma_f32_16x16x32_bf16 v[26:29], v[248:251], v[26:29], v[42:45]
	s_nop 2
	ds_read_b128 v[42:45], v190 offset:58816
	s_waitcnt lgkmcnt(2)
	v_mfma_f32_16x16x32_bf16 v[38:41], v[248:251], v[38:41], v[50:53]
	s_nop 2
	ds_read_b128 v[50:53], v149 offset:37056
	s_waitcnt lgkmcnt(2)
	v_mfma_f32_16x16x32_bf16 v[34:37], v[248:251], v[34:37], v[142:145]
	s_nop 2
	v_mul_f32_e32 v142, 0xbfb8aa3b, v215
	v_exp_f32_e32 v142, v142
	s_waitcnt lgkmcnt(1)
	v_mfma_f32_16x16x32_bf16 v[42:45], v[248:251], v[42:45], v[150:153]
	v_max_f32_e64 v142, |v172|, v142
	s_nop 1
	v_rcp_f32_e32 v150, v142
	v_mul_f32_e32 v142, 0xbfb8aa3b, v216
	v_exp_f32_e32 v142, v142
	v_mfma_f32_16x16x32_bf16 v[30:33], v[248:251], v[30:33], v[46:49]
	v_add_u32_e32 v151, 0x1aa00, v193
	v_max_f32_e64 v142, |v174|, v142
	v_rcp_f32_e32 v152, v142
	v_mul_f32_e32 v142, 0xbfb8aa3b, v213
	v_exp_f32_e32 v142, v142
	ds_read_b128 v[46:49], v190 offset:63168
	s_waitcnt lgkmcnt(0)
	ds_read_b128 v[172:175], v151
	v_max_f32_e64 v142, |v176|, v142
	v_rcp_f32_e32 v146, v142
	v_mul_f32_e32 v142, 0xbfb8aa3b, v212
	v_exp_f32_e32 v142, v142
	s_waitcnt lgkmcnt(1)
	v_mfma_f32_16x16x32_bf16 v[46:49], v[248:251], v[46:49], v[154:157]
	ds_read_b32 v160, v160
	v_max_f32_e64 v142, |v178|, v142
	v_rcp_f32_e32 v148, v142
	v_add_u32_e32 v142, s14, v192
	ds_read_b128 v[142:145], v142
	v_mfma_f32_16x16x32_bf16 v[50:53], v[248:251], v[50:53], v[200:203]
	s_waitcnt lgkmcnt(0)
	v_add_f32_e32 v151, v142, v172
	s_waitcnt vmcnt(17)
	v_add_f32_e32 v153, v184, v142
	v_max_f32_e32 v151, v151, v153
	v_sub_f32_e32 v153, v153, v151
	v_mul_f32_e32 v153, 0x3fb8aa3b, v153
	v_exp_f32_e32 v156, v153
	v_add_f32_e32 v153, v143, v173
	v_add_f32_e32 v154, v184, v143
	v_max_f32_e32 v153, v153, v154
	v_sub_f32_e32 v154, v154, v153
	v_mul_f32_e32 v154, 0x3fb8aa3b, v154
	v_exp_f32_e32 v157, v154
	v_add_f32_e32 v154, v144, v174
	v_add_f32_e32 v155, v184, v144
	v_max_f32_e32 v192, v154, v155
	v_sub_f32_e32 v154, v155, v192
	v_add_f32_e32 v155, v145, v175
	v_add_f32_e32 v158, v184, v145
	v_max_f32_e32 v193, v155, v158
	v_sub_f32_e32 v155, v158, v193
	v_add_u32_e32 v158, s15, v194
	ds_read_b32 v158, v158
	v_mul_f32_e32 v154, 0x3fb8aa3b, v154
	v_mul_f32_e32 v155, 0x3fb8aa3b, v155
	v_exp_f32_e32 v154, v154
	v_exp_f32_e32 v155, v155
	s_waitcnt lgkmcnt(0)
	v_sub_f32_e32 v158, v158, v160
	v_add_f32_e32 v160, v142, v158
	v_sub_f32_e32 v160, v160, v151
	v_mul_f32_e32 v160, 0x3fb8aa3b, v160
	v_exp_f32_e32 v160, v160
	s_nop 0
	v_mul_f32_e32 v70, v70, v160
	v_cndmask_b32_e64 v70, 0, v70, s[54:55]
	v_add_f32_e32 v160, 0, v70
	v_cvt_pk_bf16_f32 v70, v70, v163
	ds_write_b16 v195, v70
	v_add_f32_e32 v70, v143, v158
	v_sub_f32_e32 v70, v70, v153
	v_mul_f32_e32 v70, 0x3fb8aa3b, v70
	v_exp_f32_e32 v70, v70
	s_nop 0
	v_mul_f32_e32 v70, v71, v70
	v_cndmask_b32_e32 v70, 0, v70, vcc
	v_add_f32_e32 v71, 0, v70
	v_cvt_pk_bf16_f32 v70, v70, v163
	ds_write_b16 v204, v70
	v_add_f32_e32 v70, v144, v158
	v_sub_f32_e32 v70, v70, v192
	v_mul_f32_e32 v70, 0x3fb8aa3b, v70
	v_exp_f32_e32 v70, v70
	v_cmp_ge_i32_e32 vcc, v162, v181
	v_mul_f32_e32 v70, v72, v70
	s_nop 0
	v_cndmask_b32_e32 v70, 0, v70, vcc
	v_add_f32_e32 v72, 0, v70
	v_cvt_pk_bf16_f32 v70, v70, v163
	ds_write_b16 v205, v70
	v_add_f32_e32 v70, v145, v158
	v_sub_f32_e32 v70, v70, v193
	v_mul_f32_e32 v70, 0x3fb8aa3b, v70
	v_exp_f32_e32 v70, v70
	v_cmp_ge_i32_e32 vcc, v162, v171
	v_add_u32_e32 v158, s14, v207
	ds_read_b32 v158, v158
	v_mul_f32_e32 v70, v73, v70
	v_cndmask_b32_e32 v70, 0, v70, vcc
	v_add_f32_e32 v73, 0, v70
	v_cvt_pk_bf16_f32 v70, v70, v163
	ds_write_b16 v206, v70
	v_add_u32_e32 v70, s15, v207
	ds_read_b32 v70, v70
	v_cmp_ge_i32_e32 vcc, v186, v159
	s_waitcnt lgkmcnt(0)
	v_sub_f32_e32 v70, v70, v158
	v_add_f32_e32 v158, v142, v70
	v_sub_f32_e32 v158, v158, v151
	v_mul_f32_e32 v158, 0x3fb8aa3b, v158
	v_exp_f32_e32 v158, v158
	s_nop 0
	v_mul_f32_e32 v66, v66, v158
	v_cndmask_b32_e32 v66, 0, v66, vcc
	v_add_f32_e32 v158, v160, v66
	v_cvt_pk_bf16_f32 v66, v66, v163
	ds_write_b16 v208, v66
	v_add_f32_e32 v66, v143, v70
	v_sub_f32_e32 v66, v66, v153
	v_mul_f32_e32 v66, 0x3fb8aa3b, v66
	v_exp_f32_e32 v66, v66
	v_cmp_ge_i32_e32 vcc, v186, v181
	v_mul_f32_e32 v66, v67, v66
	v_cndmask_b32_e64 v66, 0, v66, s[38:39]
	v_add_f32_e32 v71, v71, v66
	v_cvt_pk_bf16_f32 v66, v66, v163
	ds_write_b16 v209, v66
	v_add_f32_e32 v66, v144, v70
	v_sub_f32_e32 v66, v66, v192
	v_mul_f32_e32 v66, 0x3fb8aa3b, v66
	v_exp_f32_e32 v66, v66
	v_add_u32_e32 v67, s14, v214
	ds_read_b32 v67, v67
	v_mul_f32_e32 v66, v68, v66
	v_cndmask_b32_e32 v66, 0, v66, vcc
	v_add_f32_e32 v68, v72, v66
	v_cvt_pk_bf16_f32 v66, v66, v163
	ds_write_b16 v210, v66
	v_add_f32_e32 v66, v145, v70
	v_sub_f32_e32 v66, v66, v193
	v_mul_f32_e32 v66, 0x3fb8aa3b, v66
	v_exp_f32_e32 v66, v66
	v_cmp_ge_i32_e32 vcc, v186, v171
	v_mul_f32_e32 v66, v69, v66
	s_nop 0
	v_cndmask_b32_e32 v66, 0, v66, vcc
	v_add_f32_e32 v69, v73, v66
	v_cvt_pk_bf16_f32 v66, v66, v163
	ds_write_b16 v211, v66
	v_add_u32_e32 v66, s15, v214
	ds_read_b32 v66, v66
	v_cmp_ge_i32_e32 vcc, v185, v159
	s_waitcnt lgkmcnt(0)
; #define LAS __attribute__((address_space(3)))
; __device__ __forceinline__ unsigned pk2(float lo, float hi) { unsigned r; asm("v_cvt_pk_bf16_f32 %0, %1, %2" : "=v"(r) : "v"(lo), "v"(hi)); return r; }
; #define SHX(v, m) (((m) < 32) ? __int_as_float(__builtin_amdgcn_ds_swizzle(__float_as_int(v), ((((m) & 31) << 10) | 0x1f))) : shx32(v))
; #define LDS_FENCE() asm volatile("s_waitcnt lgkmcnt(0)" ::: "memory")
; #define MFMA16(a, b, c) __builtin_amdgcn_mfma_f32_16x16x32_bf16((a), (b), (c), 0, 0, 0)
; template <int DIR>
; __device__ __forceinline__ void m3_dir(LAS unsigned char* L, const LAS float* ga, const f32x4 (&S)[8], const bf16x8 (&aq)[2], const bf16x8 (&cpf)[8][2], f32x4 npv, float mp, f32x4 (&acc)[8], float (&inter)[4], float (&mt)[4], float (&rs)[4], int w, int lane) {
;     ...
;     for (int r = 0; r < 4; ++r) { const int j = 16 * w + 4 * fq + r; bj[r] = bb[j]; mt[r] = fmaxf(bj[r] + pm[j], bj[r] + mp); inter[r] = __expf(bj[r] + mp - mt[r]); rs[r] = 0.f; }
; #pragma unroll
;     for (int nt = 0; nt < 8; ++nt) { const int s = nt * 16 + fr; const float xs = li[s] - bb[s];
; #pragma unroll
;         for (int r = 0; r < 4; ++r) { const int j = 16 * w + 4 * fq + r; const bool valid = DIR ? (s >= j) : (s <= j);
;             const float pv = valid ? __expf(bj[r] + xs - mt[r]) * S[nt][r] : 0.f; rs[r] += pv; *(LAS bf16*)(L + SM + j * 272 + s * 2) = (bf16)pk2(pv, 0.f); } }
; #pragma unroll
;     for (int r = 0; r < 4; ++r) { rs[r] += SHX(rs[r], 1); rs[r] += SHX(rs[r], 2); rs[r] += SHX(rs[r], 4); rs[r] += SHX(rs[r], 8); }
;     LDS_FENCE();
; #pragma unroll
;     for (int nt = 0; nt < 8; ++nt) { f32x4 a = {0.f, 0.f, 0.f, 0.f};
; #pragma unroll
;         for (int ks = 0; ks < 2; ++ks) a = MFMA16(aq[ks], cpf[nt][ks], a);
; #pragma unroll
;         for (int r = 0; r < 4; ++r) a[r] *= inter[r];
;         acc[nt] = a; }
	v_sub_f32_e32 v70, v66, v67
	v_add_f32_e32 v66, v142, v70
	v_sub_f32_e32 v66, v66, v151
	v_mul_f32_e32 v66, 0x3fb8aa3b, v66
	v_exp_f32_e32 v66, v66
	s_nop 0
	v_mul_f32_e32 v62, v62, v66
	v_cndmask_b32_e32 v62, 0, v62, vcc
	v_add_f32_e32 v67, v158, v62
	v_cvt_pk_bf16_f32 v62, v62, v163
	ds_write_b16 v217, v62
	v_add_f32_e32 v62, v143, v70
	v_sub_f32_e32 v62, v62, v153
	v_mul_f32_e32 v62, 0x3fb8aa3b, v62
	v_exp_f32_e32 v62, v62
	v_cmp_ge_i32_e32 vcc, v185, v181
	v_mul_f32_e32 v62, v63, v62
	v_cndmask_b32_e64 v62, 0, v62, s[40:41]
	v_add_f32_e32 v66, v71, v62
	v_cvt_pk_bf16_f32 v62, v62, v163
	ds_write_b16 v218, v62
	v_add_f32_e32 v62, v144, v70
	v_sub_f32_e32 v62, v62, v192
	v_mul_f32_e32 v62, 0x3fb8aa3b, v62
	v_exp_f32_e32 v62, v62
	s_add_u32 s40, s11, s4
	s_mov_b32 s4, 0x358637bd
	s_addc_u32 s41, s18, 0
	v_mul_f32_e32 v62, v64, v62
	v_cndmask_b32_e32 v62, 0, v62, vcc
	v_add_f32_e32 v63, v68, v62
	v_cvt_pk_bf16_f32 v62, v62, v163
	ds_write_b16 v219, v62
	v_add_f32_e32 v62, v145, v70
	v_sub_f32_e32 v62, v62, v193
	v_mul_f32_e32 v62, 0x3fb8aa3b, v62
	v_exp_f32_e32 v62, v62
	v_cmp_ge_i32_e32 vcc, v185, v171
	v_mul_f32_e32 v62, v65, v62
	s_nop 0
	v_cndmask_b32_e32 v64, 0, v62, vcc
	v_add_f32_e32 v62, v69, v64
	v_cvt_pk_bf16_f32 v64, v64, v163
	ds_write_b16 v220, v64
	v_add_u32_e32 v64, s15, v221
	v_add_u32_e32 v65, s14, v221
	ds_read_b32 v64, v64
	ds_read_b32 v65, v65
	v_cmp_ge_i32_e32 vcc, v187, v159
	s_waitcnt lgkmcnt(0)
	v_sub_f32_e32 v64, v64, v65
	v_add_f32_e32 v65, v142, v64
	v_sub_f32_e32 v65, v65, v151
	v_mul_f32_e32 v65, 0x3fb8aa3b, v65
	v_exp_f32_e32 v65, v65
	s_nop 0
	v_mul_f32_e32 v58, v58, v65
	v_cndmask_b32_e32 v58, 0, v58, vcc
	v_add_f32_e32 v65, v67, v58
	v_cvt_pk_bf16_f32 v58, v58, v163
	ds_write_b16 v223, v58
	v_add_f32_e32 v58, v143, v64
	v_sub_f32_e32 v58, v58, v153
	v_mul_f32_e32 v58, 0x3fb8aa3b, v58
	v_exp_f32_e32 v58, v58
	v_cmp_ge_i32_e32 vcc, v187, v181
	v_mul_f32_e32 v58, v59, v58
	v_cndmask_b32_e64 v58, 0, v58, s[42:43]
	v_add_f32_e32 v59, v66, v58
	v_cvt_pk_bf16_f32 v58, v58, v163
	ds_write_b16 v225, v58
	v_add_f32_e32 v58, v144, v64
	v_sub_f32_e32 v58, v58, v192
	v_mul_f32_e32 v58, 0x3fb8aa3b, v58
	v_exp_f32_e32 v58, v58
	s_waitcnt vmcnt(4)
	v_mfma_f32_16x16x32_bf16 v[66:69], v[2:5], v[86:89], 0
	v_mul_f32_e32 v58, v60, v58
	v_cndmask_b32_e32 v58, 0, v58, vcc
	v_add_f32_e32 v60, v63, v58
	v_cvt_pk_bf16_f32 v58, v58, v163
	ds_write_b16 v226, v58
	v_add_f32_e32 v58, v145, v64
	v_sub_f32_e32 v58, v58, v193
	v_mul_f32_e32 v58, 0x3fb8aa3b, v58
	v_exp_f32_e32 v58, v58
	v_cmp_ge_i32_e32 vcc, v187, v171
	s_waitcnt vmcnt(3)
	v_mfma_f32_16x16x32_bf16 v[66:69], v[6:9], v[90:93], v[66:69]
	v_mul_f32_e32 v58, v61, v58
	v_cndmask_b32_e32 v58, 0, v58, vcc
	v_add_f32_e32 v61, v62, v58
	v_cvt_pk_bf16_f32 v58, v58, v163
	ds_write_b16 v230, v58
	v_add_u32_e32 v58, s15, v224
	v_add_u32_e32 v62, s14, v224
	ds_read_b32 v58, v58
	ds_read_b32 v62, v62
	v_cmp_ge_i32_e32 vcc, v182, v159
	v_pk_mul_f32 v[68:69], v[154:155], v[68:69]
	v_pk_mul_f32 v[66:67], v[156:157], v[66:67]
	s_waitcnt lgkmcnt(0)
	v_sub_f32_e32 v58, v58, v62
	v_add_f32_e32 v62, v142, v58
	v_sub_f32_e32 v62, v62, v151
	v_mul_f32_e32 v62, 0x3fb8aa3b, v62
	v_exp_f32_e32 v62, v62
	s_nop 0
	v_mul_f32_e32 v54, v54, v62
	v_cndmask_b32_e32 v54, 0, v54, vcc
	v_add_f32_e32 v168, v65, v54
	v_cvt_pk_bf16_f32 v54, v54, v163
	ds_write_b16 v227, v54
	v_add_f32_e32 v54, v143, v58
	v_sub_f32_e32 v54, v54, v153
	v_mul_f32_e32 v54, 0x3fb8aa3b, v54
	v_exp_f32_e32 v54, v54
	v_cmp_ge_i32_e32 vcc, v182, v181
	v_mfma_f32_16x16x32_bf16 v[62:65], v[2:5], v[98:101], 0
	v_mul_f32_e32 v54, v55, v54
	v_cndmask_b32_e64 v54, 0, v54, s[44:45]
	v_add_f32_e32 v158, v59, v54
	v_cvt_pk_bf16_f32 v54, v54, v163
	ds_write_b16 v228, v54
	v_add_f32_e32 v54, v144, v58
	v_sub_f32_e32 v54, v54, v192
	v_mul_f32_e32 v54, 0x3fb8aa3b, v54
	v_exp_f32_e32 v54, v54
	v_add_u32_e32 v55, s14, v232
	ds_read_b32 v55, v55
	v_mfma_f32_16x16x32_bf16 v[62:65], v[6:9], v[94:97], v[62:65]
	v_mul_f32_e32 v54, v56, v54
	v_cndmask_b32_e32 v54, 0, v54, vcc
	v_add_f32_e32 v72, v60, v54
	v_cvt_pk_bf16_f32 v54, v54, v163
	ds_write_b16 v229, v54
	v_add_f32_e32 v54, v145, v58
	v_sub_f32_e32 v54, v54, v193
	v_mul_f32_e32 v54, 0x3fb8aa3b, v54
	v_exp_f32_e32 v54, v54
	v_cmp_ge_i32_e32 vcc, v182, v171
	v_pk_mul_f32 v[64:65], v[154:155], v[64:65]
	v_pk_mul_f32 v[62:63], v[156:157], v[62:63]
	v_mul_f32_e32 v54, v57, v54
	v_cndmask_b32_e32 v54, 0, v54, vcc
	v_add_f32_e32 v70, v61, v54
	v_cvt_pk_bf16_f32 v54, v54, v163
	ds_write_b16 v231, v54
	v_add_u32_e32 v54, s15, v232
	ds_read_b32 v54, v54
	v_cmp_ge_i32_e32 vcc, v180, v159
	v_mfma_f32_16x16x32_bf16 v[58:61], v[2:5], v[106:109], 0
	s_waitcnt lgkmcnt(0)
	v_sub_f32_e32 v54, v54, v55
	v_add_f32_e32 v55, v142, v54
	v_sub_f32_e32 v55, v55, v151
	v_mul_f32_e32 v55, 0x3fb8aa3b, v55
	v_exp_f32_e32 v55, v55
	v_mfma_f32_16x16x32_bf16 v[58:61], v[6:9], v[102:105], v[58:61]
	v_mul_f32_e32 v22, v22, v55
	v_cndmask_b32_e32 v178, 0, v22, vcc
	v_cvt_pk_bf16_f32 v22, v178, v163
	ds_write_b16 v233, v22
	v_add_f32_e32 v22, v143, v54
	v_sub_f32_e32 v22, v22, v153
	v_mul_f32_e32 v22, 0x3fb8aa3b, v22
	v_exp_f32_e32 v22, v22
	v_cmp_ge_i32_e32 vcc, v180, v181
	v_pk_mul_f32 v[60:61], v[154:155], v[60:61]
	v_pk_mul_f32 v[58:59], v[156:157], v[58:59]
	v_mul_f32_e32 v22, v23, v22
	v_cndmask_b32_e64 v172, 0, v22, s[46:47]
	v_cvt_pk_bf16_f32 v22, v172, v163
	ds_write_b16 v234, v22
	v_add_f32_e32 v22, v144, v54
	v_sub_f32_e32 v22, v22, v192
	v_mul_f32_e32 v22, 0x3fb8aa3b, v22
	v_exp_f32_e32 v22, v22
	v_add_u32_e32 v23, s14, v237
	ds_read_b32 v23, v23
	v_mul_f32_e32 v22, v24, v22
	v_cndmask_b32_e32 v170, 0, v22, vcc
	v_cvt_pk_bf16_f32 v22, v170, v163
	ds_write_b16 v235, v22
	v_add_f32_e32 v22, v145, v54
	v_sub_f32_e32 v22, v22, v193
	v_mul_f32_e32 v22, 0x3fb8aa3b, v22
	v_exp_f32_e32 v22, v22
	v_cmp_ge_i32_e32 vcc, v180, v171
	v_mfma_f32_16x16x32_bf16 v[54:57], v[2:5], v[114:117], 0
	v_mul_f32_e32 v22, v25, v22
	v_cndmask_b32_e32 v160, 0, v22, vcc
	v_cvt_pk_bf16_f32 v22, v160, v163
	ds_write_b16 v236, v22
	v_add_u32_e32 v22, s15, v237
	ds_read_b32 v22, v22
	v_cmp_ge_i32_e32 vcc, v183, v159
	v_mfma_f32_16x16x32_bf16 v[54:57], v[6:9], v[110:113], v[54:57]
	s_waitcnt lgkmcnt(0)
; #define LAS __attribute__((address_space(3)))
; __device__ __forceinline__ unsigned pk2(float lo, float hi) { unsigned r; asm("v_cvt_pk_bf16_f32 %0, %1, %2" : "=v"(r) : "v"(lo), "v"(hi)); return r; }
; __device__ __forceinline__ float bflo(unsigned w) { return __uint_as_float(w << 16); }
; __device__ __forceinline__ float bfhi(unsigned w) { return __uint_as_float(w & 0xffff0000u); }
; #define SHX(v, m) (((m) < 32) ? __int_as_float(__builtin_amdgcn_ds_swizzle(__float_as_int(v), ((((m) & 31) << 10) | 0x1f))) : shx32(v))
; #define LDS_FENCE() asm volatile("s_waitcnt lgkmcnt(0)" ::: "memory")
; #define MFMA16(a, b, c) __builtin_amdgcn_mfma_f32_16x16x32_bf16((a), (b), (c), 0, 0, 0)
; template <int DIR>
; __device__ __forceinline__ void m3_dir(LAS unsigned char* L, const LAS float* ga, const f32x4 (&S)[8], const bf16x8 (&aq)[2], const bf16x8 (&cpf)[8][2], f32x4 npv, float mp, f32x4 (&acc)[8], float (&inter)[4], float (&mt)[4], float (&rs)[4], int w, int lane) {
;     ...
;     for (int nt = 0; nt < 8; ++nt) { const int s = nt * 16 + fr; const float xs = li[s] - bb[s];
; #pragma unroll
;         for (int r = 0; r < 4; ++r) { const int j = 16 * w + 4 * fq + r; const bool valid = DIR ? (s >= j) : (s <= j);
;             const float pv = valid ? __expf(bj[r] + xs - mt[r]) * S[nt][r] : 0.f; rs[r] += pv; *(LAS bf16*)(L + SM + j * 272 + s * 2) = (bf16)pk2(pv, 0.f); } }
; #pragma unroll
;     for (int r = 0; r < 4; ++r) { rs[r] += SHX(rs[r], 1); rs[r] += SHX(rs[r], 2); rs[r] += SHX(rs[r], 4); rs[r] += SHX(rs[r], 8); }
;     LDS_FENCE();
; #pragma unroll
;     for (int nt = 0; nt < 8; ++nt) { f32x4 a = {0.f, 0.f, 0.f, 0.f};
; #pragma unroll
;         for (int ks = 0; ks < 2; ++ks) a = MFMA16(aq[ks], cpf[nt][ks], a);
; #pragma unroll
;         for (int r = 0; r < 4; ++r) a[r] *= inter[r];
;         acc[nt] = a; }
;     { const f32x4 np = npv;
; #pragma unroll
;       for (int r = 0; r < 4; ++r) { const int j = 16 * w + 4 * fq + r; const v2u qw = *(const LAS v2u*)(L + QS + j * 144 + fr * 8);
;           float qn = bflo(qw.x) * np[0] + bfhi(qw.x) * np[1] + bflo(qw.y) * np[2] + bfhi(qw.y) * np[3];
;           qn += SHX(qn, 1); qn += SHX(qn, 2); qn += SHX(qn, 4); qn += SHX(qn, 8);
;           rs[r] = rs[r] + inter[r] * qn; } }
	v_sub_f32_e32 v22, v22, v23
	v_add_f32_e32 v23, v142, v22
	v_sub_f32_e32 v23, v23, v151
	v_mul_f32_e32 v23, 0x3fb8aa3b, v23
	v_exp_f32_e32 v23, v23
	s_nop 1
	v_pk_mul_f32 v[56:57], v[154:155], v[56:57]
	v_pk_mul_f32 v[54:55], v[156:157], v[54:55]
	v_mul_f32_e32 v14, v14, v23
	v_cndmask_b32_e32 v182, 0, v14, vcc
	v_cvt_pk_bf16_f32 v14, v182, v163
	ds_write_b16 v238, v14
	v_add_f32_e32 v14, v143, v22
	v_sub_f32_e32 v14, v14, v153
	v_mul_f32_e32 v14, 0x3fb8aa3b, v14
	v_exp_f32_e32 v14, v14
	v_cmp_ge_i32_e32 vcc, v183, v181
	v_mul_f32_e32 v14, v15, v14
	v_cndmask_b32_e64 v180, 0, v14, s[48:49]
	v_cvt_pk_bf16_f32 v14, v180, v163
	ds_write_b16 v239, v14
	v_add_f32_e32 v14, v144, v22
	v_sub_f32_e32 v14, v14, v192
	v_mul_f32_e32 v14, 0x3fb8aa3b, v14
	v_exp_f32_e32 v14, v14
	v_add_u32_e32 v15, s14, v242
	ds_read_b32 v15, v15
	v_mul_f32_e32 v14, v16, v14
	v_cndmask_b32_e32 v176, 0, v14, vcc
	v_cvt_pk_bf16_f32 v14, v176, v163
	ds_write_b16 v240, v14
	v_add_f32_e32 v14, v145, v22
	v_sub_f32_e32 v14, v14, v193
	v_mul_f32_e32 v14, 0x3fb8aa3b, v14
	v_exp_f32_e32 v14, v14
	v_cmp_ge_i32_e32 vcc, v183, v171
	v_mfma_f32_16x16x32_bf16 v[22:25], v[2:5], v[122:125], 0
	v_mul_f32_e32 v14, v17, v14
	v_cndmask_b32_e32 v174, 0, v14, vcc
	v_cvt_pk_bf16_f32 v14, v174, v163
	ds_write_b16 v241, v14
	v_add_u32_e32 v14, s15, v242
	ds_read_b32 v14, v14
	v_cmp_ge_i32_e32 vcc, v189, v159
	v_mfma_f32_16x16x32_bf16 v[22:25], v[6:9], v[118:121], v[22:25]
	s_waitcnt lgkmcnt(0)
	v_sub_f32_e32 v14, v14, v15
	v_add_f32_e32 v15, v142, v14
	v_sub_f32_e32 v15, v15, v151
	v_mul_f32_e32 v15, 0x3fb8aa3b, v15
	v_exp_f32_e32 v15, v15
	s_nop 1
	v_pk_mul_f32 v[24:25], v[154:155], v[24:25]
	v_pk_mul_f32 v[22:23], v[156:157], v[22:23]
	v_mul_f32_e32 v10, v10, v15
	v_cndmask_b32_e32 v186, 0, v10, vcc
	v_cvt_pk_bf16_f32 v10, v186, v163
	ds_write_b16 v243, v10
	v_add_f32_e32 v10, v143, v14
	v_sub_f32_e32 v10, v10, v153
	v_mul_f32_e32 v10, 0x3fb8aa3b, v10
	v_exp_f32_e32 v10, v10
	v_cmp_ge_i32_e32 vcc, v189, v181
	v_mul_f32_e32 v10, v11, v10
	v_cndmask_b32_e64 v184, 0, v10, s[50:51]
	v_cvt_pk_bf16_f32 v10, v184, v163
	ds_write_b16 v244, v10
	v_add_f32_e32 v10, v144, v14
	v_sub_f32_e32 v10, v10, v192
	v_mul_f32_e32 v10, 0x3fb8aa3b, v10
	v_exp_f32_e32 v10, v10
	s_nop 0
	v_mul_f32_e32 v10, v12, v10
	v_cndmask_b32_e32 v144, 0, v10, vcc
	v_cvt_pk_bf16_f32 v10, v144, v163
	ds_write_b16 v245, v10
	v_add_f32_e32 v10, v145, v14
	v_sub_f32_e32 v10, v10, v193
	v_mul_f32_e32 v10, 0x3fb8aa3b, v10
	v_exp_f32_e32 v10, v10
	v_cmp_ge_i32_e32 vcc, v189, v171
	v_mfma_f32_16x16x32_bf16 v[14:17], v[2:5], v[130:133], 0
	v_mul_f32_e32 v10, v13, v10
	v_cndmask_b32_e32 v142, 0, v10, vcc
	v_cvt_pk_bf16_f32 v10, v142, v163
	ds_write_b16 v246, v10
	v_mfma_f32_16x16x32_bf16 v[10:13], v[2:5], v[138:141], 0
	s_waitcnt lgkmcnt(0)
	s_waitcnt vmcnt(2)
	v_mfma_f32_16x16x32_bf16 v[2:5], v[2:5], v[78:81], 0
	v_mfma_f32_16x16x32_bf16 v[10:13], v[6:9], v[134:137], v[10:13]
	v_mfma_f32_16x16x32_bf16 v[14:17], v[6:9], v[126:129], v[14:17]
	s_waitcnt vmcnt(1)
	v_mfma_f32_16x16x32_bf16 v[2:5], v[6:9], v[82:85], v[2:5]
	ds_read2_b64 v[6:9], v222 offset1:18
	s_nop 3
	v_pk_mul_f32 v[12:13], v[154:155], v[12:13]
	v_pk_mul_f32 v[10:11], v[156:157], v[10:11]
	v_pk_mul_f32 v[16:17], v[154:155], v[16:17]
	v_pk_mul_f32 v[14:15], v[156:157], v[14:15]
	s_waitcnt lgkmcnt(0)
	v_lshlrev_b32_e32 v71, 16, v6
	v_and_b32_e32 v6, 0xffff0000, v6
	s_waitcnt vmcnt(0)
	v_mul_f32_e32 v179, v75, v6
	v_lshlrev_b32_e32 v6, 16, v7
	v_mul_f32_e32 v169, v74, v71
	v_mul_f32_e32 v183, v76, v6
	v_and_b32_e32 v6, 0xffff0000, v7
	v_mul_f32_e32 v187, v77, v6
	v_pk_add_f32 v[6:7], v[168:169], v[178:179]
	v_pk_mul_f32 v[4:5], v[154:155], v[4:5]
	v_pk_add_f32 v[6:7], v[6:7], v[182:183]
	v_pk_mul_f32 v[2:3], v[156:157], v[2:3]
	v_pk_add_f32 v[6:7], v[6:7], v[186:187]
	s_waitcnt lgkmcnt(0)
	s_nop 1
	v_add_f32_dpp v6, v6, v6 quad_perm:[1,0,3,2] row_mask:0xf bank_mask:0xf
	v_add_f32_dpp v7, v7, v7 quad_perm:[1,0,3,2] row_mask:0xf bank_mask:0xf
	s_waitcnt lgkmcnt(0)
	s_nop 1
	v_add_f32_dpp v6, v6, v6 quad_perm:[2,3,0,1] row_mask:0xf bank_mask:0xf
	v_add_f32_dpp v7, v7, v7 quad_perm:[2,3,0,1] row_mask:0xf bank_mask:0xf
	s_waitcnt lgkmcnt(0)
	s_nop 1
	v_add_f32_dpp v6, v6, v6 row_half_mirror row_mask:0xf bank_mask:0xf
	v_add_f32_dpp v7, v7, v7 row_half_mirror row_mask:0xf bank_mask:0xf
	s_waitcnt lgkmcnt(0)
	s_nop 1
	v_add_f32_dpp v88, v6, v6 row_mirror row_mask:0xf bank_mask:0xf
	v_add_f32_dpp v89, v7, v7 row_mirror row_mask:0xf bank_mask:0xf
	v_lshlrev_b32_e32 v6, 16, v8
	v_mul_f32_e32 v159, v74, v6
	v_and_b32_e32 v6, 0xffff0000, v8
	v_mul_f32_e32 v173, v75, v6
	v_lshlrev_b32_e32 v6, 16, v9
	v_mul_f32_e32 v181, v76, v6
	v_and_b32_e32 v6, 0xffff0000, v9
	v_mul_f32_e32 v185, v77, v6
	v_pk_add_f32 v[6:7], v[158:159], v[172:173]
	v_fmac_f32_e32 v88, v156, v89
	v_pk_add_f32 v[6:7], v[6:7], v[180:181]
	s_nop 0
	v_pk_add_f32 v[6:7], v[6:7], v[184:185]
	s_waitcnt lgkmcnt(0)
	s_nop 1
	v_add_f32_dpp v6, v6, v6 quad_perm:[1,0,3,2] row_mask:0xf bank_mask:0xf
	v_add_f32_dpp v7, v7, v7 quad_perm:[1,0,3,2] row_mask:0xf bank_mask:0xf
	s_waitcnt lgkmcnt(0)
	s_nop 1
	v_add_f32_dpp v6, v6, v6 quad_perm:[2,3,0,1] row_mask:0xf bank_mask:0xf
	v_add_f32_dpp v7, v7, v7 quad_perm:[2,3,0,1] row_mask:0xf bank_mask:0xf
	s_waitcnt lgkmcnt(0)
	s_nop 1
	v_add_f32_dpp v6, v6, v6 row_half_mirror row_mask:0xf bank_mask:0xf
	v_add_f32_dpp v7, v7, v7 row_half_mirror row_mask:0xf bank_mask:0xf
	s_waitcnt lgkmcnt(0)
	s_nop 1
	v_add_f32_dpp v90, v6, v6 row_mirror row_mask:0xf bank_mask:0xf
	v_add_f32_dpp v91, v7, v7 row_mirror row_mask:0xf bank_mask:0xf
	ds_read2_b64 v[6:9], v222 offset0:36 offset1:54
	v_fmac_f32_e32 v90, v157, v91
	s_waitcnt lgkmcnt(0)
; #define LAS __attribute__((address_space(3)))
; __device__ __forceinline__ float bflo(unsigned w) { return __uint_as_float(w << 16); }
; __device__ __forceinline__ float bfhi(unsigned w) { return __uint_as_float(w & 0xffff0000u); }
; #define SHX(v, m) (((m) < 32) ? __int_as_float(__builtin_amdgcn_ds_swizzle(__float_as_int(v), ((((m) & 31) << 10) | 0x1f))) : shx32(v))
; #define MFMA16(a, b, c) __builtin_amdgcn_mfma_f32_16x16x32_bf16((a), (b), (c), 0, 0, 0)
; template <int DIR>
; __device__ __forceinline__ void m3_dir(LAS unsigned char* L, const LAS float* ga, const f32x4 (&S)[8], const bf16x8 (&aq)[2], const bf16x8 (&cpf)[8][2], f32x4 npv, float mp, f32x4 (&acc)[8], float (&inter)[4], float (&mt)[4], float (&rs)[4], int w, int lane) {
;     ...
;     { const f32x4 np = npv;
; #pragma unroll
;       for (int r = 0; r < 4; ++r) { const int j = 16 * w + 4 * fq + r; const v2u qw = *(const LAS v2u*)(L + QS + j * 144 + fr * 8);
;           float qn = bflo(qw.x) * np[0] + bfhi(qw.x) * np[1] + bflo(qw.y) * np[2] + bfhi(qw.y) * np[3];
;           qn += SHX(qn, 1); qn += SHX(qn, 2); qn += SHX(qn, 4); qn += SHX(qn, 8);
;           rs[r] = rs[r] + inter[r] * qn; } }
; }
; __device__ __forceinline__ void m3_pv(LAS unsigned char* L, f32x4 (&acc)[8], int w, int lane) {
;     constexpr int VT = 36864, SM = 71680; const int fr = lane & 15, fq = lane >> 4;
; #pragma unroll
;     for (int ks = 0; ks < 4; ++ks) { const bf16x8 ap = *(const LAS bf16x8*)(L + SM + (16 * w + fr) * 272 + ks * 64 + fq * 16);
; #pragma unroll
;         for (int nt = 0; nt < 8; ++nt) { const bf16x8 bv = *(const LAS bf16x8*)(L + VT + (nt * 16 + fr) * 272 + ks * 64 + fq * 16); acc[nt] = MFMA16(ap, bv, acc[nt]); } }
; }
; __device__ __forceinline__ void m3_unit(LAS unsigned char* L, int u, const bf16* z, const float* gates, const float* cw, const bf16* cprev, const float* nprev, const float* mprev, const float* normg, bf16* mix, int tid_) {
;     ...
;     unsigned short zo[4][8];
; #pragma unroll
;     for (int r = 0; r < 4; ++r)
; #pragma unroll
;         for (int nt = 0; nt < 8; ++nt) zo[r][nt] = z[(size_t)(t0 + 16 * w + 4 * fq + r) * 2048 + 1536 + hh * 128 + nt * 16 + fr];
;     m3_pv(L, acc, w, lane);
	v_lshlrev_b32_e32 v71, 16, v6
	v_and_b32_e32 v6, 0xffff0000, v6
	v_mul_f32_e32 v171, v75, v6
	v_lshlrev_b32_e32 v6, 16, v7
	v_mul_f32_e32 v73, v74, v71
	v_mul_f32_e32 v177, v76, v6
	v_and_b32_e32 v6, 0xffff0000, v7
	v_mul_f32_e32 v145, v77, v6
	v_pk_add_f32 v[6:7], v[72:73], v[170:171]
	s_nop 0
	v_pk_add_f32 v[6:7], v[6:7], v[176:177]
	s_nop 0
	v_pk_add_f32 v[6:7], v[6:7], v[144:145]
	s_waitcnt lgkmcnt(0)
	s_nop 1
	v_add_f32_dpp v6, v6, v6 quad_perm:[1,0,3,2] row_mask:0xf bank_mask:0xf
	v_add_f32_dpp v7, v7, v7 quad_perm:[1,0,3,2] row_mask:0xf bank_mask:0xf
	s_waitcnt lgkmcnt(0)
	s_nop 1
	v_add_f32_dpp v6, v6, v6 quad_perm:[2,3,0,1] row_mask:0xf bank_mask:0xf
	v_add_f32_dpp v7, v7, v7 quad_perm:[2,3,0,1] row_mask:0xf bank_mask:0xf
	s_waitcnt lgkmcnt(0)
	s_nop 1
	v_add_f32_dpp v6, v6, v6 row_half_mirror row_mask:0xf bank_mask:0xf
	v_add_f32_dpp v7, v7, v7 row_half_mirror row_mask:0xf bank_mask:0xf
	s_waitcnt lgkmcnt(0)
	s_nop 1
	v_add_f32_dpp v92, v6, v6 row_mirror row_mask:0xf bank_mask:0xf
	v_add_f32_dpp v93, v7, v7 row_mirror row_mask:0xf bank_mask:0xf
	v_lshlrev_b32_e32 v6, 16, v8
	v_mul_f32_e32 v71, v74, v6
	v_and_b32_e32 v6, 0xffff0000, v8
	v_mul_f32_e32 v161, v75, v6
	v_lshlrev_b32_e32 v6, 16, v9
	v_mul_f32_e32 v175, v76, v6
	v_and_b32_e32 v6, 0xffff0000, v9
	v_mul_f32_e32 v143, v77, v6
	v_pk_add_f32 v[6:7], v[70:71], v[160:161]
	v_lshlrev_b32_e32 v70, 1, v162
	v_pk_add_f32 v[6:7], v[6:7], v[174:175]
	v_mov_b32_e32 v71, v163
	v_pk_add_f32 v[6:7], v[6:7], v[142:143]
	v_fmac_f32_e32 v92, v154, v93
	s_waitcnt lgkmcnt(0)
	s_nop 1
	v_add_f32_dpp v6, v6, v6 quad_perm:[1,0,3,2] row_mask:0xf bank_mask:0xf
	v_add_f32_dpp v7, v7, v7 quad_perm:[1,0,3,2] row_mask:0xf bank_mask:0xf
	s_waitcnt lgkmcnt(0)
	s_nop 1
	v_add_f32_dpp v6, v6, v6 quad_perm:[2,3,0,1] row_mask:0xf bank_mask:0xf
	v_add_f32_dpp v7, v7, v7 quad_perm:[2,3,0,1] row_mask:0xf bank_mask:0xf
	s_waitcnt lgkmcnt(0)
	s_nop 1
	v_add_f32_dpp v6, v6, v6 row_half_mirror row_mask:0xf bank_mask:0xf
	v_add_f32_dpp v7, v7, v7 row_half_mirror row_mask:0xf bank_mask:0xf
	s_waitcnt lgkmcnt(0)
	s_nop 1
	v_add_f32_dpp v94, v6, v6 row_mirror row_mask:0xf bank_mask:0xf
	v_add_f32_dpp v95, v7, v7 row_mirror row_mask:0xf bank_mask:0xf
	v_add_u32_e32 v6, s60, v188
	v_lshl_or_b32 v78, v1, 2, v6
	v_ashrrev_i32_e32 v79, 31, v78
	v_or_b32_e32 v76, 1, v78
	v_lshl_add_u64 v[6:7], s[8:9], 0, v[70:71]
	v_lshlrev_b64 v[8:9], 12, v[78:79]
	v_ashrrev_i32_e32 v77, 31, v76
	v_or_b32_e32 v74, 2, v78
	v_lshl_add_u64 v[86:87], v[6:7], 0, v[8:9]
	v_lshlrev_b64 v[8:9], 12, v[76:77]
	v_ashrrev_i32_e32 v75, 31, v74
	v_or_b32_e32 v72, 3, v78
	v_lshl_add_u64 v[84:85], v[6:7], 0, v[8:9]
	v_lshlrev_b64 v[8:9], 12, v[74:75]
	v_ashrrev_i32_e32 v73, 31, v72
	v_lshl_add_u64 v[82:83], v[6:7], 0, v[8:9]
	v_lshlrev_b64 v[8:9], 12, v[72:73]
	v_lshl_add_u64 v[80:81], v[6:7], 0, v[8:9]
	ds_read_b128 v[6:9], v191
	ds_read_b128 v[96:99], v190 offset:36864
	s_waitcnt lgkmcnt(0)
	v_mfma_f32_16x16x32_bf16 v[10:13], v[6:9], v[96:99], v[10:13]
	ds_read_b128 v[96:99], v190 offset:41216
	v_mul_f32_e32 v1, 0xbfb8aa3b, v151
	v_exp_f32_e32 v1, v1
	s_waitcnt lgkmcnt(0)
	v_mfma_f32_16x16x32_bf16 v[14:17], v[6:9], v[96:99], v[14:17]
	ds_read_b128 v[96:99], v190 offset:45568
	v_max_f32_e64 v1, |v88|, v1
	v_rcp_f32_e32 v88, v1
	s_waitcnt lgkmcnt(0)
	v_mfma_f32_16x16x32_bf16 v[22:25], v[6:9], v[96:99], v[22:25]
	ds_read_b128 v[96:99], v147 offset:36864
	v_mul_f32_e32 v1, 0xbfb8aa3b, v153
	v_exp_f32_e32 v1, v1
	s_waitcnt lgkmcnt(0)
	v_mfma_f32_16x16x32_bf16 v[54:57], v[6:9], v[96:99], v[54:57]
	ds_read_b128 v[96:99], v190 offset:54272
	v_max_f32_e64 v1, |v90|, v1
	v_rcp_f32_e32 v90, v1
	s_waitcnt lgkmcnt(0)
	v_mfma_f32_16x16x32_bf16 v[58:61], v[6:9], v[96:99], v[58:61]
	ds_read_b128 v[96:99], v190 offset:58624
	v_mul_f32_e32 v1, 0xbfb8aa3b, v192
	v_exp_f32_e32 v1, v1
	s_waitcnt lgkmcnt(0)
	v_mfma_f32_16x16x32_bf16 v[62:65], v[6:9], v[96:99], v[62:65]
	ds_read_b128 v[96:99], v190 offset:62976
	v_max_f32_e64 v1, |v92|, v1
	v_fmac_f32_e32 v94, v155, v95
	s_waitcnt lgkmcnt(0)
	v_mfma_f32_16x16x32_bf16 v[66:69], v[6:9], v[96:99], v[66:69]
	ds_read_b128 v[96:99], v149 offset:36864
	s_brev_b32 s8, 60
	v_lshlrev_b64 v[78:79], 11, v[78:79]
	s_waitcnt lgkmcnt(0)
	v_mfma_f32_16x16x32_bf16 v[2:5], v[6:9], v[96:99], v[2:5]
	ds_read_b128 v[6:9], v191 offset:64
	ds_read_b128 v[96:99], v190 offset:36928
	v_lshl_add_u64 v[78:79], s[40:41], 0, v[78:79]
	v_lshl_add_u64 v[78:79], v[78:79], 0, v[70:71]
	s_waitcnt lgkmcnt(0)
	v_mfma_f32_16x16x32_bf16 v[10:13], v[6:9], v[96:99], v[10:13]
	ds_read_b128 v[96:99], v190 offset:41280
	s_waitcnt lgkmcnt(0)
	v_mfma_f32_16x16x32_bf16 v[14:17], v[6:9], v[96:99], v[14:17]
	ds_read_b128 v[96:99], v190 offset:45632
	s_waitcnt lgkmcnt(0)
	v_mfma_f32_16x16x32_bf16 v[22:25], v[6:9], v[96:99], v[22:25]
	ds_read_b128 v[96:99], v147 offset:36928
	s_waitcnt lgkmcnt(0)
	v_mfma_f32_16x16x32_bf16 v[54:57], v[6:9], v[96:99], v[54:57]
	ds_read_b128 v[96:99], v190 offset:54336
	s_waitcnt lgkmcnt(0)
	v_mfma_f32_16x16x32_bf16 v[58:61], v[6:9], v[96:99], v[58:61]
	ds_read_b128 v[96:99], v190 offset:58688
	s_waitcnt lgkmcnt(0)
	v_mfma_f32_16x16x32_bf16 v[62:65], v[6:9], v[96:99], v[62:65]
	ds_read_b128 v[96:99], v190 offset:63040
	s_waitcnt lgkmcnt(0)
	v_mfma_f32_16x16x32_bf16 v[66:69], v[6:9], v[96:99], v[66:69]
	ds_read_b128 v[96:99], v149 offset:36928
	s_waitcnt lgkmcnt(0)
	v_mfma_f32_16x16x32_bf16 v[2:5], v[6:9], v[96:99], v[2:5]
	ds_read_b128 v[6:9], v191 offset:128
	ds_read_b128 v[96:99], v190 offset:36992
	s_waitcnt lgkmcnt(0)
	v_mfma_f32_16x16x32_bf16 v[10:13], v[6:9], v[96:99], v[10:13]
	ds_read_b128 v[96:99], v190 offset:41344
	s_waitcnt lgkmcnt(0)
; #define LAS __attribute__((address_space(3)))
; #define MFMA16(a, b, c) __builtin_amdgcn_mfma_f32_16x16x32_bf16((a), (b), (c), 0, 0, 0)
; __device__ __forceinline__ void m3_pv(LAS unsigned char* L, f32x4 (&acc)[8], int w, int lane) {
;     constexpr int VT = 36864, SM = 71680; const int fr = lane & 15, fq = lane >> 4;
; #pragma unroll
;     for (int ks = 0; ks < 4; ++ks) { const bf16x8 ap = *(const LAS bf16x8*)(L + SM + (16 * w + fr) * 272 + ks * 64 + fq * 16);
; #pragma unroll
;         for (int nt = 0; nt < 8; ++nt) { const bf16x8 bv = *(const LAS bf16x8*)(L + VT + (nt * 16 + fr) * 272 + ks * 64 + fq * 16); acc[nt] = MFMA16(ap, bv, acc[nt]); } }
; }
; __device__ __forceinline__ void m3_unit(LAS unsigned char* L, int u, const bf16* z, const float* gates, const float* cw, const bf16* cprev, const float* nprev, const float* mprev, const float* normg, bf16* mix, int tid_) {
;     ...
;     unsigned short zo[4][8];
; #pragma unroll
;     for (int r = 0; r < 4; ++r)
; #pragma unroll
;         for (int nt = 0; nt < 8; ++nt) zo[r][nt] = z[(size_t)(t0 + 16 * w + 4 * fq + r) * 2048 + 1536 + hh * 128 + nt * 16 + fr];
;     m3_pv(L, acc, w, lane);
; #pragma unroll
;     for (int nt = 0; nt < 8; ++nt)
; #pragma unroll
;         for (int r = 0; r < 4; ++r) hsum[nt][r] += acc[nt][r] * __builtin_amdgcn_rcpf(fmaxf(fabsf(den[r]), __expf(-mt[r])));
	v_mfma_f32_16x16x32_bf16 v[14:17], v[6:9], v[96:99], v[14:17]
	ds_read_b128 v[96:99], v190 offset:45696
	s_waitcnt lgkmcnt(0)
	v_mfma_f32_16x16x32_bf16 v[22:25], v[6:9], v[96:99], v[22:25]
	ds_read_b128 v[96:99], v147 offset:36992
	s_waitcnt lgkmcnt(0)
	v_mfma_f32_16x16x32_bf16 v[54:57], v[6:9], v[96:99], v[54:57]
	ds_read_b128 v[96:99], v190 offset:54400
	s_waitcnt lgkmcnt(0)
	v_mfma_f32_16x16x32_bf16 v[58:61], v[6:9], v[96:99], v[58:61]
	ds_read_b128 v[96:99], v190 offset:58752
	s_waitcnt lgkmcnt(0)
	v_mfma_f32_16x16x32_bf16 v[62:65], v[6:9], v[96:99], v[62:65]
	ds_read_b128 v[96:99], v190 offset:63104
	s_waitcnt lgkmcnt(0)
	v_mfma_f32_16x16x32_bf16 v[66:69], v[6:9], v[96:99], v[66:69]
	ds_read_b128 v[96:99], v149 offset:36992
	s_waitcnt lgkmcnt(0)
	v_mfma_f32_16x16x32_bf16 v[96:99], v[6:9], v[96:99], v[2:5]
	ds_read_b128 v[100:103], v191 offset:192
	s_nop 1
	ds_read_b128 v[2:5], v190 offset:37056
	s_waitcnt lgkmcnt(0)
	v_mfma_f32_16x16x32_bf16 v[6:9], v[100:103], v[2:5], v[10:13]
	ds_read_b128 v[2:5], v190 offset:41408
	s_nop 1
	ds_read_b128 v[10:13], v190 offset:45760
	s_waitcnt lgkmcnt(1)
	v_mfma_f32_16x16x32_bf16 v[2:5], v[100:103], v[2:5], v[14:17]
	s_nop 2
	ds_read_b128 v[14:17], v147 offset:37056
	s_waitcnt lgkmcnt(1)
	v_mfma_f32_16x16x32_bf16 v[10:13], v[100:103], v[10:13], v[22:25]
	s_waitcnt lgkmcnt(0)
	v_mfma_f32_16x16x32_bf16 v[14:17], v[100:103], v[14:17], v[54:57]
	s_nop 0
	ds_read_b128 v[22:25], v190 offset:54464
	s_nop 0
	ds_read_b128 v[54:57], v190 offset:58816
	s_waitcnt lgkmcnt(0)
	v_mfma_f32_16x16x32_bf16 v[54:57], v[100:103], v[54:57], v[62:65]
	s_nop 2
	ds_read_b128 v[62:65], v149 offset:37056
	v_mfma_f32_16x16x32_bf16 v[22:25], v[100:103], v[22:25], v[58:61]
	s_nop 2
	ds_read_b128 v[58:61], v190 offset:63168
	s_waitcnt lgkmcnt(0)
	v_mfma_f32_16x16x32_bf16 v[58:61], v[100:103], v[58:61], v[66:69]
	s_nop 2
	v_rcp_f32_e32 v66, v1
	v_mul_f32_e32 v1, 0xbfb8aa3b, v193
	v_exp_f32_e32 v1, v1
	v_mfma_f32_16x16x32_bf16 v[62:65], v[100:103], v[62:65], v[96:99]
	v_mov_b32_e32 v101, v10
	v_mov_b32_e32 v100, v14
	v_max_f32_e64 v1, |v94|, v1
	v_rcp_f32_e32 v68, v1
	global_load_ushort v1, v[86:87], off offset:3072
	global_load_ushort v69, v[86:87], off offset:3104
	global_load_ushort v89, v[86:87], off offset:3136
	global_load_ushort v91, v[86:87], off offset:3168
	global_load_ushort v92, v[86:87], off offset:3200
	global_load_ushort v93, v[86:87], off offset:3232
	global_load_ushort v94, v[86:87], off offset:3264
	global_load_ushort v95, v[86:87], off offset:3296
	global_load_ushort v106, v[84:85], off offset:3072
	global_load_ushort v107, v[84:85], off offset:3104
	global_load_ushort v127, v[84:85], off offset:3136
	global_load_ushort v128, v[84:85], off offset:3168
	global_load_ushort v129, v[84:85], off offset:3200
	global_load_ushort v130, v[84:85], off offset:3232
	global_load_ushort v131, v[84:85], off offset:3264
	global_load_ushort v132, v[84:85], off offset:3296
	global_load_ushort v126, v[82:83], off offset:3072
	global_load_ushort v125, v[82:83], off offset:3104
	global_load_ushort v124, v[82:83], off offset:3136
	global_load_ushort v123, v[82:83], off offset:3168
	global_load_ushort v122, v[82:83], off offset:3200
	global_load_ushort v121, v[82:83], off offset:3232
	global_load_ushort v120, v[82:83], off offset:3264
	global_load_ushort v119, v[82:83], off offset:3296
	global_load_ushort v118, v[80:81], off offset:3072
	global_load_ushort v117, v[80:81], off offset:3104
	global_load_ushort v116, v[80:81], off offset:3136
	global_load_ushort v115, v[80:81], off offset:3168
	global_load_ushort v114, v[80:81], off offset:3200
	global_load_ushort v113, v[80:81], off offset:3232
	global_load_ushort v112, v[80:81], off offset:3264
	global_load_ushort v67, v[80:81], off offset:3296
	s_barrier
	v_mov_b32_e32 v96, v62
	v_mov_b32_e32 v98, v54
	v_mov_b32_e32 v97, v58
	v_mov_b32_e32 v99, v22
	v_mov_b32_e32 v22, v55
	v_mov_b32_e32 v58, v63
	s_waitcnt vmcnt(31)
	v_lshlrev_b32_e32 v1, 16, v1
	v_mul_f32_e32 v1, 0xbfb8aa3b, v1
	v_exp_f32_e32 v1, v1
	s_waitcnt vmcnt(29)
	v_pk_mul_f32 v[96:97], v[88:89], v[96:97] op_sel_hi:[0,1]
	v_pk_mul_f32 v[98:99], v[88:89], v[98:99] op_sel_hi:[0,1]
	v_pk_mul_f32 v[100:101], v[88:89], v[100:101] op_sel_hi:[0,1]
	v_add_f32_e32 v1, 1.0, v1
	v_rcp_f32_e32 v80, v1
	v_lshlrev_b32_e32 v1, 16, v69
	v_mul_f32_e32 v1, 0xbfb8aa3b, v1
	v_exp_f32_e32 v1, v1
	s_waitcnt vmcnt(23)
	v_lshlrev_b32_e32 v10, 16, v106
	v_mul_f32_e32 v10, 0xbfb8aa3b, v10
	v_exp_f32_e32 v10, v10
	v_add_f32_e32 v1, 1.0, v1
	v_rcp_f32_e32 v82, v1
	v_lshlrev_b32_e32 v1, 16, v89
	v_mul_f32_e32 v1, 0xbfb8aa3b, v1
	v_exp_f32_e32 v1, v1
	v_add_f32_e32 v10, 1.0, v10
	v_rcp_f32_e32 v81, v10
	s_waitcnt vmcnt(22)
	v_lshlrev_b32_e32 v10, 16, v107
	v_add_f32_e32 v1, 1.0, v1
	v_rcp_f32_e32 v85, v1
	v_lshlrev_b32_e32 v1, 16, v91
	v_mul_f32_e32 v1, 0xbfb8aa3b, v1
	v_exp_f32_e32 v1, v1
	v_mul_f32_e32 v10, 0xbfb8aa3b, v10
	v_exp_f32_e32 v10, v10
	v_mov_b32_e32 v89, v90
	v_add_f32_e32 v1, 1.0, v1
	v_rcp_f32_e32 v84, v1
	v_lshlrev_b32_e32 v1, 16, v92
	v_mul_f32_e32 v1, 0xbfb8aa3b, v1
	v_exp_f32_e32 v1, v1
	v_add_f32_e32 v10, 1.0, v10
	v_rcp_f32_e32 v83, v10
	s_waitcnt vmcnt(21)
; __device__ __forceinline__ float bf2f(unsigned b) { return __uint_as_float(b << 16); }
; __device__ __forceinline__ float sigmoidf_(float x) { return __builtin_amdgcn_rcpf(1.f + __expf(-x)); }
; #define SHX(v, m) (((m) < 32) ? __int_as_float(__builtin_amdgcn_ds_swizzle(__float_as_int(v), ((((m) & 31) << 10) | 0x1f))) : shx32(v))
; __device__ __forceinline__ void m3_unit(LAS unsigned char* L, int u, const bf16* z, const float* gates, const float* cw, const bf16* cprev, const float* nprev, const float* mprev, const float* normg, bf16* mix, int tid_) {
;     ...
;     m3_pv(L, acc, w, lane);
; #pragma unroll
;     for (int nt = 0; nt < 8; ++nt)
; #pragma unroll
;         for (int r = 0; r < 4; ++r) hsum[nt][r] += acc[nt][r] * __builtin_amdgcn_rcpf(fmaxf(fabsf(den[r]), __expf(-mt[r])));
;     __syncthreads();
; #pragma unroll
;     for (int r = 0; r < 4; ++r) { const int j = 16 * w + 4 * fq + r; const size_t t = (size_t)(t0 + j); float xv[8]; float s1 = 0.f;
; #pragma unroll
;         for (int nt = 0; nt < 8; ++nt) { xv[nt] = sigmoidf_(bf2f(zo[r][nt])) * hsum[nt][r]; s1 += xv[nt]; }
;         s1 += SHX(s1, 1); s1 += SHX(s1, 2); s1 += SHX(s1, 4); s1 += SHX(s1, 8);
;         const float mean = s1 * (1.f / 128.f); float s2 = 0.f;
; #pragma unroll
;         for (int nt = 0; nt < 8; ++nt) { xv[nt] -= mean; s2 += xv[nt] * xv[nt]; }
;         s2 += SHX(s2, 1); s2 += SHX(s2, 2); s2 += SHX(s2, 4); s2 += SHX(s2, 8);
;         const float rstd = rsqrtf(s2 * (1.f / 128.f) + EPS);
; #pragma unroll
	v_lshlrev_b32_e32 v10, 16, v127
	v_add_f32_e32 v1, 1.0, v1
	v_rcp_f32_e32 v87, v1
	v_lshlrev_b32_e32 v1, 16, v93
	v_mul_f32_e32 v1, 0xbfb8aa3b, v1
	v_exp_f32_e32 v1, v1
	v_mul_f32_e32 v10, 0xbfb8aa3b, v10
	v_exp_f32_e32 v10, v10
	v_pk_mul_f32 v[6:7], v[88:89], v[6:7]
	v_add_f32_e32 v1, 1.0, v1
	v_rcp_f32_e32 v86, v1
	v_lshlrev_b32_e32 v1, 16, v94
	v_mul_f32_e32 v1, 0xbfb8aa3b, v1
	v_exp_f32_e32 v1, v1
	v_mov_b32_e32 v94, v50
	v_add_f32_e32 v10, 1.0, v10
	v_pk_mul_f32 v[2:3], v[88:89], v[2:3]
	v_add_f32_e32 v1, 1.0, v1
	v_rcp_f32_e32 v93, v1
	v_lshlrev_b32_e32 v1, 16, v95
	v_mul_f32_e32 v1, 0xbfb8aa3b, v1
	v_exp_f32_e32 v1, v1
	v_mov_b32_e32 v95, v46
	v_pk_fma_f32 v[94:95], v[150:151], v[94:95], v[96:97] op_sel_hi:[0,1,1]
	v_mov_b32_e32 v96, v42
	v_add_f32_e32 v1, 1.0, v1
	v_rcp_f32_e32 v92, v1
	v_or_b32_e32 v1, s35, v162
	v_lshlrev_b32_e32 v1, 2, v1
	global_load_dword v111, v1, s[0:1]
	v_add_lshl_u32 v1, v162, s35, 2
	global_load_dword v110, v1, s[0:1] offset:64
	global_load_dword v91, v1, s[0:1] offset:128
	global_load_dword v69, v1, s[0:1] offset:192
	global_load_dword v62, v1, s[0:1] offset:256
	global_load_dword v54, v1, s[0:1] offset:320
	global_load_dword v50, v1, s[0:1] offset:384
	s_nop 0
	global_load_dword v1, v1, s[0:1] offset:448
	v_mov_b32_e32 v97, v38
	v_pk_fma_f32 v[96:97], v[150:151], v[96:97], v[98:99] op_sel_hi:[0,1,1]
	v_mov_b32_e32 v98, v34
	v_mov_b32_e32 v99, v30
	v_pk_fma_f32 v[98:99], v[150:151], v[98:99], v[100:101] op_sel_hi:[0,1,1]
	v_rcp_f32_e32 v101, v10
	s_waitcnt vmcnt(28)
	v_lshlrev_b32_e32 v10, 16, v128
	v_mul_f32_e32 v10, 0xbfb8aa3b, v10
	v_exp_f32_e32 v10, v10
	v_mov_b32_e32 v30, v35
	v_mov_b32_e32 v151, v152
	v_pk_fma_f32 v[6:7], v[150:151], v[18:19], v[6:7]
	v_add_f32_e32 v10, 1.0, v10
	v_rcp_f32_e32 v100, v10
	s_waitcnt vmcnt(27)
	v_lshlrev_b32_e32 v10, 16, v129
	v_mul_f32_e32 v10, 0xbfb8aa3b, v10
	v_exp_f32_e32 v10, v10
	v_pk_mul_f32 v[108:109], v[84:85], v[98:99]
	v_mov_b32_e32 v38, v43
	v_pk_fma_f32 v[2:3], v[150:151], v[26:27], v[2:3]
	v_add_f32_e32 v10, 1.0, v10
	v_rcp_f32_e32 v107, v10
	s_waitcnt vmcnt(26)
	v_lshlrev_b32_e32 v10, 16, v130
	v_mul_f32_e32 v10, 0xbfb8aa3b, v10
	v_exp_f32_e32 v10, v10
	v_pk_fma_f32 v[18:19], v[80:81], v[6:7], 0 op_sel_hi:[1,1,0]
	v_mov_b32_e32 v26, v109
	v_pk_fma_f32 v[18:19], v[82:83], v[2:3], v[18:19]
	v_add_f32_e32 v10, 1.0, v10
	v_rcp_f32_e32 v106, v10
	s_waitcnt vmcnt(25)
	v_lshlrev_b32_e32 v10, 16, v131
	v_mul_f32_e32 v10, 0xbfb8aa3b, v10
	v_exp_f32_e32 v10, v10
	v_pk_mul_f32 v[104:105], v[86:87], v[96:97]
	v_mov_b32_e32 v46, v51
	v_pk_mul_f32 v[102:103], v[92:93], v[94:95]
	v_add_f32_e32 v10, 1.0, v10
	v_rcp_f32_e32 v129, v10
	s_waitcnt vmcnt(24)
	v_lshlrev_b32_e32 v10, 16, v132
	v_mul_f32_e32 v10, 0xbfb8aa3b, v10
	v_exp_f32_e32 v10, v10
	s_waitcnt vmcnt(5)
	v_pk_mul_f32 v[22:23], v[90:91], v[22:23] op_sel_hi:[0,1]
	v_add_f32_e32 v10, 1.0, v10
	v_rcp_f32_e32 v128, v10
	v_mov_b32_e32 v10, v15
	v_pk_mul_f32 v[10:11], v[90:91], v[10:11] op_sel_hi:[0,1]
	v_pk_fma_f32 v[10:11], v[152:153], v[30:31], v[10:11] op_sel_hi:[0,1,1]
	v_pk_mul_f32 v[14:15], v[100:101], v[10:11]
	v_pk_fma_f32 v[22:23], v[152:153], v[38:39], v[22:23] op_sel_hi:[0,1,1]
	v_mov_b32_e32 v27, v15
	v_pk_mul_f32 v[58:59], v[90:91], v[58:59] op_sel_hi:[0,1]
	v_pk_mul_f32 v[38:39], v[106:107], v[22:23]
	v_pk_add_f32 v[18:19], v[18:19], v[26:27]
	v_mov_b32_e32 v109, v14
	v_pk_fma_f32 v[46:47], v[152:153], v[46:47], v[58:59] op_sel_hi:[0,1,1]
	v_pk_add_f32 v[14:15], v[18:19], v[108:109]
	v_mov_b32_e32 v18, v105
	v_mov_b32_e32 v19, v39
	v_pk_mul_f32 v[58:59], v[128:129], v[46:47]
	v_pk_add_f32 v[14:15], v[14:15], v[18:19]
	v_mov_b32_e32 v105, v38
	v_pk_add_f32 v[14:15], v[14:15], v[104:105]
	v_mov_b32_e32 v18, v103
	v_mov_b32_e32 v19, v59
	v_pk_add_f32 v[14:15], v[14:15], v[18:19]
	v_mov_b32_e32 v103, v58
	v_pk_add_f32 v[14:15], v[14:15], v[102:103]
	s_waitcnt lgkmcnt(0)
	s_nop 1
	v_add_f32_dpp v14, v14, v14 quad_perm:[1,0,3,2] row_mask:0xf bank_mask:0xf
	v_add_f32_dpp v15, v15, v15 quad_perm:[1,0,3,2] row_mask:0xf bank_mask:0xf
	s_waitcnt lgkmcnt(0)
	s_nop 1
	v_add_f32_dpp v14, v14, v14 quad_perm:[2,3,0,1] row_mask:0xf bank_mask:0xf
	v_add_f32_dpp v15, v15, v15 quad_perm:[2,3,0,1] row_mask:0xf bank_mask:0xf
	s_waitcnt lgkmcnt(0)
	s_nop 1
	v_add_f32_dpp v14, v14, v14 row_half_mirror row_mask:0xf bank_mask:0xf
	v_add_f32_dpp v15, v15, v15 row_half_mirror row_mask:0xf bank_mask:0xf
	s_waitcnt lgkmcnt(0)
	s_nop 1
	v_add_f32_dpp v14, v14, v14 row_mirror row_mask:0xf bank_mask:0xf
	v_add_f32_dpp v15, v15, v15 row_mirror row_mask:0xf bank_mask:0xf
	s_nop 0
	v_pk_mul_f32 v[14:15], v[14:15], s[8:9] op_sel_hi:[1,0]
	s_nop 0
	v_pk_fma_f32 v[18:19], v[84:85], v[98:99], v[14:15] op_sel_hi:[1,1,0] neg_lo:[0,0,1] neg_hi:[0,0,1]
	v_pk_fma_f32 v[58:59], v[82:83], v[2:3], v[14:15] neg_lo:[0,0,1] neg_hi:[0,0,1]
	v_pk_fma_f32 v[10:11], v[100:101], v[10:11], v[14:15] op_sel:[0,0,1] neg_lo:[0,0,1] neg_hi:[0,0,1]
	v_pk_mul_f32 v[26:27], v[18:19], v[18:19]
	v_pk_fma_f32 v[6:7], v[80:81], v[6:7], v[14:15] neg_lo:[0,0,1] neg_hi:[0,0,1]
	v_pk_mul_f32 v[2:3], v[58:59], v[58:59]
	v_pk_mul_f32 v[80:81], v[10:11], v[10:11]
	v_pk_fma_f32 v[30:31], v[86:87], v[96:97], v[14:15] op_sel_hi:[1,1,0] neg_lo:[0,0,1] neg_hi:[0,0,1]
	v_pk_fma_f32 v[2:3], v[6:7], v[6:7], v[2:3]
	v_pk_fma_f32 v[22:23], v[106:107], v[22:23], v[14:15] op_sel:[0,0,1] neg_lo:[0,0,1] neg_hi:[0,0,1]
	v_mov_b32_e32 v85, v26
	v_mov_b32_e32 v26, v81
	v_pk_mul_f32 v[34:35], v[30:31], v[30:31]
	v_pk_mul_f32 v[82:83], v[22:23], v[22:23]
	v_mov_b32_e32 v84, v80
	v_pk_add_f32 v[2:3], v[26:27], v[2:3] op_sel:[0,1] op_sel_hi:[1,0]
	v_pk_fma_f32 v[38:39], v[92:93], v[94:95], v[14:15] op_sel_hi:[1,1,0] neg_lo:[0,0,1] neg_hi:[0,0,1]
	v_pk_fma_f32 v[14:15], v[128:129], v[46:47], v[14:15] op_sel:[0,0,1] neg_lo:[0,0,1] neg_hi:[0,0,1]
	v_pk_add_f32 v[2:3], v[84:85], v[2:3]
	v_mov_b32_e32 v26, v83
	v_mov_b32_e32 v27, v35
	v_pk_mul_f32 v[42:43], v[38:39], v[38:39]
	v_pk_mul_f32 v[46:47], v[14:15], v[14:15]
	v_pk_add_f32 v[2:3], v[26:27], v[2:3]
	v_mov_b32_e32 v83, v34
	v_pk_add_f32 v[2:3], v[82:83], v[2:3]
	v_mov_b32_e32 v26, v47
	v_mov_b32_e32 v27, v43
	v_pk_add_f32 v[2:3], v[26:27], v[2:3]
	v_mov_b32_e32 v47, v42
	v_pk_add_f32 v[2:3], v[46:47], v[2:3]
	v_mov_b32_e32 v35, v24
	v_mov_b32_e32 v24, v57
	s_waitcnt vmcnt(4)
; __device__ __forceinline__ unsigned f2bf(float f) { unsigned u = __float_as_uint(f); return (u + 0x7fffu + ((u >> 16) & 1u)) >> 16; }
; __device__ __forceinline__ float bf2f(unsigned b) { return __uint_as_float(b << 16); }
; __device__ __forceinline__ float sigmoidf_(float x) { return __builtin_amdgcn_rcpf(1.f + __expf(-x)); }
; #define SHX(v, m) (((m) < 32) ? __int_as_float(__builtin_amdgcn_ds_swizzle(__float_as_int(v), ((((m) & 31) << 10) | 0x1f))) : shx32(v))
; __device__ __forceinline__ void m3_unit(LAS unsigned char* L, int u, const bf16* z, const float* gates, const float* cw, const bf16* cprev, const float* nprev, const float* mprev, const float* normg, bf16* mix, int tid_) {
;     ...
;     for (int r = 0; r < 4; ++r) { const int j = 16 * w + 4 * fq + r; const size_t t = (size_t)(t0 + j); float xv[8]; float s1 = 0.f;
; #pragma unroll
;         for (int nt = 0; nt < 8; ++nt) { xv[nt] = sigmoidf_(bf2f(zo[r][nt])) * hsum[nt][r]; s1 += xv[nt]; }
;         s1 += SHX(s1, 1); s1 += SHX(s1, 2); s1 += SHX(s1, 4); s1 += SHX(s1, 8);
;         const float mean = s1 * (1.f / 128.f); float s2 = 0.f;
; #pragma unroll
;         for (int nt = 0; nt < 8; ++nt) { xv[nt] -= mean; s2 += xv[nt] * xv[nt]; }
;         s2 += SHX(s2, 1); s2 += SHX(s2, 2); s2 += SHX(s2, 4); s2 += SHX(s2, 8);
;         const float rstd = rsqrtf(s2 * (1.f / 128.f) + EPS);
; #pragma unroll
;         for (int nt = 0; nt < 8; ++nt) { const int e = nt * 16 + fr; mix[t * 1024 + 512 + hh * 128 + e] = (bf16)f2bf(xv[nt] * rstd * normg[hh * 128 + e]); } }
	v_pk_mul_f32 v[24:25], v[68:69], v[24:25] op_sel_hi:[0,1]
	s_waitcnt lgkmcnt(0)
	s_nop 1
	v_add_f32_dpp v2, v2, v2 quad_perm:[1,0,3,2] row_mask:0xf bank_mask:0xf
	v_add_f32_dpp v3, v3, v3 quad_perm:[1,0,3,2] row_mask:0xf bank_mask:0xf
	s_waitcnt lgkmcnt(0)
	s_nop 1
	v_add_f32_dpp v2, v2, v2 quad_perm:[2,3,0,1] row_mask:0xf bank_mask:0xf
	v_add_f32_dpp v3, v3, v3 quad_perm:[2,3,0,1] row_mask:0xf bank_mask:0xf
	s_waitcnt lgkmcnt(0)
	s_nop 1
	v_add_f32_dpp v2, v2, v2 row_half_mirror row_mask:0xf bank_mask:0xf
	v_add_f32_dpp v3, v3, v3 row_half_mirror row_mask:0xf bank_mask:0xf
	s_waitcnt lgkmcnt(0)
	s_nop 1
	v_add_f32_dpp v26, v2, v2 row_mirror row_mask:0xf bank_mask:0xf
	v_add_f32_dpp v27, v3, v3 row_mirror row_mask:0xf bank_mask:0xf
	v_mov_b64_e32 v[2:3], s[4:5]
	v_pk_fma_f32 v[26:27], v[26:27], s[8:9], v[2:3] op_sel_hi:[1,0,0]
	v_readlane_b32 s4, v255, 46
	v_mul_f32_e32 v34, 0x4b800000, v27
	v_cmp_gt_f32_e64 s[38:39], s73, v27
	v_cmp_gt_f32_e32 vcc, s73, v26
	v_readlane_b32 s5, v255, 47
	v_cndmask_b32_e64 v27, v27, v34, s[38:39]
	v_rsq_f32_e32 v27, v27
	s_add_i32 s34, s34, s4
	v_readlane_b32 s4, v255, 12
	s_add_i32 s19, s19, s4
	v_mul_f32_e32 v34, 0x45800000, v27
	v_cndmask_b32_e64 v27, v27, v34, s[38:39]
	v_mul_f32_e32 v6, v6, v27
	v_mul_f32_e32 v6, v111, v6
	v_bfe_u32 v34, v6, 16, 1
	v_add3_u32 v6, v6, v34, s78
	global_store_short_d16_hi v[78:79], v6, off offset:1024
	v_mul_f32_e32 v6, v58, v27
	v_mul_f32_e32 v6, v110, v6
	v_bfe_u32 v34, v6, 16, 1
	v_add3_u32 v6, v6, v34, s78
	global_store_short_d16_hi v[78:79], v6, off offset:1056
	v_mul_f32_e32 v6, v19, v27
	v_mul_f32_e32 v6, v91, v6
	v_bfe_u32 v19, v6, 16, 1
	v_add3_u32 v6, v6, v19, s78
	global_store_short_d16_hi v[78:79], v6, off offset:1088
	v_mul_f32_e32 v6, v18, v27
	v_mul_f32_e32 v6, v69, v6
	v_bfe_u32 v18, v6, 16, 1
	v_add3_u32 v6, v6, v18, s78
	global_store_short_d16_hi v[78:79], v6, off offset:1120
	v_mul_f32_e32 v6, v31, v27
	s_waitcnt vmcnt(7)
	v_mul_f32_e32 v6, v62, v6
	v_bfe_u32 v18, v6, 16, 1
	v_add3_u32 v6, v6, v18, s78
	global_store_short_d16_hi v[78:79], v6, off offset:1152
	v_mul_f32_e32 v6, v30, v27
	s_waitcnt vmcnt(7)
	v_mul_f32_e32 v6, v54, v6
	v_bfe_u32 v18, v6, 16, 1
	v_add3_u32 v6, v6, v18, s78
	global_store_short_d16_hi v[78:79], v6, off offset:1184
	v_mul_f32_e32 v6, v39, v27
	s_waitcnt vmcnt(7)
	v_mul_f32_e32 v6, v50, v6
	v_bfe_u32 v18, v6, 16, 1
	v_add3_u32 v6, v6, v18, s78
	global_store_short_d16_hi v[78:79], v6, off offset:1216
	v_mul_f32_e32 v6, v38, v27
	s_waitcnt vmcnt(7)
	v_mul_f32_e32 v6, v1, v6
	v_bfe_u32 v18, v6, 16, 1
	v_add3_u32 v6, v6, v18, s78
	global_store_short_d16_hi v[78:79], v6, off offset:1248
	v_mul_f32_e32 v6, 0x4b800000, v26
	v_cndmask_b32_e32 v6, v26, v6, vcc
	v_rsq_f32_e32 v6, v6
	v_mov_b32_e32 v39, v12
	v_lshlrev_b32_e32 v12, 16, v117
	v_mul_f32_e32 v12, 0xbfb8aa3b, v12
	v_mul_f32_e32 v18, 0x45800000, v6
	v_cndmask_b32_e32 v26, v6, v18, vcc
	v_mul_f32_e32 v6, v7, v26
	v_lshlrev_b64 v[18:19], 11, v[76:77]
	v_mul_f32_e32 v6, v111, v6
	v_lshl_add_u64 v[18:19], s[40:41], 0, v[18:19]
	v_bfe_u32 v7, v6, 16, 1
	v_add3_u32 v27, v6, v7, s78
	v_lshl_add_u64 v[6:7], v[18:19], 0, v[70:71]
	v_mul_f32_e32 v18, v59, v26
	v_mul_f32_e32 v18, v110, v18
	v_bfe_u32 v19, v18, 16, 1
	v_mul_f32_e32 v11, v11, v26
	v_add3_u32 v18, v18, v19, s78
	v_mul_f32_e32 v11, v91, v11
	global_store_short_d16_hi v[6:7], v18, off offset:1056
	v_bfe_u32 v18, v11, 16, 1
	v_mul_f32_e32 v10, v10, v26
	v_add3_u32 v11, v11, v18, s78
	v_mul_f32_e32 v10, v69, v10
	global_store_short_d16_hi v[6:7], v11, off offset:1088
	v_bfe_u32 v11, v10, 16, 1
	v_add3_u32 v10, v10, v11, s78
	global_store_short_d16_hi v[6:7], v10, off offset:1120
	v_mul_f32_e32 v10, v23, v26
	v_mul_f32_e32 v10, v62, v10
	v_bfe_u32 v11, v10, 16, 1
	v_add3_u32 v10, v10, v11, s78
	global_store_short_d16_hi v[6:7], v10, off offset:1152
	v_mul_f32_e32 v10, v22, v26
	v_mul_f32_e32 v10, v54, v10
	v_bfe_u32 v11, v10, 16, 1
	v_add3_u32 v10, v10, v11, s78
	global_store_short_d16_hi v[6:7], v10, off offset:1184
	v_mul_f32_e32 v10, v15, v26
	v_mul_f32_e32 v10, v50, v10
	v_bfe_u32 v11, v10, 16, 1
	v_add3_u32 v10, v10, v11, s78
	global_store_short_d16_hi v[6:7], v10, off offset:1216
	v_mul_f32_e32 v10, v14, v26
	v_mul_f32_e32 v10, v1, v10
	v_bfe_u32 v11, v10, 16, 1
	v_add3_u32 v10, v10, v11, s78
	global_store_short_d16_hi v[6:7], v27, off offset:1024
	global_store_short_d16_hi v[6:7], v10, off offset:1248
	v_lshlrev_b32_e32 v6, 16, v126
	v_mul_f32_e32 v6, 0xbfb8aa3b, v6
	v_exp_f32_e32 v6, v6
	v_exp_f32_e32 v12, v12
	v_mov_b32_e32 v30, v64
	v_mov_b32_e32 v31, v60
	v_add_f32_e32 v6, 1.0, v6
	v_rcp_f32_e32 v10, v6
	v_lshlrev_b32_e32 v6, 16, v125
	v_mul_f32_e32 v6, 0xbfb8aa3b, v6
	v_exp_f32_e32 v6, v6
	v_add_f32_e32 v12, 1.0, v12
	v_rcp_f32_e32 v15, v12
	v_lshlrev_b32_e32 v12, 16, v116
	v_add_f32_e32 v6, 1.0, v6
	v_rcp_f32_e32 v14, v6
	v_lshlrev_b32_e32 v6, 16, v124
	v_mul_f32_e32 v6, 0xbfb8aa3b, v6
	v_exp_f32_e32 v6, v6
	v_mul_f32_e32 v12, 0xbfb8aa3b, v12
	v_exp_f32_e32 v12, v12
	v_mov_b32_e32 v7, v48
	v_add_f32_e32 v6, 1.0, v6
	v_rcp_f32_e32 v19, v6
	v_lshlrev_b32_e32 v6, 16, v123
	v_mul_f32_e32 v6, 0xbfb8aa3b, v6
	v_exp_f32_e32 v6, v6
	v_add_f32_e32 v12, 1.0, v12
	v_rcp_f32_e32 v43, v12
	v_lshlrev_b32_e32 v12, 16, v115
	v_add_f32_e32 v6, 1.0, v6
	v_rcp_f32_e32 v18, v6
	v_lshlrev_b32_e32 v6, 16, v122
	v_mul_f32_e32 v6, 0xbfb8aa3b, v6
	v_exp_f32_e32 v6, v6
	v_mul_f32_e32 v12, 0xbfb8aa3b, v12
	v_exp_f32_e32 v12, v12
	v_pk_mul_f32 v[30:31], v[66:67], v[30:31] op_sel_hi:[0,1]
	v_add_f32_e32 v6, 1.0, v6
	v_rcp_f32_e32 v23, v6
	v_lshlrev_b32_e32 v6, 16, v121
	v_mul_f32_e32 v6, 0xbfb8aa3b, v6
	v_exp_f32_e32 v6, v6
	v_add_f32_e32 v12, 1.0, v12
; __device__ __forceinline__ float bf2f(unsigned b) { return __uint_as_float(b << 16); }
; __device__ __forceinline__ float sigmoidf_(float x) { return __builtin_amdgcn_rcpf(1.f + __expf(-x)); }
; #define SHX(v, m) (((m) < 32) ? __int_as_float(__builtin_amdgcn_ds_swizzle(__float_as_int(v), ((((m) & 31) << 10) | 0x1f))) : shx32(v))
; __device__ __forceinline__ void m3_unit(LAS unsigned char* L, int u, const bf16* z, const float* gates, const float* cw, const bf16* cprev, const float* nprev, const float* mprev, const float* normg, bf16* mix, int tid_) {
;     ...
;     for (int r = 0; r < 4; ++r) { const int j = 16 * w + 4 * fq + r; const size_t t = (size_t)(t0 + j); float xv[8]; float s1 = 0.f;
; #pragma unroll
;         for (int nt = 0; nt < 8; ++nt) { xv[nt] = sigmoidf_(bf2f(zo[r][nt])) * hsum[nt][r]; s1 += xv[nt]; }
;         s1 += SHX(s1, 1); s1 += SHX(s1, 2); s1 += SHX(s1, 4); s1 += SHX(s1, 8);
;         const float mean = s1 * (1.f / 128.f); float s2 = 0.f;
; #pragma unroll
;         for (int nt = 0; nt < 8; ++nt) { xv[nt] -= mean; s2 += xv[nt] * xv[nt]; }
;         s2 += SHX(s2, 1); s2 += SHX(s2, 2); s2 += SHX(s2, 4); s2 += SHX(s2, 8);
	v_rcp_f32_e32 v42, v12
	v_lshlrev_b32_e32 v12, 16, v114
	v_add_f32_e32 v6, 1.0, v6
	v_rcp_f32_e32 v22, v6
	v_lshlrev_b32_e32 v6, 16, v120
	v_mul_f32_e32 v6, 0xbfb8aa3b, v6
	v_exp_f32_e32 v6, v6
	v_mul_f32_e32 v12, 0xbfb8aa3b, v12
	v_exp_f32_e32 v12, v12
	v_mov_b32_e32 v34, v56
	v_add_f32_e32 v6, 1.0, v6
	v_rcp_f32_e32 v27, v6
	v_lshlrev_b32_e32 v6, 16, v119
	v_mul_f32_e32 v6, 0xbfb8aa3b, v6
	v_exp_f32_e32 v6, v6
	v_pk_mul_f32 v[34:35], v[66:67], v[34:35] op_sel_hi:[0,1]
	v_mov_b32_e32 v38, v16
	v_pk_mul_f32 v[38:39], v[66:67], v[38:39] op_sel_hi:[0,1]
	v_add_f32_e32 v6, 1.0, v6
	v_rcp_f32_e32 v26, v6
	v_mov_b32_e32 v6, v52
	v_pk_fma_f32 v[30:31], v[146:147], v[6:7], v[30:31] op_sel_hi:[0,1,1]
	v_mov_b32_e32 v6, v44
	v_mov_b32_e32 v7, v40
	v_pk_fma_f32 v[34:35], v[146:147], v[6:7], v[34:35] op_sel_hi:[0,1,1]
	v_mov_b32_e32 v6, v36
	v_mov_b32_e32 v7, v32
	v_add_f32_e32 v12, 1.0, v12
	v_pk_fma_f32 v[38:39], v[146:147], v[6:7], v[38:39] op_sel_hi:[0,1,1]
	v_lshlrev_b64 v[6:7], 11, v[74:75]
	v_rcp_f32_e32 v75, v12
	v_lshlrev_b32_e32 v12, 16, v113
	v_mul_f32_e32 v12, 0xbfb8aa3b, v12
	v_exp_f32_e32 v12, v12
	v_lshlrev_b32_e32 v11, 16, v118
	v_mul_f32_e32 v11, 0xbfb8aa3b, v11
	v_exp_f32_e32 v11, v11
	v_add_f32_e32 v12, 1.0, v12
	v_rcp_f32_e32 v74, v12
	v_lshlrev_b32_e32 v12, 16, v112
	v_mul_f32_e32 v12, 0xbfb8aa3b, v12
	v_exp_f32_e32 v12, v12
	v_add_f32_e32 v11, 1.0, v11
	v_rcp_f32_e32 v11, v11
	v_mov_b32_e32 v32, v37
	v_add_f32_e32 v12, 1.0, v12
	v_rcp_f32_e32 v79, v12
	v_lshlrev_b32_e32 v12, 16, v67
	v_mul_f32_e32 v12, 0xbfb8aa3b, v12
	v_exp_f32_e32 v12, v12
	v_mov_b32_e32 v67, v68
	v_mov_b32_e32 v147, v148
	v_pk_mul_f32 v[8:9], v[66:67], v[8:9]
	v_add_f32_e32 v12, 1.0, v12
	v_rcp_f32_e32 v78, v12
	v_mov_b32_e32 v12, v17
	v_pk_mul_f32 v[12:13], v[68:69], v[12:13] op_sel_hi:[0,1]
	v_pk_fma_f32 v[12:13], v[148:149], v[32:33], v[12:13] op_sel_hi:[0,1,1]
	v_pk_fma_f32 v[8:9], v[146:147], v[20:21], v[8:9]
	v_pk_mul_f32 v[4:5], v[66:67], v[4:5]
	v_pk_mul_f32 v[76:77], v[18:19], v[38:39]
	v_mov_b32_e32 v40, v45
	v_pk_mul_f32 v[16:17], v[42:43], v[12:13]
	v_pk_fma_f32 v[4:5], v[146:147], v[28:29], v[4:5]
	v_pk_fma_f32 v[20:21], v[10:11], v[8:9], 0 op_sel_hi:[1,1,0]
	v_mov_b32_e32 v60, v65
	v_pk_fma_f32 v[24:25], v[148:149], v[40:41], v[24:25] op_sel_hi:[0,1,1]
	v_pk_fma_f32 v[20:21], v[14:15], v[4:5], v[20:21]
	v_mov_b32_e32 v28, v77
	v_mov_b32_e32 v29, v17
	v_pk_mul_f32 v[58:59], v[22:23], v[34:35]
	v_mov_b32_e32 v48, v53
	v_pk_mul_f32 v[52:53], v[68:69], v[60:61] op_sel_hi:[0,1]
	v_pk_mul_f32 v[40:41], v[74:75], v[24:25]
	v_pk_add_f32 v[20:21], v[20:21], v[28:29]
	v_mov_b32_e32 v77, v16
	v_pk_fma_f32 v[48:49], v[148:149], v[48:49], v[52:53] op_sel_hi:[0,1,1]
	v_pk_add_f32 v[16:17], v[20:21], v[76:77]
	v_mov_b32_e32 v20, v59
	v_mov_b32_e32 v21, v41
	v_pk_mul_f32 v[46:47], v[26:27], v[30:31]
	v_pk_mul_f32 v[52:53], v[78:79], v[48:49]
	v_pk_add_f32 v[16:17], v[16:17], v[20:21]
	v_mov_b32_e32 v59, v40
	v_pk_add_f32 v[16:17], v[16:17], v[58:59]
	v_mov_b32_e32 v20, v47
	v_mov_b32_e32 v21, v53
	v_pk_add_f32 v[16:17], v[16:17], v[20:21]
	v_mov_b32_e32 v47, v52
	v_pk_add_f32 v[16:17], v[16:17], v[46:47]
	v_lshl_add_u64 v[6:7], s[40:41], 0, v[6:7]
	v_lshl_add_u64 v[6:7], v[6:7], 0, v[70:71]
	v_readlane_b32 s4, v255, 48
	v_readlane_b32 s5, v255, 49
	s_waitcnt lgkmcnt(0)
	s_nop 1
	v_add_f32_dpp v16, v16, v16 quad_perm:[1,0,3,2] row_mask:0xf bank_mask:0xf
	v_add_f32_dpp v17, v17, v17 quad_perm:[1,0,3,2] row_mask:0xf bank_mask:0xf
	s_add_u32 s20, s20, s4
	s_addc_u32 s21, s21, s5
	v_readlane_b32 s4, v255, 36
	v_readlane_b32 s5, v255, 37
	s_waitcnt lgkmcnt(0)
	s_nop 1
	v_add_f32_dpp v16, v16, v16 quad_perm:[2,3,0,1] row_mask:0xf bank_mask:0xf
	v_add_f32_dpp v17, v17, v17 quad_perm:[2,3,0,1] row_mask:0xf bank_mask:0xf
	s_add_u32 s30, s30, s4
	s_addc_u32 s31, s31, s5
	v_readlane_b32 s4, v255, 40
	v_readlane_b32 s5, v255, 41
	s_waitcnt lgkmcnt(0)
	s_nop 1
	v_add_f32_dpp v16, v16, v16 row_half_mirror row_mask:0xf bank_mask:0xf
	v_add_f32_dpp v17, v17, v17 row_half_mirror row_mask:0xf bank_mask:0xf
	s_add_u32 s28, s28, s4
	s_addc_u32 s29, s29, s5
	s_cmp_ge_i32 s34, s71
	s_waitcnt lgkmcnt(0)
; __device__ __forceinline__ unsigned f2bf(float f) { unsigned u = __float_as_uint(f); return (u + 0x7fffu + ((u >> 16) & 1u)) >> 16; }
; __device__ __forceinline__ float bf2f(unsigned b) { return __uint_as_float(b << 16); }
; __device__ __forceinline__ float sigmoidf_(float x) { return __builtin_amdgcn_rcpf(1.f + __expf(-x)); }
; #define SHX(v, m) (((m) < 32) ? __int_as_float(__builtin_amdgcn_ds_swizzle(__float_as_int(v), ((((m) & 31) << 10) | 0x1f))) : shx32(v))
; __device__ __forceinline__ void m3_unit(LAS unsigned char* L, int u, const bf16* z, const float* gates, const float* cw, const bf16* cprev, const float* nprev, const float* mprev, const float* normg, bf16* mix, int tid_) {
;     ...
;     for (int r = 0; r < 4; ++r) { const int j = 16 * w + 4 * fq + r; const size_t t = (size_t)(t0 + j); float xv[8]; float s1 = 0.f;
; #pragma unroll
;         for (int nt = 0; nt < 8; ++nt) { xv[nt] = sigmoidf_(bf2f(zo[r][nt])) * hsum[nt][r]; s1 += xv[nt]; }
;         s1 += SHX(s1, 1); s1 += SHX(s1, 2); s1 += SHX(s1, 4); s1 += SHX(s1, 8);
;         const float mean = s1 * (1.f / 128.f); float s2 = 0.f;
; #pragma unroll
;         for (int nt = 0; nt < 8; ++nt) { xv[nt] -= mean; s2 += xv[nt] * xv[nt]; }
;         s2 += SHX(s2, 1); s2 += SHX(s2, 2); s2 += SHX(s2, 4); s2 += SHX(s2, 8);
;         const float rstd = rsqrtf(s2 * (1.f / 128.f) + EPS);
; #pragma unroll
;         for (int nt = 0; nt < 8; ++nt) { const int e = nt * 16 + fr; mix[t * 1024 + 512 + hh * 128 + e] = (bf16)f2bf(xv[nt] * rstd * normg[hh * 128 + e]); } }
;     __syncthreads();
	s_nop 1
	v_add_f32_dpp v16, v16, v16 row_mirror row_mask:0xf bank_mask:0xf
	v_add_f32_dpp v17, v17, v17 row_mirror row_mask:0xf bank_mask:0xf
	s_nop 0
	v_pk_mul_f32 v[16:17], v[16:17], s[8:9] op_sel_hi:[1,0]
	s_nop 0
	v_pk_fma_f32 v[18:19], v[18:19], v[38:39], v[16:17] op_sel_hi:[1,1,0] neg_lo:[0,0,1] neg_hi:[0,0,1]
	v_pk_fma_f32 v[4:5], v[14:15], v[4:5], v[16:17] neg_lo:[0,0,1] neg_hi:[0,0,1]
	v_pk_fma_f32 v[12:13], v[42:43], v[12:13], v[16:17] op_sel:[0,0,1] neg_lo:[0,0,1] neg_hi:[0,0,1]
	v_pk_mul_f32 v[20:21], v[18:19], v[18:19]
	v_pk_fma_f32 v[8:9], v[10:11], v[8:9], v[16:17] neg_lo:[0,0,1] neg_hi:[0,0,1]
	v_pk_mul_f32 v[10:11], v[4:5], v[4:5]
	v_pk_mul_f32 v[14:15], v[12:13], v[12:13]
	v_pk_fma_f32 v[22:23], v[22:23], v[34:35], v[16:17] op_sel_hi:[1,1,0] neg_lo:[0,0,1] neg_hi:[0,0,1]
	v_pk_fma_f32 v[10:11], v[8:9], v[8:9], v[10:11]
	v_pk_fma_f32 v[24:25], v[74:75], v[24:25], v[16:17] op_sel:[0,0,1] neg_lo:[0,0,1] neg_hi:[0,0,1]
	v_mov_b32_e32 v37, v20
	v_mov_b32_e32 v20, v15
	v_pk_mul_f32 v[28:29], v[22:23], v[22:23]
	v_pk_mul_f32 v[32:33], v[24:25], v[24:25]
	v_mov_b32_e32 v36, v14
	v_pk_add_f32 v[10:11], v[20:21], v[10:11] op_sel:[0,1] op_sel_hi:[1,0]
	v_pk_fma_f32 v[26:27], v[26:27], v[30:31], v[16:17] op_sel_hi:[1,1,0] neg_lo:[0,0,1] neg_hi:[0,0,1]
	v_pk_fma_f32 v[16:17], v[78:79], v[48:49], v[16:17] op_sel:[0,0,1] neg_lo:[0,0,1] neg_hi:[0,0,1]
	v_pk_add_f32 v[10:11], v[36:37], v[10:11]
	v_mov_b32_e32 v14, v33
	v_mov_b32_e32 v15, v29
	v_pk_mul_f32 v[30:31], v[26:27], v[26:27]
	v_pk_mul_f32 v[34:35], v[16:17], v[16:17]
	v_pk_add_f32 v[10:11], v[14:15], v[10:11]
	v_mov_b32_e32 v33, v28
	v_pk_add_f32 v[10:11], v[32:33], v[10:11]
	v_mov_b32_e32 v14, v35
	v_mov_b32_e32 v15, v31
	v_pk_add_f32 v[10:11], v[14:15], v[10:11]
	v_mov_b32_e32 v35, v30
	v_pk_add_f32 v[10:11], v[34:35], v[10:11]
	s_waitcnt lgkmcnt(0)
	s_nop 1
	v_add_f32_dpp v10, v10, v10 quad_perm:[1,0,3,2] row_mask:0xf bank_mask:0xf
	v_add_f32_dpp v11, v11, v11 quad_perm:[1,0,3,2] row_mask:0xf bank_mask:0xf
	s_waitcnt lgkmcnt(0)
	s_nop 1
	v_add_f32_dpp v10, v10, v10 quad_perm:[2,3,0,1] row_mask:0xf bank_mask:0xf
	v_add_f32_dpp v11, v11, v11 quad_perm:[2,3,0,1] row_mask:0xf bank_mask:0xf
	s_waitcnt lgkmcnt(0)
	s_nop 1
	v_add_f32_dpp v10, v10, v10 row_half_mirror row_mask:0xf bank_mask:0xf
	v_add_f32_dpp v11, v11, v11 row_half_mirror row_mask:0xf bank_mask:0xf
	s_waitcnt lgkmcnt(0)
	s_nop 1
	v_add_f32_dpp v10, v10, v10 row_mirror row_mask:0xf bank_mask:0xf
	v_add_f32_dpp v11, v11, v11 row_mirror row_mask:0xf bank_mask:0xf
	s_nop 0
	v_pk_fma_f32 v[2:3], v[10:11], s[8:9], v[2:3] op_sel_hi:[1,0,0]
	s_nop 0
	v_mul_f32_e32 v10, 0x4b800000, v3
	v_cmp_gt_f32_e64 s[38:39], s73, v3
	v_cmp_gt_f32_e32 vcc, s73, v2
	s_nop 0
	v_cndmask_b32_e64 v3, v3, v10, s[38:39]
	v_rsq_f32_e32 v3, v3
	s_nop 0
	v_mul_f32_e32 v10, 0x45800000, v3
	v_cndmask_b32_e64 v3, v3, v10, s[38:39]
	v_mul_f32_e32 v8, v8, v3
	v_mul_f32_e32 v8, v111, v8
	v_bfe_u32 v10, v8, 16, 1
	v_mul_f32_e32 v4, v4, v3
	v_add3_u32 v8, v8, v10, s78
	v_mul_f32_e32 v4, v110, v4
	global_store_short_d16_hi v[6:7], v8, off offset:1024
	v_bfe_u32 v8, v4, 16, 1
	v_add3_u32 v4, v4, v8, s78
	global_store_short_d16_hi v[6:7], v4, off offset:1056
	v_mul_f32_e32 v4, v19, v3
	v_mul_f32_e32 v4, v91, v4
	v_bfe_u32 v8, v4, 16, 1
	v_add3_u32 v4, v4, v8, s78
	global_store_short_d16_hi v[6:7], v4, off offset:1088
	v_mul_f32_e32 v4, v18, v3
	v_mul_f32_e32 v4, v69, v4
	v_bfe_u32 v8, v4, 16, 1
	v_add3_u32 v4, v4, v8, s78
	global_store_short_d16_hi v[6:7], v4, off offset:1120
	v_mul_f32_e32 v4, v23, v3
	v_mul_f32_e32 v4, v62, v4
	v_bfe_u32 v8, v4, 16, 1
	v_add3_u32 v4, v4, v8, s78
	global_store_short_d16_hi v[6:7], v4, off offset:1152
	v_mul_f32_e32 v4, v22, v3
	v_mul_f32_e32 v4, v54, v4
	v_bfe_u32 v8, v4, 16, 1
	v_add3_u32 v4, v4, v8, s78
	global_store_short_d16_hi v[6:7], v4, off offset:1184
	v_mul_f32_e32 v4, v27, v3
	v_mul_f32_e32 v4, v50, v4
	v_bfe_u32 v8, v4, 16, 1
	v_mul_f32_e32 v3, v26, v3
	v_add3_u32 v4, v4, v8, s78
	v_mul_f32_e32 v3, v1, v3
	global_store_short_d16_hi v[6:7], v4, off offset:1216
	v_bfe_u32 v4, v3, 16, 1
	v_add3_u32 v3, v3, v4, s78
	global_store_short_d16_hi v[6:7], v3, off offset:1248
	v_mul_f32_e32 v3, 0x4b800000, v2
	v_cndmask_b32_e32 v2, v2, v3, vcc
	v_rsq_f32_e32 v2, v2
	s_nop 0
	v_mul_f32_e32 v3, 0x45800000, v2
	v_cndmask_b32_e32 v4, v2, v3, vcc
	v_mul_f32_e32 v6, v9, v4
	v_lshlrev_b64 v[2:3], 11, v[72:73]
	v_mul_f32_e32 v6, v111, v6
	v_lshl_add_u64 v[2:3], s[40:41], 0, v[2:3]
	v_bfe_u32 v7, v6, 16, 1
	v_mul_f32_e32 v5, v5, v4
	v_add3_u32 v6, v6, v7, s78
	v_lshl_add_u64 v[2:3], v[2:3], 0, v[70:71]
	v_mul_f32_e32 v5, v110, v5
	global_store_short_d16_hi v[2:3], v6, off offset:1024
	v_bfe_u32 v6, v5, 16, 1
	v_add3_u32 v5, v5, v6, s78
	global_store_short_d16_hi v[2:3], v5, off offset:1056
	v_mul_f32_e32 v5, v13, v4
	v_mul_f32_e32 v5, v91, v5
	v_bfe_u32 v6, v5, 16, 1
	v_add3_u32 v5, v5, v6, s78
	global_store_short_d16_hi v[2:3], v5, off offset:1088
	v_mul_f32_e32 v5, v12, v4
	v_mul_f32_e32 v5, v69, v5
	v_bfe_u32 v6, v5, 16, 1
	v_add3_u32 v5, v5, v6, s78
	global_store_short_d16_hi v[2:3], v5, off offset:1120
	v_mul_f32_e32 v5, v25, v4
	v_mul_f32_e32 v5, v62, v5
	v_bfe_u32 v6, v5, 16, 1
	v_add3_u32 v5, v5, v6, s78
	global_store_short_d16_hi v[2:3], v5, off offset:1152
	v_mul_f32_e32 v5, v24, v4
	v_mul_f32_e32 v5, v54, v5
	v_bfe_u32 v6, v5, 16, 1
	v_add3_u32 v5, v5, v6, s78
	global_store_short_d16_hi v[2:3], v5, off offset:1184
	v_mul_f32_e32 v5, v17, v4
	v_mul_f32_e32 v4, v16, v4
	v_mul_f32_e32 v5, v50, v5
	v_mul_f32_e32 v1, v1, v4
	v_bfe_u32 v6, v5, 16, 1
	v_bfe_u32 v4, v1, 16, 1
	v_add3_u32 v5, v5, v6, s78
	v_add3_u32 v1, v1, v4, s78
	global_store_short_d16_hi v[2:3], v5, off offset:1216
	global_store_short_d16_hi v[2:3], v1, off offset:1248
	s_barrier
	s_cbranch_scc1 .LBB0_800
